# speedup vs baseline: 1.0092x; 1.0092x over previous
.LBB0_2:
	s_or_b64 exec, exec, s[80:81]
	v_lshl_add_u32 v1, v206, 2, s22
	s_add_i32 s19, s19, 0x22200
	ds_write_b32 v1, v72
	v_lshl_or_b32 v1, v124, 3, s19
	v_lshl_add_u32 v187, v67, 2, s22
	s_movk_i32 s22, 0x110
	v_mad_u32_u24 v186, v67, s22, v1
	s_add_i32 s22, s7, 0x180
	v_and_b32_e32 v102, 15, v0
	s_lshl_b32 s27, s34, 8
	s_and_b32 s25, s22, 0x380
	s_add_i32 s22, s7, 0x280
	v_lshlrev_b32_e32 v66, 2, v124
	v_mul_u32_u24_e32 v1, 0x110, v102
	v_and_b32_e32 v209, 48, v0
	s_and_b32 s23, s22, 0x380
	s_add_i32 s22, s7, 0x300
	v_mov_b32_e32 v67, 0x200
	s_addk_i32 s27, 0x380
	v_or_b32_e32 v133, s7, v66
	v_add3_u32 v1, s19, v1, v209
	s_lshl_b32 s19, s35, 15
	v_lshlrev_b32_e32 v210, 4, v206
	v_or_b32_e32 v189, s24, v66
	s_xor_b32 s24, s7, 0x200
	s_and_b32 s22, s22, 0x300
	v_bitop3_b32 v197, s7, v66, v67 bitop3:0xde
	s_and_b32 s7, s27, 0x380
	v_lshrrev_b32_e32 v185, 4, v206
	s_ashr_i32 s11, s10, 31
	v_or_b32_e32 v184, s19, v210
	v_or_b32_e32 v188, s26, v66
	v_or_b32_e32 v198, s25, v66
	v_or_b32_e32 v196, s23, v66
	v_or_b32_e32 v195, s22, v66
	v_or_b32_e32 v194, s7, v66
	v_mov_b32_e32 v102, v133
	v_and_b32_e32 v248, 2, v206
	v_cmp_ne_u32_e32 vcc, 0, v248
	v_mov_b32_e32 v249, 0x44444444
	v_mov_b32_e32 v250, 0xeeeeeeee
	s_nop 1
	v_cndmask_b32_e32 v223, v249, v250, vcc
	v_lshrrev_b32_e32 v248, 4, v206
	v_lshl_add_u32 v248, v248, 4, 1
	v_add_u32_e32 v249, 0, v248
	v_cvt_f32_u32_e32 v249, v249
	v_add_u32_e32 v250, 1, v248
	v_cvt_f32_u32_e32 v250, v250
	v_cvt_pk_bf16_f32 v232, v249, v250
	v_add_u32_e32 v249, 2, v248
	v_cvt_f32_u32_e32 v249, v249
	v_add_u32_e32 v250, 3, v248
	v_cvt_f32_u32_e32 v250, v250
	v_cvt_pk_bf16_f32 v233, v249, v250
	v_add_u32_e32 v249, 4, v248
	v_cvt_f32_u32_e32 v249, v249
	v_add_u32_e32 v250, 5, v248
	v_cvt_f32_u32_e32 v250, v250
	v_cvt_pk_bf16_f32 v234, v249, v250
	v_add_u32_e32 v249, 6, v248
	v_cvt_f32_u32_e32 v249, v249
	v_add_u32_e32 v250, 7, v248
	v_cvt_f32_u32_e32 v250, v250
	v_cvt_pk_bf16_f32 v235, v249, v250
	v_add_u32_e32 v249, 8, v248
	v_cvt_f32_u32_e32 v249, v249
	v_add_u32_e32 v250, 9, v248
	v_cvt_f32_u32_e32 v250, v250
	v_cvt_pk_bf16_f32 v236, v249, v250
	v_add_u32_e32 v249, 10, v248
	v_cvt_f32_u32_e32 v249, v249
	v_add_u32_e32 v250, 11, v248
	v_cvt_f32_u32_e32 v250, v250
	v_cvt_pk_bf16_f32 v237, v249, v250
	v_add_u32_e32 v249, 12, v248
	v_cvt_f32_u32_e32 v249, v249
	v_add_u32_e32 v250, 13, v248
	v_cvt_f32_u32_e32 v250, v250
	v_cvt_pk_bf16_f32 v238, v249, v250
	v_add_u32_e32 v249, 14, v248
	v_cvt_f32_u32_e32 v249, v249
	v_add_u32_e32 v250, 15, v248
	v_cvt_f32_u32_e32 v250, v250
	v_cvt_pk_bf16_f32 v239, v249, v250
	v_and_b32_e32 v248, 15, v206
	v_lshrrev_b32_e32 v249, 2, v248
	v_and_b32_e32 v250, 1, v248
	v_lshl_add_u32 v249, v249, 1, v250
	v_and_b32_e32 v250, 3, v249
	v_lshrrev_b32_e32 v251, 4, v206
	v_cmp_eq_u32_e32 vcc, v250, v251
	v_lshrrev_b32_e32 v249, 2, v249
	v_cmp_ne_u32_e64 s[78:79], 0, v249
	v_mov_b32_e32 v250, 0x3f80
	v_mov_b32_e32 v251, 0x3f800000
	s_nop 1
	v_cndmask_b32_e64 v250, v250, v251, s[78:79]
	v_cndmask_b32_e32 v252, 0, v250, vcc
	s_lshr_b32 s77, s19, 15
	s_mulk_i32 s77, 0x1100
	s_add_i32 s77, s77, 0x22200
	v_lshrrev_b32_e32 v248, 4, v206
	v_and_b32_e32 v249, 1, v248
	v_lshrrev_b32_e32 v250, 1, v248
	v_lshlrev_b32_e32 v249, 6, v249
	v_lshl_add_u32 v253, v250, 1, v249
	v_and_b32_e32 v248, 15, v206
	v_cmp_eq_u32_e64 s[78:79], 0, v248
	v_mov_b32_e32 v244, v252
	v_mov_b32_e32 v245, 0
	v_mov_b32_e32 v246, 0
	v_mov_b32_e32 v247, 0
	v_mov_b64_e32 v[240:241], 0
	v_mov_b64_e32 v[242:243], 0
	s_nop 1
	v_smfmac_f32_16x16x64_bf16 v[240:243], v[244:247], v[232:239], v223
	s_nop 15
	s_nop 3
	s_and_saveexec_b64 s[80:81], s[78:79]
	v_cvt_u32_f32_e32 v248, v240
	v_add_u32_e32 v248, -1, v248
	v_lshl_add_u32 v248, v248, 2, s77
	v_add_u32_e32 v249, 0, v253
	ds_write_b32 v248, v249
	v_cvt_u32_f32_e32 v248, v241
	v_add_u32_e32 v248, -1, v248
	v_lshl_add_u32 v248, v248, 2, s77
	v_add_u32_e32 v249, 32, v253
	ds_write_b32 v248, v249
	v_cvt_u32_f32_e32 v248, v242
	v_add_u32_e32 v248, -1, v248
	v_lshl_add_u32 v248, v248, 2, s77
	v_add_u32_e32 v249, 16, v253
	ds_write_b32 v248, v249
	v_cvt_u32_f32_e32 v248, v243
	v_add_u32_e32 v248, -1, v248
	v_lshl_add_u32 v248, v248, 2, s77
	v_add_u32_e32 v249, 48, v253
	ds_write_b32 v248, v249
	s_or_b64 exec, exec, s[80:81]
	v_mov_b32_e32 v244, 0
	v_mov_b32_e32 v245, v252
	v_mov_b32_e32 v246, 0
	v_mov_b32_e32 v247, 0
	v_mov_b64_e32 v[240:241], 0
	v_mov_b64_e32 v[242:243], 0
	s_nop 1
	v_smfmac_f32_16x16x64_bf16 v[240:243], v[244:247], v[232:239], v223
	s_nop 15
	s_nop 3
	s_and_saveexec_b64 s[80:81], s[78:79]
	v_cvt_u32_f32_e32 v248, v240
	v_add_u32_e32 v248, -1, v248
	v_lshl_add_u32 v248, v248, 2, s77
	v_add_u32_e32 v249, 4, v253
	ds_write_b32 v248, v249
	v_cvt_u32_f32_e32 v248, v241
	v_add_u32_e32 v248, -1, v248
	v_lshl_add_u32 v248, v248, 2, s77
	v_add_u32_e32 v249, 36, v253
	ds_write_b32 v248, v249
	v_cvt_u32_f32_e32 v248, v242
	v_add_u32_e32 v248, -1, v248
	v_lshl_add_u32 v248, v248, 2, s77
	v_add_u32_e32 v249, 20, v253
	ds_write_b32 v248, v249
	v_cvt_u32_f32_e32 v248, v243
	v_add_u32_e32 v248, -1, v248
	v_lshl_add_u32 v248, v248, 2, s77
	v_add_u32_e32 v249, 52, v253
	ds_write_b32 v248, v249
	s_or_b64 exec, exec, s[80:81]
	v_mov_b32_e32 v244, 0
	v_mov_b32_e32 v245, 0
	v_mov_b32_e32 v246, v252
	v_mov_b32_e32 v247, 0
	v_mov_b64_e32 v[240:241], 0
	v_mov_b64_e32 v[242:243], 0
	s_nop 1
	v_smfmac_f32_16x16x64_bf16 v[240:243], v[244:247], v[232:239], v223
	s_nop 15
	s_nop 3
	s_and_saveexec_b64 s[80:81], s[78:79]
	v_cvt_u32_f32_e32 v248, v240
	v_add_u32_e32 v248, -1, v248
	v_lshl_add_u32 v248, v248, 2, s77
	v_add_u32_e32 v249, 8, v253
	ds_write_b32 v248, v249
	v_cvt_u32_f32_e32 v248, v241
	v_add_u32_e32 v248, -1, v248
	v_lshl_add_u32 v248, v248, 2, s77
	v_add_u32_e32 v249, 40, v253
	ds_write_b32 v248, v249
	v_cvt_u32_f32_e32 v248, v242
	v_add_u32_e32 v248, -1, v248
	v_lshl_add_u32 v248, v248, 2, s77
	v_add_u32_e32 v249, 24, v253
	ds_write_b32 v248, v249
	v_cvt_u32_f32_e32 v248, v243
	v_add_u32_e32 v248, -1, v248
	v_lshl_add_u32 v248, v248, 2, s77
	v_add_u32_e32 v249, 56, v253
	ds_write_b32 v248, v249
	s_or_b64 exec, exec, s[80:81]
	v_mov_b32_e32 v244, 0
	v_mov_b32_e32 v245, 0
	v_mov_b32_e32 v246, 0
	v_mov_b32_e32 v247, v252
	v_mov_b64_e32 v[240:241], 0
	v_mov_b64_e32 v[242:243], 0
	s_nop 1
	v_smfmac_f32_16x16x64_bf16 v[240:243], v[244:247], v[232:239], v223
	s_nop 15
	s_nop 3
	s_and_saveexec_b64 s[80:81], s[78:79]
	v_cvt_u32_f32_e32 v248, v240
	v_add_u32_e32 v248, -1, v248
	v_lshl_add_u32 v248, v248, 2, s77
	v_add_u32_e32 v249, 12, v253
	ds_write_b32 v248, v249
	v_cvt_u32_f32_e32 v248, v241
	v_add_u32_e32 v248, -1, v248
	v_lshl_add_u32 v248, v248, 2, s77
	v_add_u32_e32 v249, 44, v253
	ds_write_b32 v248, v249
	v_cvt_u32_f32_e32 v248, v242
	v_add_u32_e32 v248, -1, v248
	v_lshl_add_u32 v248, v248, 2, s77
	v_add_u32_e32 v249, 28, v253
	ds_write_b32 v248, v249
	v_cvt_u32_f32_e32 v248, v243
	v_add_u32_e32 v248, -1, v248
	v_lshl_add_u32 v248, v248, 2, s77
	v_add_u32_e32 v249, 60, v253
	ds_write_b32 v248, v249
	s_or_b64 exec, exec, s[80:81]
	v_bfe_u32 v248, v206, 3, 2
	v_lshrrev_b32_e32 v249, 5, v206
	v_lshlrev_b32_e32 v248, 4, v248
	v_lshl_or_b32 v248, v249, 3, v248
	v_and_b32_e32 v249, 7, v206
	v_or_b32_e32 v248, v248, v249
	v_lshl_add_u32 v248, v248, 2, s77
	s_waitcnt lgkmcnt(0)
	ds_read_b32 v254, v248
	v_and_b32_e32 v248, 15, v206
	v_bfe_u32 v249, v248, 1, 2
	v_lshrrev_b32_e32 v250, 3, v248
	v_lshlrev_b32_e32 v249, 4, v249
	v_lshl_or_b32 v249, v250, 3, v249
	v_and_b32_e32 v250, 1, v248
	v_lshl_or_b32 v249, v250, 2, v249
	v_lshl_add_u32 v249, v249, 2, s77
	ds_read_b128 v[248:251], v249
	s_lshr_b32 s76, s19, 6
	s_add_i32 s76, s76, 0x20000
	v_lshrrev_b32_e32 v252, 4, v206
	v_lshl_add_u32 v252, v252, 7, s76
	s_waitcnt lgkmcnt(0)
	v_add_u32_e32 v248, v252, v248
	v_add_u32_e32 v249, v252, v249
	v_add_u32_e32 v250, v252, v250
	v_add_u32_e32 v251, v252, v251
	v_cvt_pk_bf16_f32 v236, v224, v225
	v_cvt_pk_bf16_f32 v237, v226, v227
	v_lshlrev_b32_e32 v238, 16, v236
	v_and_b32_e32 v239, 0xffff0000, v236
	v_lshlrev_b32_e32 v240, 16, v237
	v_and_b32_e32 v241, 0xffff0000, v237
	v_sub_f32_e32 v238, v224, v238
	v_sub_f32_e32 v239, v225, v239
	v_sub_f32_e32 v240, v226, v240
	v_sub_f32_e32 v241, v227, v241
	v_cvt_pk_bf16_f32 v238, v238, v239
	v_cvt_pk_bf16_f32 v239, v240, v241
	ds_write_b16 v248, v236
	ds_write_b16_d16_hi v249, v236
	ds_write_b16 v250, v237
	ds_write_b16_d16_hi v251, v237
	ds_write_b16 v248, v238 offset:2176
	ds_write_b16_d16_hi v249, v238 offset:2176
	ds_write_b16 v250, v239 offset:2176
	ds_write_b16_d16_hi v251, v239 offset:2176
	s_waitcnt vmcnt(23)
	s_waitcnt vmcnt(22)
	s_waitcnt vmcnt(21)
	s_waitcnt vmcnt(20)
	s_waitcnt vmcnt(19)
	s_waitcnt vmcnt(18)
	s_waitcnt vmcnt(17)
	s_waitcnt vmcnt(16)
	ds_read_b32 v232, v187 offset:192
	ds_read_b32 v234, v187 offset:200
	ds_read_b32 v236, v187 offset:208
	ds_read_b32 v238, v187 offset:216
	ds_read_b32 v240, v187 offset:224
	ds_read_b32 v242, v187 offset:232
	ds_read_b32 v244, v187 offset:240
	ds_read_b32 v246, v187 offset:248
	v_or_b32_e32 v103, 48, v132
	v_add_u32_e32 v104, 1, v102
	v_cmp_eq_u32_e32 vcc, v102, v103
	v_add_u32_e32 v105, 3, v102
	v_add_u32_e32 v106, 2, v102
	v_cndmask_b32_e64 v72, 0, 1.0, vcc
	v_cmp_eq_u32_e32 vcc, v104, v103
	v_or_b32_e32 v107, 50, v132
	v_or_b32_e32 v108, 52, v132
	v_cndmask_b32_e64 v73, 0, 1.0, vcc
	v_cmp_eq_u32_e32 vcc, v105, v103
	s_waitcnt lgkmcnt(0)
	v_pk_fma_f32 v[68:69], v[232:233], v[68:69], v[72:73] op_sel_hi:[0,1,1] neg_lo:[1,0,0] neg_hi:[1,0,0]
	v_cvt_pk_bf16_f32 v68, v68, v69
	v_cndmask_b32_e64 v73, 0, 1.0, vcc
	v_cmp_eq_u32_e32 vcc, v106, v103
	v_or_b32_e32 v109, 54, v132
	v_or_b32_e32 v110, 56, v132
	v_cndmask_b32_e64 v72, 0, 1.0, vcc
	v_pk_fma_f32 v[66:67], v[232:233], v[70:71], v[72:73] op_sel_hi:[0,1,1] neg_lo:[1,0,0] neg_hi:[1,0,0]
	v_cvt_pk_bf16_f32 v69, v66, v67
	ds_write_b64 v186, v[68:69]
	v_cmp_eq_u32_e32 vcc, v102, v107
	v_or_b32_e32 v111, 58, v132
	v_or_b32_e32 v112, 60, v132
	v_cndmask_b32_e64 v68, 0, 1.0, vcc
	v_cmp_eq_u32_e32 vcc, v104, v107
	v_or_b32_e32 v113, 62, v132
	v_or_b32_e32 v193, 2, v132
	v_cndmask_b32_e64 v69, 0, 1.0, vcc
	v_cmp_eq_u32_e32 vcc, v105, v107
	v_pk_fma_f32 v[68:69], v[234:235], v[78:79], v[68:69] op_sel_hi:[0,1,1] neg_lo:[1,0,0] neg_hi:[1,0,0]
	v_cvt_pk_bf16_f32 v68, v68, v69
	v_cndmask_b32_e64 v71, 0, 1.0, vcc
	v_cmp_eq_u32_e32 vcc, v106, v107
	v_or_b32_e32 v192, 4, v132
	v_or_b32_e32 v190, 6, v132
	v_cndmask_b32_e64 v70, 0, 1.0, vcc
	v_pk_fma_f32 v[66:67], v[234:235], v[80:81], v[70:71] op_sel_hi:[0,1,1] neg_lo:[1,0,0] neg_hi:[1,0,0]
	v_cvt_pk_bf16_f32 v69, v66, v67
	ds_write_b64 v186, v[68:69] offset:544
	v_cmp_eq_u32_e32 vcc, v102, v108
	v_or_b32_e32 v149, 8, v132
	v_or_b32_e32 v148, 10, v132
	v_cndmask_b32_e64 v68, 0, 1.0, vcc
	v_cmp_eq_u32_e32 vcc, v104, v108
	v_or_b32_e32 v147, 12, v132
	v_or_b32_e32 v146, 14, v132
	v_cndmask_b32_e64 v69, 0, 1.0, vcc
	v_cmp_eq_u32_e32 vcc, v105, v108
	v_pk_fma_f32 v[68:69], v[236:237], v[82:83], v[68:69] op_sel_hi:[0,1,1] neg_lo:[1,0,0] neg_hi:[1,0,0]
	v_cvt_pk_bf16_f32 v68, v68, v69
	v_cndmask_b32_e64 v71, 0, 1.0, vcc
	v_cmp_eq_u32_e32 vcc, v106, v108
	s_nop 1
	v_cndmask_b32_e64 v70, 0, 1.0, vcc
	v_pk_fma_f32 v[66:67], v[236:237], v[84:85], v[70:71] op_sel_hi:[0,1,1] neg_lo:[1,0,0] neg_hi:[1,0,0]
	v_cvt_pk_bf16_f32 v69, v66, v67
	ds_write_b64 v186, v[68:69] offset:1088
	v_cmp_eq_u32_e32 vcc, v102, v109
	s_nop 1
	v_cndmask_b32_e64 v68, 0, 1.0, vcc
	v_cmp_eq_u32_e32 vcc, v104, v109
	s_nop 1
	v_cndmask_b32_e64 v69, 0, 1.0, vcc
	v_cmp_eq_u32_e32 vcc, v105, v109
	v_pk_fma_f32 v[68:69], v[238:239], v[90:91], v[68:69] op_sel_hi:[0,1,1] neg_lo:[1,0,0] neg_hi:[1,0,0]
	v_cvt_pk_bf16_f32 v68, v68, v69
	v_cndmask_b32_e64 v71, 0, 1.0, vcc
	v_cmp_eq_u32_e32 vcc, v106, v109
	s_nop 1
	v_cndmask_b32_e64 v70, 0, 1.0, vcc
	v_pk_fma_f32 v[66:67], v[238:239], v[92:93], v[70:71] op_sel_hi:[0,1,1] neg_lo:[1,0,0] neg_hi:[1,0,0]
	v_cvt_pk_bf16_f32 v69, v66, v67
	ds_write_b64 v186, v[68:69] offset:1632
	v_cmp_eq_u32_e32 vcc, v102, v110
	s_nop 1
	v_cndmask_b32_e64 v68, 0, 1.0, vcc
	v_cmp_eq_u32_e32 vcc, v104, v110
	s_nop 1
	v_cndmask_b32_e64 v69, 0, 1.0, vcc
	v_cmp_eq_u32_e32 vcc, v105, v110
	v_pk_fma_f32 v[68:69], v[240:241], v[98:99], v[68:69] op_sel_hi:[0,1,1] neg_lo:[1,0,0] neg_hi:[1,0,0]
	v_cvt_pk_bf16_f32 v68, v68, v69
	v_cndmask_b32_e64 v71, 0, 1.0, vcc
	v_cmp_eq_u32_e32 vcc, v106, v110
	s_nop 1
	v_cndmask_b32_e64 v70, 0, 1.0, vcc
	v_pk_fma_f32 v[66:67], v[240:241], v[100:101], v[70:71] op_sel_hi:[0,1,1] neg_lo:[1,0,0] neg_hi:[1,0,0]
	v_cvt_pk_bf16_f32 v69, v66, v67
	ds_write_b64 v186, v[68:69] offset:2176
	v_cmp_eq_u32_e32 vcc, v102, v111
	s_nop 1
	v_cndmask_b32_e64 v68, 0, 1.0, vcc
	v_cmp_eq_u32_e32 vcc, v104, v111
	s_nop 1
	v_cndmask_b32_e64 v69, 0, 1.0, vcc
	v_cmp_eq_u32_e32 vcc, v105, v111
	v_pk_fma_f32 v[62:63], v[242:243], v[62:63], v[68:69] op_sel_hi:[0,1,1] neg_lo:[1,0,0] neg_hi:[1,0,0]
	v_cvt_pk_bf16_f32 v62, v62, v63
	v_cndmask_b32_e64 v69, 0, 1.0, vcc
	v_cmp_eq_u32_e32 vcc, v106, v111
	s_nop 1
	v_cndmask_b32_e64 v68, 0, 1.0, vcc
	v_pk_fma_f32 v[64:65], v[242:243], v[64:65], v[68:69] op_sel_hi:[0,1,1] neg_lo:[1,0,0] neg_hi:[1,0,0]
	v_cvt_pk_bf16_f32 v63, v64, v65
	ds_write_b64 v186, v[62:63] offset:2720
	v_cmp_eq_u32_e32 vcc, v102, v112
	s_nop 1
	v_cndmask_b32_e64 v64, 0, 1.0, vcc
	v_cmp_eq_u32_e32 vcc, v104, v112
	s_nop 1
	v_cndmask_b32_e64 v65, 0, 1.0, vcc
	v_cmp_eq_u32_e32 vcc, v105, v112
	v_pk_fma_f32 v[54:55], v[244:245], v[54:55], v[64:65] op_sel_hi:[0,1,1] neg_lo:[1,0,0] neg_hi:[1,0,0]
	v_cvt_pk_bf16_f32 v54, v54, v55
	v_cndmask_b32_e64 v65, 0, 1.0, vcc
	v_cmp_eq_u32_e32 vcc, v106, v112
	s_nop 1
	v_cndmask_b32_e64 v64, 0, 1.0, vcc
	v_pk_fma_f32 v[56:57], v[244:245], v[56:57], v[64:65] op_sel_hi:[0,1,1] neg_lo:[1,0,0] neg_hi:[1,0,0]
	v_cvt_pk_bf16_f32 v55, v56, v57
	ds_write_b64 v186, v[54:55] offset:3264
	v_cmp_eq_u32_e32 vcc, v102, v113
	s_nop 1
	v_cndmask_b32_e64 v56, 0, 1.0, vcc
	v_cmp_eq_u32_e32 vcc, v104, v113
	s_nop 1
	v_cndmask_b32_e64 v57, 0, 1.0, vcc
	v_cmp_eq_u32_e32 vcc, v105, v113
	v_pk_fma_f32 v[46:47], v[246:247], v[46:47], v[56:57] op_sel_hi:[0,1,1] neg_lo:[1,0,0] neg_hi:[1,0,0]
	v_cvt_pk_bf16_f32 v46, v46, v47
	v_cndmask_b32_e64 v57, 0, 1.0, vcc
	v_cmp_eq_u32_e32 vcc, v106, v113
	s_nop 1
	v_cndmask_b32_e64 v56, 0, 1.0, vcc
	v_pk_fma_f32 v[48:49], v[246:247], v[48:49], v[56:57] op_sel_hi:[0,1,1] neg_lo:[1,0,0] neg_hi:[1,0,0]
	v_cvt_pk_bf16_f32 v47, v48, v49
	ds_write_b64 v186, v[46:47] offset:3808
	ds_read_b128 v[46:49], v1
	s_waitcnt lgkmcnt(0)
	ds_write_b128 v184, v[46:49]
	ds_read_b128 v[46:49], v1 offset:64
	s_waitcnt lgkmcnt(0)
	ds_write_b128 v184, v[46:49] offset:1024
	ds_read_b128 v[46:49], v1 offset:128
	s_waitcnt lgkmcnt(0)
	ds_write_b128 v184, v[46:49] offset:2048
	ds_read_b128 v[46:49], v1 offset:192
	s_waitcnt lgkmcnt(0)
	ds_write_b128 v184, v[46:49] offset:3072
	s_lshl_b32 s30, s25, 2
	s_mov_b32 s31, s21
	v_lshl_add_u64 v[46:47], v[126:127], 0, s[30:31]
	v_lshl_add_u64 v[48:49], v[128:129], 0, s[30:31]
	v_lshl_add_u64 v[54:55], v[134:135], 0, s[30:31]
	v_lshl_add_u64 v[56:57], v[136:137], 0, s[30:31]
	v_lshl_add_u64 v[62:63], v[138:139], 0, s[30:31]
	v_lshl_add_u64 v[64:65], v[140:141], 0, s[30:31]
	v_lshl_add_u64 v[98:99], v[142:143], 0, s[30:31]
	v_lshl_add_u64 v[100:101], v[144:145], 0, s[30:31]
	global_load_dwordx4 v[90:93], v[46:47], off nt
	global_load_dwordx4 v[82:85], v[48:49], off nt
	global_load_dwordx4 v[78:81], v[54:55], off nt
	global_load_dwordx4 v[70:73], v[56:57], off nt
	global_load_dwordx4 v[66:69], v[62:63], off nt
	s_nop 0
	global_load_dwordx4 v[62:65], v[64:65], off nt
	s_nop 0
	global_load_dwordx4 v[54:57], v[98:99], off nt
	global_load_dwordx4 v[46:49], v[100:101], off nt
	v_mov_b32_e32 v99, v189
	s_waitcnt vmcnt(23)
	s_waitcnt vmcnt(22)
	s_waitcnt vmcnt(21)
	s_waitcnt vmcnt(20)
	s_waitcnt vmcnt(19)
	s_waitcnt vmcnt(18)
	s_waitcnt vmcnt(17)
	s_waitcnt vmcnt(16)
	ds_read_b32 v232, v187 offset:192
	ds_read_b32 v234, v187 offset:200
	ds_read_b32 v236, v187 offset:208
	ds_read_b32 v238, v187 offset:216
	ds_read_b32 v240, v187 offset:224
	ds_read_b32 v242, v187 offset:232
	ds_read_b32 v244, v187 offset:240
	ds_read_b32 v246, v187 offset:248
	v_add_u32_e32 v102, 1, v99
	v_cmp_eq_u32_e32 vcc, v99, v103
	v_add_u32_e32 v104, 3, v99
	v_add_u32_e32 v105, 2, v99
	v_cndmask_b32_e64 v100, 0, 1.0, vcc
	v_cmp_eq_u32_e32 vcc, v102, v103
	s_nop 1
	v_cndmask_b32_e64 v101, 0, 1.0, vcc
	v_cmp_eq_u32_e32 vcc, v104, v103
	s_waitcnt lgkmcnt(0)
	v_pk_fma_f32 v[94:95], v[232:233], v[94:95], v[100:101] op_sel_hi:[0,1,1] neg_lo:[1,0,0] neg_hi:[1,0,0]
	v_cvt_pk_bf16_f32 v94, v94, v95
	v_cndmask_b32_e64 v101, 0, 1.0, vcc
	v_cmp_eq_u32_e32 vcc, v105, v103
	s_nop 1
	v_cndmask_b32_e64 v100, 0, 1.0, vcc
	v_pk_fma_f32 v[96:97], v[232:233], v[96:97], v[100:101] op_sel_hi:[0,1,1] neg_lo:[1,0,0] neg_hi:[1,0,0]
	v_cvt_pk_bf16_f32 v95, v96, v97
	ds_write_b64 v186, v[94:95]
	v_cmp_eq_u32_e32 vcc, v99, v107
	s_nop 1
	v_cndmask_b32_e64 v96, 0, 1.0, vcc
	v_cmp_eq_u32_e32 vcc, v102, v107
	s_nop 1
	v_cndmask_b32_e64 v97, 0, 1.0, vcc
	v_cmp_eq_u32_e32 vcc, v104, v107
	v_pk_fma_f32 v[86:87], v[234:235], v[86:87], v[96:97] op_sel_hi:[0,1,1] neg_lo:[1,0,0] neg_hi:[1,0,0]
	v_cvt_pk_bf16_f32 v86, v86, v87
	v_cndmask_b32_e64 v97, 0, 1.0, vcc
	v_cmp_eq_u32_e32 vcc, v105, v107
	s_nop 1
	v_cndmask_b32_e64 v96, 0, 1.0, vcc
	v_pk_fma_f32 v[88:89], v[234:235], v[88:89], v[96:97] op_sel_hi:[0,1,1] neg_lo:[1,0,0] neg_hi:[1,0,0]
	v_cvt_pk_bf16_f32 v87, v88, v89
	ds_write_b64 v186, v[86:87] offset:544
	v_cmp_eq_u32_e32 vcc, v99, v108
	s_nop 1
	v_cndmask_b32_e64 v88, 0, 1.0, vcc
	v_cmp_eq_u32_e32 vcc, v102, v108
	s_nop 1
	v_cndmask_b32_e64 v89, 0, 1.0, vcc
	v_cmp_eq_u32_e32 vcc, v104, v108
	v_pk_fma_f32 v[74:75], v[236:237], v[74:75], v[88:89] op_sel_hi:[0,1,1] neg_lo:[1,0,0] neg_hi:[1,0,0]
	v_cvt_pk_bf16_f32 v74, v74, v75
	v_cndmask_b32_e64 v89, 0, 1.0, vcc
	v_cmp_eq_u32_e32 vcc, v105, v108
	s_nop 1
	v_cndmask_b32_e64 v88, 0, 1.0, vcc
	v_pk_fma_f32 v[76:77], v[236:237], v[76:77], v[88:89] op_sel_hi:[0,1,1] neg_lo:[1,0,0] neg_hi:[1,0,0]
	v_cvt_pk_bf16_f32 v75, v76, v77
	ds_write_b64 v186, v[74:75] offset:1088
	v_cmp_eq_u32_e32 vcc, v99, v109
	s_nop 1
	v_cndmask_b32_e64 v76, 0, 1.0, vcc
	v_cmp_eq_u32_e32 vcc, v102, v109
	s_nop 1
	v_cndmask_b32_e64 v77, 0, 1.0, vcc
	v_cmp_eq_u32_e32 vcc, v104, v109
	v_pk_fma_f32 v[58:59], v[238:239], v[58:59], v[76:77] op_sel_hi:[0,1,1] neg_lo:[1,0,0] neg_hi:[1,0,0]
	v_cvt_pk_bf16_f32 v58, v58, v59
	v_cndmask_b32_e64 v77, 0, 1.0, vcc
	v_cmp_eq_u32_e32 vcc, v105, v109
	s_nop 1
	v_cndmask_b32_e64 v76, 0, 1.0, vcc
	v_pk_fma_f32 v[60:61], v[238:239], v[60:61], v[76:77] op_sel_hi:[0,1,1] neg_lo:[1,0,0] neg_hi:[1,0,0]
	v_cvt_pk_bf16_f32 v59, v60, v61
	ds_write_b64 v186, v[58:59] offset:1632
	v_cmp_eq_u32_e32 vcc, v99, v110
	s_nop 1
	v_cndmask_b32_e64 v60, 0, 1.0, vcc
	v_cmp_eq_u32_e32 vcc, v102, v110
	s_nop 1
	v_cndmask_b32_e64 v61, 0, 1.0, vcc
	v_cmp_eq_u32_e32 vcc, v104, v110
	v_pk_fma_f32 v[50:51], v[240:241], v[50:51], v[60:61] op_sel_hi:[0,1,1] neg_lo:[1,0,0] neg_hi:[1,0,0]
	v_cvt_pk_bf16_f32 v50, v50, v51
	v_cndmask_b32_e64 v61, 0, 1.0, vcc
	v_cmp_eq_u32_e32 vcc, v105, v110
	s_nop 1
	v_cndmask_b32_e64 v60, 0, 1.0, vcc
	v_pk_fma_f32 v[52:53], v[240:241], v[52:53], v[60:61] op_sel_hi:[0,1,1] neg_lo:[1,0,0] neg_hi:[1,0,0]
	v_cvt_pk_bf16_f32 v51, v52, v53
	ds_write_b64 v186, v[50:51] offset:2176
	v_cmp_eq_u32_e32 vcc, v99, v111
	s_nop 1
	v_cndmask_b32_e64 v52, 0, 1.0, vcc
	v_cmp_eq_u32_e32 vcc, v102, v111
	s_nop 1
	v_cndmask_b32_e64 v53, 0, 1.0, vcc
	v_cmp_eq_u32_e32 vcc, v104, v111
	v_pk_fma_f32 v[42:43], v[242:243], v[42:43], v[52:53] op_sel_hi:[0,1,1] neg_lo:[1,0,0] neg_hi:[1,0,0]
	v_cvt_pk_bf16_f32 v42, v42, v43
	v_cndmask_b32_e64 v53, 0, 1.0, vcc
	v_cmp_eq_u32_e32 vcc, v105, v111
	s_nop 1
	v_cndmask_b32_e64 v52, 0, 1.0, vcc
	v_pk_fma_f32 v[44:45], v[242:243], v[44:45], v[52:53] op_sel_hi:[0,1,1] neg_lo:[1,0,0] neg_hi:[1,0,0]
	v_cvt_pk_bf16_f32 v43, v44, v45
	ds_write_b64 v186, v[42:43] offset:2720
	v_cmp_eq_u32_e32 vcc, v99, v112
	s_nop 1
	v_cndmask_b32_e64 v44, 0, 1.0, vcc
	v_cmp_eq_u32_e32 vcc, v102, v112
	s_nop 1
	v_cndmask_b32_e64 v45, 0, 1.0, vcc
	v_cmp_eq_u32_e32 vcc, v104, v112
	v_pk_fma_f32 v[38:39], v[244:245], v[38:39], v[44:45] op_sel_hi:[0,1,1] neg_lo:[1,0,0] neg_hi:[1,0,0]
	v_cvt_pk_bf16_f32 v38, v38, v39
	v_cndmask_b32_e64 v45, 0, 1.0, vcc
	v_cmp_eq_u32_e32 vcc, v105, v112
	s_nop 1
	v_cndmask_b32_e64 v44, 0, 1.0, vcc
	v_pk_fma_f32 v[40:41], v[244:245], v[40:41], v[44:45] op_sel_hi:[0,1,1] neg_lo:[1,0,0] neg_hi:[1,0,0]
	v_cvt_pk_bf16_f32 v39, v40, v41
	ds_write_b64 v186, v[38:39] offset:3264
	v_cmp_eq_u32_e32 vcc, v99, v113
	s_nop 1
	v_cndmask_b32_e64 v40, 0, 1.0, vcc
	v_cmp_eq_u32_e32 vcc, v102, v113
	s_nop 1
	v_cndmask_b32_e64 v41, 0, 1.0, vcc
	v_cmp_eq_u32_e32 vcc, v104, v113
	v_pk_fma_f32 v[34:35], v[246:247], v[34:35], v[40:41] op_sel_hi:[0,1,1] neg_lo:[1,0,0] neg_hi:[1,0,0]
	v_cvt_pk_bf16_f32 v34, v34, v35
	v_cndmask_b32_e64 v41, 0, 1.0, vcc
	v_cmp_eq_u32_e32 vcc, v105, v113
	s_nop 1
	v_cndmask_b32_e64 v40, 0, 1.0, vcc
	v_pk_fma_f32 v[36:37], v[246:247], v[36:37], v[40:41] op_sel_hi:[0,1,1] neg_lo:[1,0,0] neg_hi:[1,0,0]
	v_cvt_pk_bf16_f32 v35, v36, v37
	ds_write_b64 v186, v[34:35] offset:3808
	ds_read_b128 v[34:37], v1
	s_waitcnt lgkmcnt(0)
	ds_write_b128 v184, v[34:37] offset:4096
	ds_read_b128 v[34:37], v1 offset:64
	s_waitcnt lgkmcnt(0)
	ds_write_b128 v184, v[34:37] offset:5120
	ds_read_b128 v[34:37], v1 offset:128
	s_waitcnt lgkmcnt(0)
	ds_write_b128 v184, v[34:37] offset:6144
	ds_read_b128 v[34:37], v1 offset:192
	s_waitcnt lgkmcnt(0)
	ds_write_b128 v184, v[34:37] offset:7168
	s_lshl_b32 s28, s24, 2
	s_mov_b32 s29, s21
	v_lshl_add_u64 v[34:35], v[126:127], 0, s[28:29]
	v_lshl_add_u64 v[36:37], v[128:129], 0, s[28:29]
	v_lshl_add_u64 v[38:39], v[134:135], 0, s[28:29]
	v_lshl_add_u64 v[40:41], v[136:137], 0, s[28:29]
	v_lshl_add_u64 v[42:43], v[138:139], 0, s[28:29]
	v_lshl_add_u64 v[44:45], v[140:141], 0, s[28:29]
	v_lshl_add_u64 v[50:51], v[142:143], 0, s[28:29]
	v_lshl_add_u64 v[52:53], v[144:145], 0, s[28:29]
	global_load_dwordx4 v[122:125], v[34:35], off nt
	global_load_dwordx4 v[114:117], v[36:37], off nt
	global_load_dwordx4 v[106:109], v[38:39], off nt
	global_load_dwordx4 v[86:89], v[40:41], off nt
	global_load_dwordx4 v[74:77], v[42:43], off nt
	s_nop 0
	global_load_dwordx4 v[42:45], v[44:45], off nt
	s_nop 0
	global_load_dwordx4 v[38:41], v[50:51], off nt
	global_load_dwordx4 v[34:37], v[52:53], off nt
	v_mov_b32_e32 v50, v188
	s_waitcnt vmcnt(23)
	s_waitcnt vmcnt(22)
	s_waitcnt vmcnt(21)
	s_waitcnt vmcnt(20)
	s_waitcnt vmcnt(19)
	s_waitcnt vmcnt(18)
	s_waitcnt vmcnt(17)
	s_waitcnt vmcnt(16)
	ds_read_b32 v232, v187 offset:192
	ds_read_b32 v234, v187 offset:200
	ds_read_b32 v236, v187 offset:208
	ds_read_b32 v238, v187 offset:216
	ds_read_b32 v240, v187 offset:224
	ds_read_b32 v242, v187 offset:232
	ds_read_b32 v244, v187 offset:240
	ds_read_b32 v246, v187 offset:248
	s_waitcnt lgkmcnt(0)
	v_pk_fma_f32 v[30:31], v[232:233], v[30:31], 0 op_sel_hi:[0,1,0] neg_lo:[1,0,0] neg_hi:[1,0,0]
	v_pk_fma_f32 v[32:33], v[232:233], v[32:33], 0 op_sel_hi:[0,1,0] neg_lo:[1,0,0] neg_hi:[1,0,0]
	v_cvt_pk_bf16_f32 v30, v30, v31
	v_cvt_pk_bf16_f32 v31, v32, v33
	ds_write_b64 v186, v[30:31]
	v_pk_fma_f32 v[26:27], v[234:235], v[26:27], 0 op_sel_hi:[0,1,0] neg_lo:[1,0,0] neg_hi:[1,0,0]
	v_pk_fma_f32 v[28:29], v[234:235], v[28:29], 0 op_sel_hi:[0,1,0] neg_lo:[1,0,0] neg_hi:[1,0,0]
	v_cvt_pk_bf16_f32 v26, v26, v27
	v_cvt_pk_bf16_f32 v27, v28, v29
	ds_write_b64 v186, v[26:27] offset:544
	v_pk_fma_f32 v[22:23], v[236:237], v[22:23], 0 op_sel_hi:[0,1,0] neg_lo:[1,0,0] neg_hi:[1,0,0]
	v_pk_fma_f32 v[24:25], v[236:237], v[24:25], 0 op_sel_hi:[0,1,0] neg_lo:[1,0,0] neg_hi:[1,0,0]
	v_cvt_pk_bf16_f32 v22, v22, v23
	v_cvt_pk_bf16_f32 v23, v24, v25
	ds_write_b64 v186, v[22:23] offset:1088
	v_pk_fma_f32 v[18:19], v[238:239], v[18:19], 0 op_sel_hi:[0,1,0] neg_lo:[1,0,0] neg_hi:[1,0,0]
	v_pk_fma_f32 v[20:21], v[238:239], v[20:21], 0 op_sel_hi:[0,1,0] neg_lo:[1,0,0] neg_hi:[1,0,0]
	v_cvt_pk_bf16_f32 v18, v18, v19
	v_cvt_pk_bf16_f32 v19, v20, v21
	ds_write_b64 v186, v[18:19] offset:1632
	v_pk_fma_f32 v[14:15], v[240:241], v[14:15], 0 op_sel_hi:[0,1,0] neg_lo:[1,0,0] neg_hi:[1,0,0]
	v_pk_fma_f32 v[16:17], v[240:241], v[16:17], 0 op_sel_hi:[0,1,0] neg_lo:[1,0,0] neg_hi:[1,0,0]
	v_cvt_pk_bf16_f32 v14, v14, v15
	v_cvt_pk_bf16_f32 v15, v16, v17
	ds_write_b64 v186, v[14:15] offset:2176
	v_pk_fma_f32 v[10:11], v[242:243], v[10:11], 0 op_sel_hi:[0,1,0] neg_lo:[1,0,0] neg_hi:[1,0,0]
	v_pk_fma_f32 v[12:13], v[242:243], v[12:13], 0 op_sel_hi:[0,1,0] neg_lo:[1,0,0] neg_hi:[1,0,0]
	v_cvt_pk_bf16_f32 v10, v10, v11
	v_cvt_pk_bf16_f32 v11, v12, v13
	ds_write_b64 v186, v[10:11] offset:2720
	v_pk_fma_f32 v[6:7], v[244:245], v[6:7], 0 op_sel_hi:[0,1,0] neg_lo:[1,0,0] neg_hi:[1,0,0]
	v_pk_fma_f32 v[8:9], v[244:245], v[8:9], 0 op_sel_hi:[0,1,0] neg_lo:[1,0,0] neg_hi:[1,0,0]
	v_cvt_pk_bf16_f32 v6, v6, v7
	v_cvt_pk_bf16_f32 v7, v8, v9
	ds_write_b64 v186, v[6:7] offset:3264
	v_pk_fma_f32 v[2:3], v[246:247], v[2:3], 0 op_sel_hi:[0,1,0] neg_lo:[1,0,0] neg_hi:[1,0,0]
	v_pk_fma_f32 v[4:5], v[246:247], v[4:5], 0 op_sel_hi:[0,1,0] neg_lo:[1,0,0] neg_hi:[1,0,0]
	v_cvt_pk_bf16_f32 v2, v2, v3
	v_cvt_pk_bf16_f32 v3, v4, v5
	ds_write_b64 v186, v[2:3] offset:3808
	ds_read_b128 v[2:5], v1
	s_waitcnt lgkmcnt(0)
	ds_write_b128 v184, v[2:5] offset:8192
	ds_read_b128 v[2:5], v1 offset:64
	s_waitcnt lgkmcnt(0)
	ds_write_b128 v184, v[2:5] offset:9216
	ds_read_b128 v[2:5], v1 offset:128
	s_waitcnt lgkmcnt(0)
	ds_write_b128 v184, v[2:5] offset:10240
	ds_read_b128 v[2:5], v1 offset:192
	s_waitcnt lgkmcnt(0)
	ds_write_b128 v184, v[2:5] offset:11264
	s_lshl_b32 s26, s23, 2
	s_mov_b32 s27, s21
	v_lshl_add_u64 v[2:3], v[126:127], 0, s[26:27]
	v_lshl_add_u64 v[4:5], v[128:129], 0, s[26:27]
	v_lshl_add_u64 v[6:7], v[134:135], 0, s[26:27]
	v_lshl_add_u64 v[8:9], v[136:137], 0, s[26:27]
	v_lshl_add_u64 v[10:11], v[138:139], 0, s[26:27]
	v_lshl_add_u64 v[12:13], v[140:141], 0, s[26:27]
	v_lshl_add_u64 v[14:15], v[142:143], 0, s[26:27]
	v_lshl_add_u64 v[16:17], v[144:145], 0, s[26:27]
	global_load_dwordx4 v[118:121], v[2:3], off nt
	global_load_dwordx4 v[110:113], v[4:5], off nt
	global_load_dwordx4 v[102:105], v[6:7], off nt
	global_load_dwordx4 v[98:101], v[8:9], off nt
	global_load_dwordx4 v[58:61], v[10:11], off nt
	global_load_dwordx4 v[50:53], v[12:13], off nt
	global_load_dwordx4 v[30:33], v[14:15], off nt
	global_load_dwordx4 v[22:25], v[16:17], off nt
	v_mov_b32_e32 v2, v198
	s_waitcnt vmcnt(23)
	s_waitcnt vmcnt(22)
	s_waitcnt vmcnt(21)
	s_waitcnt vmcnt(20)
	s_waitcnt vmcnt(19)
	s_waitcnt vmcnt(18)
	s_waitcnt vmcnt(17)
	s_waitcnt vmcnt(16)
	ds_read_b32 v232, v187 offset:192
	ds_read_b32 v234, v187 offset:200
	ds_read_b32 v236, v187 offset:208
	ds_read_b32 v238, v187 offset:216
	ds_read_b32 v240, v187 offset:224
	ds_read_b32 v242, v187 offset:232
	ds_read_b32 v244, v187 offset:240
	ds_read_b32 v246, v187 offset:248
	s_waitcnt lgkmcnt(0)
	v_pk_fma_f32 v[4:5], v[232:233], v[90:91], 0 op_sel_hi:[0,1,0] neg_lo:[1,0,0] neg_hi:[1,0,0]
	v_pk_fma_f32 v[2:3], v[232:233], v[92:93], 0 op_sel_hi:[0,1,0] neg_lo:[1,0,0] neg_hi:[1,0,0]
	v_cvt_pk_bf16_f32 v4, v4, v5
	v_cvt_pk_bf16_f32 v5, v2, v3
	ds_write_b64 v186, v[4:5]
	v_pk_fma_f32 v[4:5], v[234:235], v[82:83], 0 op_sel_hi:[0,1,0] neg_lo:[1,0,0] neg_hi:[1,0,0]
	v_pk_fma_f32 v[2:3], v[234:235], v[84:85], 0 op_sel_hi:[0,1,0] neg_lo:[1,0,0] neg_hi:[1,0,0]
	v_cvt_pk_bf16_f32 v4, v4, v5
	v_cvt_pk_bf16_f32 v5, v2, v3
	ds_write_b64 v186, v[4:5] offset:544
	v_pk_fma_f32 v[4:5], v[236:237], v[78:79], 0 op_sel_hi:[0,1,0] neg_lo:[1,0,0] neg_hi:[1,0,0]
	v_pk_fma_f32 v[2:3], v[236:237], v[80:81], 0 op_sel_hi:[0,1,0] neg_lo:[1,0,0] neg_hi:[1,0,0]
	v_cvt_pk_bf16_f32 v4, v4, v5
	v_cvt_pk_bf16_f32 v5, v2, v3
	ds_write_b64 v186, v[4:5] offset:1088
	v_pk_fma_f32 v[4:5], v[238:239], v[70:71], 0 op_sel_hi:[0,1,0] neg_lo:[1,0,0] neg_hi:[1,0,0]
	v_pk_fma_f32 v[2:3], v[238:239], v[72:73], 0 op_sel_hi:[0,1,0] neg_lo:[1,0,0] neg_hi:[1,0,0]
	v_cvt_pk_bf16_f32 v4, v4, v5
	v_cvt_pk_bf16_f32 v5, v2, v3
	ds_write_b64 v186, v[4:5] offset:1632
	v_pk_fma_f32 v[4:5], v[240:241], v[66:67], 0 op_sel_hi:[0,1,0] neg_lo:[1,0,0] neg_hi:[1,0,0]
	v_pk_fma_f32 v[2:3], v[240:241], v[68:69], 0 op_sel_hi:[0,1,0] neg_lo:[1,0,0] neg_hi:[1,0,0]
	v_cvt_pk_bf16_f32 v4, v4, v5
	v_cvt_pk_bf16_f32 v5, v2, v3
	ds_write_b64 v186, v[4:5] offset:2176
	v_pk_fma_f32 v[4:5], v[242:243], v[62:63], 0 op_sel_hi:[0,1,0] neg_lo:[1,0,0] neg_hi:[1,0,0]
	v_pk_fma_f32 v[2:3], v[242:243], v[64:65], 0 op_sel_hi:[0,1,0] neg_lo:[1,0,0] neg_hi:[1,0,0]
	v_cvt_pk_bf16_f32 v4, v4, v5
	v_cvt_pk_bf16_f32 v5, v2, v3
	ds_write_b64 v186, v[4:5] offset:2720
	v_pk_fma_f32 v[4:5], v[244:245], v[54:55], 0 op_sel_hi:[0,1,0] neg_lo:[1,0,0] neg_hi:[1,0,0]
	v_pk_fma_f32 v[2:3], v[244:245], v[56:57], 0 op_sel_hi:[0,1,0] neg_lo:[1,0,0] neg_hi:[1,0,0]
	v_cvt_pk_bf16_f32 v4, v4, v5
	v_cvt_pk_bf16_f32 v5, v2, v3
	ds_write_b64 v186, v[4:5] offset:3264
	v_pk_fma_f32 v[4:5], v[246:247], v[46:47], 0 op_sel_hi:[0,1,0] neg_lo:[1,0,0] neg_hi:[1,0,0]
	v_pk_fma_f32 v[2:3], v[246:247], v[48:49], 0 op_sel_hi:[0,1,0] neg_lo:[1,0,0] neg_hi:[1,0,0]
	v_cvt_pk_bf16_f32 v4, v4, v5
	v_cvt_pk_bf16_f32 v5, v2, v3
	ds_write_b64 v186, v[4:5] offset:3808
	ds_read_b128 v[2:5], v1
	s_waitcnt lgkmcnt(0)
	ds_write_b128 v184, v[2:5] offset:12288
	ds_read_b128 v[2:5], v1 offset:64
	s_waitcnt lgkmcnt(0)
	ds_write_b128 v184, v[2:5] offset:13312
	ds_read_b128 v[2:5], v1 offset:128
	s_waitcnt lgkmcnt(0)
	ds_write_b128 v184, v[2:5] offset:14336
	ds_read_b128 v[2:5], v1 offset:192
	s_waitcnt lgkmcnt(0)
	ds_write_b128 v184, v[2:5] offset:15360
	s_lshl_b32 s24, s22, 2
	s_mov_b32 s25, s21
	v_lshl_add_u64 v[2:3], v[126:127], 0, s[24:25]
	v_lshl_add_u64 v[6:7], v[134:135], 0, s[24:25]
	v_lshl_add_u64 v[8:9], v[136:137], 0, s[24:25]
	v_lshl_add_u64 v[14:15], v[142:143], 0, s[24:25]
	v_lshl_add_u64 v[4:5], v[128:129], 0, s[24:25]
	v_lshl_add_u64 v[10:11], v[138:139], 0, s[24:25]
	v_lshl_add_u64 v[12:13], v[140:141], 0, s[24:25]
	v_lshl_add_u64 v[18:19], v[144:145], 0, s[24:25]
	global_load_dwordx4 v[94:97], v[2:3], off nt
	global_load_dwordx4 v[90:93], v[4:5], off nt
	global_load_dwordx4 v[82:85], v[6:7], off nt
	global_load_dwordx4 v[70:73], v[8:9], off nt
	global_load_dwordx4 v[54:57], v[10:11], off nt
	global_load_dwordx4 v[26:29], v[12:13], off nt
	s_nop 0
	global_load_dwordx4 v[14:17], v[14:15], off nt
	s_nop 0
	global_load_dwordx4 v[6:9], v[18:19], off nt
	v_mov_b32_e32 v2, v197
	s_waitcnt vmcnt(23)
	s_waitcnt vmcnt(22)
	s_waitcnt vmcnt(21)
	s_waitcnt vmcnt(20)
	s_waitcnt vmcnt(19)
	s_waitcnt vmcnt(18)
	s_waitcnt vmcnt(17)
	s_waitcnt vmcnt(16)
	ds_read_b32 v232, v187 offset:192
	ds_read_b32 v234, v187 offset:200
	ds_read_b32 v236, v187 offset:208
	ds_read_b32 v238, v187 offset:216
	ds_read_b32 v240, v187 offset:224
	ds_read_b32 v242, v187 offset:232
	ds_read_b32 v244, v187 offset:240
	ds_read_b32 v246, v187 offset:248
	s_waitcnt lgkmcnt(0)
	v_pk_fma_f32 v[4:5], v[232:233], v[122:123], 0 op_sel_hi:[0,1,0] neg_lo:[1,0,0] neg_hi:[1,0,0]
	v_pk_fma_f32 v[2:3], v[232:233], v[124:125], 0 op_sel_hi:[0,1,0] neg_lo:[1,0,0] neg_hi:[1,0,0]
	v_cvt_pk_bf16_f32 v4, v4, v5
	v_cvt_pk_bf16_f32 v5, v2, v3
	ds_write_b64 v186, v[4:5]
	v_pk_fma_f32 v[4:5], v[234:235], v[114:115], 0 op_sel_hi:[0,1,0] neg_lo:[1,0,0] neg_hi:[1,0,0]
	v_pk_fma_f32 v[2:3], v[234:235], v[116:117], 0 op_sel_hi:[0,1,0] neg_lo:[1,0,0] neg_hi:[1,0,0]
	v_cvt_pk_bf16_f32 v4, v4, v5
	v_cvt_pk_bf16_f32 v5, v2, v3
	ds_write_b64 v186, v[4:5] offset:544
	v_pk_fma_f32 v[4:5], v[236:237], v[106:107], 0 op_sel_hi:[0,1,0] neg_lo:[1,0,0] neg_hi:[1,0,0]
	v_pk_fma_f32 v[2:3], v[236:237], v[108:109], 0 op_sel_hi:[0,1,0] neg_lo:[1,0,0] neg_hi:[1,0,0]
	v_cvt_pk_bf16_f32 v4, v4, v5
	v_cvt_pk_bf16_f32 v5, v2, v3
	ds_write_b64 v186, v[4:5] offset:1088
	v_pk_fma_f32 v[4:5], v[238:239], v[86:87], 0 op_sel_hi:[0,1,0] neg_lo:[1,0,0] neg_hi:[1,0,0]
	v_pk_fma_f32 v[2:3], v[238:239], v[88:89], 0 op_sel_hi:[0,1,0] neg_lo:[1,0,0] neg_hi:[1,0,0]
	v_cvt_pk_bf16_f32 v4, v4, v5
	v_cvt_pk_bf16_f32 v5, v2, v3
	ds_write_b64 v186, v[4:5] offset:1632
	v_pk_fma_f32 v[4:5], v[240:241], v[74:75], 0 op_sel_hi:[0,1,0] neg_lo:[1,0,0] neg_hi:[1,0,0]
	v_pk_fma_f32 v[2:3], v[240:241], v[76:77], 0 op_sel_hi:[0,1,0] neg_lo:[1,0,0] neg_hi:[1,0,0]
	v_cvt_pk_bf16_f32 v4, v4, v5
	v_cvt_pk_bf16_f32 v5, v2, v3
	ds_write_b64 v186, v[4:5] offset:2176
	v_pk_fma_f32 v[4:5], v[242:243], v[42:43], 0 op_sel_hi:[0,1,0] neg_lo:[1,0,0] neg_hi:[1,0,0]
	v_pk_fma_f32 v[2:3], v[242:243], v[44:45], 0 op_sel_hi:[0,1,0] neg_lo:[1,0,0] neg_hi:[1,0,0]
	v_cvt_pk_bf16_f32 v4, v4, v5
	v_cvt_pk_bf16_f32 v5, v2, v3
	ds_write_b64 v186, v[4:5] offset:2720
	v_pk_fma_f32 v[4:5], v[244:245], v[38:39], 0 op_sel_hi:[0,1,0] neg_lo:[1,0,0] neg_hi:[1,0,0]
	v_pk_fma_f32 v[2:3], v[244:245], v[40:41], 0 op_sel_hi:[0,1,0] neg_lo:[1,0,0] neg_hi:[1,0,0]
	v_cvt_pk_bf16_f32 v4, v4, v5
	v_cvt_pk_bf16_f32 v5, v2, v3
	ds_write_b64 v186, v[4:5] offset:3264
	v_pk_fma_f32 v[4:5], v[246:247], v[34:35], 0 op_sel_hi:[0,1,0] neg_lo:[1,0,0] neg_hi:[1,0,0]
	v_pk_fma_f32 v[2:3], v[246:247], v[36:37], 0 op_sel_hi:[0,1,0] neg_lo:[1,0,0] neg_hi:[1,0,0]
	v_cvt_pk_bf16_f32 v4, v4, v5
	v_cvt_pk_bf16_f32 v5, v2, v3
	ds_write_b64 v186, v[4:5] offset:3808
	ds_read_b128 v[2:5], v1
	s_waitcnt lgkmcnt(0)
	ds_write_b128 v184, v[2:5] offset:16384
	ds_read_b128 v[2:5], v1 offset:64
	s_waitcnt lgkmcnt(0)
	ds_write_b128 v184, v[2:5] offset:17408
	ds_read_b128 v[2:5], v1 offset:128
	s_waitcnt lgkmcnt(0)
	ds_write_b128 v184, v[2:5] offset:18432
	ds_read_b128 v[2:5], v1 offset:192
	s_waitcnt lgkmcnt(0)
	ds_write_b128 v184, v[2:5] offset:19456
	s_lshl_b32 s22, s7, 2
	s_mov_b32 s23, s21
	v_lshl_add_u64 v[2:3], v[126:127], 0, s[22:23]
	v_lshl_add_u64 v[4:5], v[128:129], 0, s[22:23]
	v_lshl_add_u64 v[10:11], v[134:135], 0, s[22:23]
	v_lshl_add_u64 v[12:13], v[136:137], 0, s[22:23]
	v_lshl_add_u64 v[34:35], v[138:139], 0, s[22:23]
	v_lshl_add_u64 v[36:37], v[140:141], 0, s[22:23]
	v_lshl_add_u64 v[46:47], v[142:143], 0, s[22:23]
	v_lshl_add_u64 v[48:49], v[144:145], 0, s[22:23]
	global_load_dwordx4 v[86:89], v[2:3], off nt
	global_load_dwordx4 v[78:81], v[4:5], off nt
	global_load_dwordx4 v[66:69], v[10:11], off nt
	global_load_dwordx4 v[42:45], v[12:13], off nt
	global_load_dwordx4 v[38:41], v[34:35], off nt
	global_load_dwordx4 v[18:21], v[36:37], off nt
	s_nop 0
	global_load_dwordx4 v[10:13], v[46:47], off nt
	global_load_dwordx4 v[2:5], v[48:49], off nt
	v_mov_b32_e32 v34, v196
	s_waitcnt vmcnt(23)
	s_waitcnt vmcnt(22)
	s_waitcnt vmcnt(21)
	s_waitcnt vmcnt(20)
	s_waitcnt vmcnt(19)
	s_waitcnt vmcnt(18)
	s_waitcnt vmcnt(17)
	s_waitcnt vmcnt(16)
	ds_read_b32 v232, v187 offset:192
	ds_read_b32 v234, v187 offset:200
	ds_read_b32 v236, v187 offset:208
	ds_read_b32 v238, v187 offset:216
	ds_read_b32 v240, v187 offset:224
	ds_read_b32 v242, v187 offset:232
	ds_read_b32 v244, v187 offset:240
	ds_read_b32 v246, v187 offset:248
	s_waitcnt lgkmcnt(0)
	v_pk_fma_f32 v[36:37], v[232:233], v[118:119], 0 op_sel_hi:[0,1,0] neg_lo:[1,0,0] neg_hi:[1,0,0]
	v_pk_fma_f32 v[34:35], v[232:233], v[120:121], 0 op_sel_hi:[0,1,0] neg_lo:[1,0,0] neg_hi:[1,0,0]
	v_cvt_pk_bf16_f32 v36, v36, v37
	v_cvt_pk_bf16_f32 v37, v34, v35
	ds_write_b64 v186, v[36:37]
	v_pk_fma_f32 v[36:37], v[234:235], v[110:111], 0 op_sel_hi:[0,1,0] neg_lo:[1,0,0] neg_hi:[1,0,0]
	v_pk_fma_f32 v[34:35], v[234:235], v[112:113], 0 op_sel_hi:[0,1,0] neg_lo:[1,0,0] neg_hi:[1,0,0]
	v_cvt_pk_bf16_f32 v36, v36, v37
	v_cvt_pk_bf16_f32 v37, v34, v35
	ds_write_b64 v186, v[36:37] offset:544
	v_pk_fma_f32 v[36:37], v[236:237], v[102:103], 0 op_sel_hi:[0,1,0] neg_lo:[1,0,0] neg_hi:[1,0,0]
	v_pk_fma_f32 v[34:35], v[236:237], v[104:105], 0 op_sel_hi:[0,1,0] neg_lo:[1,0,0] neg_hi:[1,0,0]
	v_cvt_pk_bf16_f32 v36, v36, v37
	v_cvt_pk_bf16_f32 v37, v34, v35
	ds_write_b64 v186, v[36:37] offset:1088
	v_pk_fma_f32 v[36:37], v[238:239], v[98:99], 0 op_sel_hi:[0,1,0] neg_lo:[1,0,0] neg_hi:[1,0,0]
	v_pk_fma_f32 v[34:35], v[238:239], v[100:101], 0 op_sel_hi:[0,1,0] neg_lo:[1,0,0] neg_hi:[1,0,0]
	v_cvt_pk_bf16_f32 v36, v36, v37
	v_cvt_pk_bf16_f32 v37, v34, v35
	ds_write_b64 v186, v[36:37] offset:1632
	v_pk_fma_f32 v[36:37], v[240:241], v[58:59], 0 op_sel_hi:[0,1,0] neg_lo:[1,0,0] neg_hi:[1,0,0]
	v_pk_fma_f32 v[34:35], v[240:241], v[60:61], 0 op_sel_hi:[0,1,0] neg_lo:[1,0,0] neg_hi:[1,0,0]
	v_cvt_pk_bf16_f32 v36, v36, v37
	v_cvt_pk_bf16_f32 v37, v34, v35
	ds_write_b64 v186, v[36:37] offset:2176
	v_pk_fma_f32 v[36:37], v[242:243], v[50:51], 0 op_sel_hi:[0,1,0] neg_lo:[1,0,0] neg_hi:[1,0,0]
	v_pk_fma_f32 v[34:35], v[242:243], v[52:53], 0 op_sel_hi:[0,1,0] neg_lo:[1,0,0] neg_hi:[1,0,0]
	v_cvt_pk_bf16_f32 v36, v36, v37
	v_cvt_pk_bf16_f32 v37, v34, v35
	ds_write_b64 v186, v[36:37] offset:2720
	v_pk_fma_f32 v[30:31], v[244:245], v[30:31], 0 op_sel_hi:[0,1,0] neg_lo:[1,0,0] neg_hi:[1,0,0]
	v_pk_fma_f32 v[32:33], v[244:245], v[32:33], 0 op_sel_hi:[0,1,0] neg_lo:[1,0,0] neg_hi:[1,0,0]
	v_cvt_pk_bf16_f32 v30, v30, v31
	v_cvt_pk_bf16_f32 v31, v32, v33
	ds_write_b64 v186, v[30:31] offset:3264
	v_pk_fma_f32 v[22:23], v[246:247], v[22:23], 0 op_sel_hi:[0,1,0] neg_lo:[1,0,0] neg_hi:[1,0,0]
	v_pk_fma_f32 v[24:25], v[246:247], v[24:25], 0 op_sel_hi:[0,1,0] neg_lo:[1,0,0] neg_hi:[1,0,0]
	v_cvt_pk_bf16_f32 v22, v22, v23
	v_cvt_pk_bf16_f32 v23, v24, v25
	ds_write_b64 v186, v[22:23] offset:3808
	ds_read_b128 v[22:25], v1
	s_waitcnt lgkmcnt(0)
	ds_write_b128 v184, v[22:25] offset:20480
	ds_read_b128 v[22:25], v1 offset:64
	s_waitcnt lgkmcnt(0)
	ds_write_b128 v184, v[22:25] offset:21504
	ds_read_b128 v[22:25], v1 offset:128
	s_waitcnt lgkmcnt(0)
	ds_write_b128 v184, v[22:25] offset:22528
	ds_read_b128 v[22:25], v1 offset:192
	s_waitcnt lgkmcnt(0)
	ds_write_b128 v184, v[22:25] offset:23552
	v_lshl_add_u64 v[22:23], v[130:131], 0, s[30:31]
	s_movk_i32 s7, 0x2000
	v_add_co_u32_e32 v24, vcc, s7, v22
	s_movk_i32 s36, 0x4000
	s_nop 0
	v_addc_co_u32_e32 v25, vcc, 0, v23, vcc
	global_load_dwordx4 v[74:77], v[22:23], off nt
	global_load_dwordx4 v[62:65], v[24:25], off nt
	v_add_co_u32_e32 v24, vcc, s36, v22
	s_movk_i32 s37, 0x6000
	s_nop 0
	v_addc_co_u32_e32 v25, vcc, 0, v23, vcc
	v_add_co_u32_e32 v30, vcc, s37, v22
	s_mov_b32 s38, 0x8000
	s_nop 0
	v_addc_co_u32_e32 v31, vcc, 0, v23, vcc
	global_load_dwordx4 v[58:61], v[24:25], off nt
	global_load_dwordx4 v[46:49], v[30:31], off nt
	v_add_co_u32_e32 v24, vcc, s38, v22
	s_mov_b32 s39, 0xa000
	s_nop 0
	v_addc_co_u32_e32 v25, vcc, 0, v23, vcc
	v_add_co_u32_e32 v34, vcc, s39, v22
	s_mov_b32 s41, 0xc000
	s_nop 0
	v_addc_co_u32_e32 v35, vcc, 0, v23, vcc
	global_load_dwordx4 v[50:53], v[24:25], off nt
	global_load_dwordx4 v[30:33], v[34:35], off nt
	v_add_co_u32_e32 v24, vcc, s41, v22
	s_mov_b32 s42, 0xe000
	s_nop 0
	v_addc_co_u32_e32 v25, vcc, 0, v23, vcc
	v_add_co_u32_e32 v22, vcc, s42, v22
	s_nop 1
	v_addc_co_u32_e32 v23, vcc, 0, v23, vcc
	global_load_dwordx4 v[34:37], v[24:25], off nt
	s_nop 0
	global_load_dwordx4 v[22:25], v[22:23], off nt
	v_mov_b32_e32 v98, v195
	s_waitcnt vmcnt(23)
	s_waitcnt vmcnt(22)
	s_waitcnt vmcnt(21)
	s_waitcnt vmcnt(20)
	s_waitcnt vmcnt(19)
	s_waitcnt vmcnt(18)
	s_waitcnt vmcnt(17)
	s_waitcnt vmcnt(16)
	ds_read_b32 v232, v187 offset:192
	ds_read_b32 v234, v187 offset:200
	ds_read_b32 v236, v187 offset:208
	ds_read_b32 v238, v187 offset:216
	ds_read_b32 v240, v187 offset:224
	ds_read_b32 v242, v187 offset:232
	ds_read_b32 v244, v187 offset:240
	ds_read_b32 v246, v187 offset:248
	s_waitcnt lgkmcnt(0)
	v_pk_fma_f32 v[94:95], v[232:233], v[94:95], 0 op_sel_hi:[0,1,0] neg_lo:[1,0,0] neg_hi:[1,0,0]
	v_pk_fma_f32 v[96:97], v[232:233], v[96:97], 0 op_sel_hi:[0,1,0] neg_lo:[1,0,0] neg_hi:[1,0,0]
	v_cvt_pk_bf16_f32 v94, v94, v95
	v_cvt_pk_bf16_f32 v95, v96, v97
	ds_write_b64 v186, v[94:95]
	v_pk_fma_f32 v[90:91], v[234:235], v[90:91], 0 op_sel_hi:[0,1,0] neg_lo:[1,0,0] neg_hi:[1,0,0]
	v_pk_fma_f32 v[92:93], v[234:235], v[92:93], 0 op_sel_hi:[0,1,0] neg_lo:[1,0,0] neg_hi:[1,0,0]
	v_cvt_pk_bf16_f32 v90, v90, v91
	v_cvt_pk_bf16_f32 v91, v92, v93
	ds_write_b64 v186, v[90:91] offset:544
	v_pk_fma_f32 v[82:83], v[236:237], v[82:83], 0 op_sel_hi:[0,1,0] neg_lo:[1,0,0] neg_hi:[1,0,0]
	v_pk_fma_f32 v[84:85], v[236:237], v[84:85], 0 op_sel_hi:[0,1,0] neg_lo:[1,0,0] neg_hi:[1,0,0]
	v_cvt_pk_bf16_f32 v82, v82, v83
	v_cvt_pk_bf16_f32 v83, v84, v85
	ds_write_b64 v186, v[82:83] offset:1088
	v_pk_fma_f32 v[70:71], v[238:239], v[70:71], 0 op_sel_hi:[0,1,0] neg_lo:[1,0,0] neg_hi:[1,0,0]
	v_pk_fma_f32 v[72:73], v[238:239], v[72:73], 0 op_sel_hi:[0,1,0] neg_lo:[1,0,0] neg_hi:[1,0,0]
	v_cvt_pk_bf16_f32 v70, v70, v71
	v_cvt_pk_bf16_f32 v71, v72, v73
	ds_write_b64 v186, v[70:71] offset:1632
	v_pk_fma_f32 v[54:55], v[240:241], v[54:55], 0 op_sel_hi:[0,1,0] neg_lo:[1,0,0] neg_hi:[1,0,0]
	v_pk_fma_f32 v[56:57], v[240:241], v[56:57], 0 op_sel_hi:[0,1,0] neg_lo:[1,0,0] neg_hi:[1,0,0]
	v_cvt_pk_bf16_f32 v54, v54, v55
	v_cvt_pk_bf16_f32 v55, v56, v57
	ds_write_b64 v186, v[54:55] offset:2176
	v_pk_fma_f32 v[26:27], v[242:243], v[26:27], 0 op_sel_hi:[0,1,0] neg_lo:[1,0,0] neg_hi:[1,0,0]
	v_pk_fma_f32 v[28:29], v[242:243], v[28:29], 0 op_sel_hi:[0,1,0] neg_lo:[1,0,0] neg_hi:[1,0,0]
	v_cvt_pk_bf16_f32 v26, v26, v27
	v_cvt_pk_bf16_f32 v27, v28, v29
	ds_write_b64 v186, v[26:27] offset:2720
	v_pk_fma_f32 v[14:15], v[244:245], v[14:15], 0 op_sel_hi:[0,1,0] neg_lo:[1,0,0] neg_hi:[1,0,0]
	v_pk_fma_f32 v[16:17], v[244:245], v[16:17], 0 op_sel_hi:[0,1,0] neg_lo:[1,0,0] neg_hi:[1,0,0]
	v_cvt_pk_bf16_f32 v14, v14, v15
	v_cvt_pk_bf16_f32 v15, v16, v17
	ds_write_b64 v186, v[14:15] offset:3264
	v_pk_fma_f32 v[6:7], v[246:247], v[6:7], 0 op_sel_hi:[0,1,0] neg_lo:[1,0,0] neg_hi:[1,0,0]
	v_pk_fma_f32 v[8:9], v[246:247], v[8:9], 0 op_sel_hi:[0,1,0] neg_lo:[1,0,0] neg_hi:[1,0,0]
	v_cvt_pk_bf16_f32 v6, v6, v7
	v_cvt_pk_bf16_f32 v7, v8, v9
	ds_write_b64 v186, v[6:7] offset:3808
	ds_read_b128 v[6:9], v1
	s_waitcnt lgkmcnt(0)
	ds_write_b128 v184, v[6:9] offset:24576
	ds_read_b128 v[6:9], v1 offset:64
	s_waitcnt lgkmcnt(0)
	ds_write_b128 v184, v[6:9] offset:25600
	ds_read_b128 v[6:9], v1 offset:128
	s_waitcnt lgkmcnt(0)
	ds_write_b128 v184, v[6:9] offset:26624
	ds_read_b128 v[6:9], v1 offset:192
	s_waitcnt lgkmcnt(0)
	ds_write_b128 v184, v[6:9] offset:27648
	s_mov_b64 s[44:45], 0x10000
	v_lshl_add_u64 v[150:151], v[130:131], 0, s[44:45]
	s_mov_b64 s[44:45], 0x12000
	v_lshl_add_u64 v[152:153], v[130:131], 0, s[44:45]
	s_mov_b64 s[44:45], 0x14000
	v_lshl_add_u64 v[156:157], v[130:131], 0, s[44:45]
	s_mov_b64 s[44:45], 0x16000
	v_lshl_add_u64 v[158:159], v[130:131], 0, s[44:45]
	s_mov_b64 s[44:45], 0x18000
	v_lshl_add_u64 v[160:161], v[130:131], 0, s[44:45]
	s_mov_b64 s[44:45], 0x1a000
	v_lshl_add_u64 v[162:163], v[130:131], 0, s[44:45]
	s_mov_b64 s[44:45], 0x1c000
	v_lshl_add_u64 v[164:165], v[130:131], 0, s[44:45]
	s_mov_b64 s[44:45], 0x1e000
	v_lshl_add_u64 v[6:7], v[150:151], 0, s[30:31]
	v_lshl_add_u64 v[8:9], v[152:153], 0, s[30:31]
	v_lshl_add_u64 v[14:15], v[156:157], 0, s[30:31]
	v_lshl_add_u64 v[16:17], v[158:159], 0, s[30:31]
	v_lshl_add_u64 v[26:27], v[160:161], 0, s[30:31]
	v_lshl_add_u64 v[28:29], v[162:163], 0, s[30:31]
	v_lshl_add_u64 v[166:167], v[130:131], 0, s[44:45]
	v_lshl_add_u64 v[98:99], v[164:165], 0, s[30:31]
	v_lshl_add_u64 v[100:101], v[166:167], 0, s[30:31]
	global_load_dwordx4 v[94:97], v[6:7], off nt
	global_load_dwordx4 v[90:93], v[8:9], off nt
	global_load_dwordx4 v[82:85], v[14:15], off nt
	global_load_dwordx4 v[70:73], v[16:17], off nt
	global_load_dwordx4 v[54:57], v[26:27], off nt
	s_nop 0
	global_load_dwordx4 v[26:29], v[28:29], off nt
	s_nop 0
	global_load_dwordx4 v[14:17], v[98:99], off nt
	global_load_dwordx4 v[6:9], v[100:101], off nt
	v_mov_b32_e32 v98, v194
	s_waitcnt vmcnt(23)
	s_waitcnt vmcnt(22)
	s_waitcnt vmcnt(21)
	s_waitcnt vmcnt(20)
	s_waitcnt vmcnt(19)
	s_waitcnt vmcnt(18)
	s_waitcnt vmcnt(17)
	s_waitcnt vmcnt(16)
	ds_read_b32 v232, v187 offset:192
	ds_read_b32 v234, v187 offset:200
	ds_read_b32 v236, v187 offset:208
	ds_read_b32 v238, v187 offset:216
	ds_read_b32 v240, v187 offset:224
	ds_read_b32 v242, v187 offset:232
	ds_read_b32 v244, v187 offset:240
	ds_read_b32 v246, v187 offset:248
	s_waitcnt lgkmcnt(0)
	v_pk_fma_f32 v[86:87], v[232:233], v[86:87], 0 op_sel_hi:[0,1,0] neg_lo:[1,0,0] neg_hi:[1,0,0]
	v_pk_fma_f32 v[88:89], v[232:233], v[88:89], 0 op_sel_hi:[0,1,0] neg_lo:[1,0,0] neg_hi:[1,0,0]
	v_cvt_pk_bf16_f32 v86, v86, v87
	v_cvt_pk_bf16_f32 v87, v88, v89
	ds_write_b64 v186, v[86:87]
	v_pk_fma_f32 v[78:79], v[234:235], v[78:79], 0 op_sel_hi:[0,1,0] neg_lo:[1,0,0] neg_hi:[1,0,0]
	v_pk_fma_f32 v[80:81], v[234:235], v[80:81], 0 op_sel_hi:[0,1,0] neg_lo:[1,0,0] neg_hi:[1,0,0]
	v_cvt_pk_bf16_f32 v78, v78, v79
	v_cvt_pk_bf16_f32 v79, v80, v81
	ds_write_b64 v186, v[78:79] offset:544
	v_pk_fma_f32 v[66:67], v[236:237], v[66:67], 0 op_sel_hi:[0,1,0] neg_lo:[1,0,0] neg_hi:[1,0,0]
	v_pk_fma_f32 v[68:69], v[236:237], v[68:69], 0 op_sel_hi:[0,1,0] neg_lo:[1,0,0] neg_hi:[1,0,0]
	v_cvt_pk_bf16_f32 v66, v66, v67
	v_cvt_pk_bf16_f32 v67, v68, v69
	ds_write_b64 v186, v[66:67] offset:1088
	v_pk_fma_f32 v[42:43], v[238:239], v[42:43], 0 op_sel_hi:[0,1,0] neg_lo:[1,0,0] neg_hi:[1,0,0]
	v_pk_fma_f32 v[44:45], v[238:239], v[44:45], 0 op_sel_hi:[0,1,0] neg_lo:[1,0,0] neg_hi:[1,0,0]
	v_cvt_pk_bf16_f32 v42, v42, v43
	v_cvt_pk_bf16_f32 v43, v44, v45
	ds_write_b64 v186, v[42:43] offset:1632
	v_pk_fma_f32 v[38:39], v[240:241], v[38:39], 0 op_sel_hi:[0,1,0] neg_lo:[1,0,0] neg_hi:[1,0,0]
	v_pk_fma_f32 v[40:41], v[240:241], v[40:41], 0 op_sel_hi:[0,1,0] neg_lo:[1,0,0] neg_hi:[1,0,0]
	v_cvt_pk_bf16_f32 v38, v38, v39
	v_cvt_pk_bf16_f32 v39, v40, v41
	ds_write_b64 v186, v[38:39] offset:2176
	v_pk_fma_f32 v[18:19], v[242:243], v[18:19], 0 op_sel_hi:[0,1,0] neg_lo:[1,0,0] neg_hi:[1,0,0]
	v_pk_fma_f32 v[20:21], v[242:243], v[20:21], 0 op_sel_hi:[0,1,0] neg_lo:[1,0,0] neg_hi:[1,0,0]
	v_cvt_pk_bf16_f32 v18, v18, v19
	v_cvt_pk_bf16_f32 v19, v20, v21
	ds_write_b64 v186, v[18:19] offset:2720
	v_pk_fma_f32 v[10:11], v[244:245], v[10:11], 0 op_sel_hi:[0,1,0] neg_lo:[1,0,0] neg_hi:[1,0,0]
	v_pk_fma_f32 v[12:13], v[244:245], v[12:13], 0 op_sel_hi:[0,1,0] neg_lo:[1,0,0] neg_hi:[1,0,0]
	v_cvt_pk_bf16_f32 v10, v10, v11
	v_cvt_pk_bf16_f32 v11, v12, v13
	ds_write_b64 v186, v[10:11] offset:3264
	v_pk_fma_f32 v[2:3], v[246:247], v[2:3], 0 op_sel_hi:[0,1,0] neg_lo:[1,0,0] neg_hi:[1,0,0]
	v_pk_fma_f32 v[4:5], v[246:247], v[4:5], 0 op_sel_hi:[0,1,0] neg_lo:[1,0,0] neg_hi:[1,0,0]
	v_cvt_pk_bf16_f32 v2, v2, v3
	v_cvt_pk_bf16_f32 v3, v4, v5
	ds_write_b64 v186, v[2:3] offset:3808
	ds_read_b128 v[2:5], v1
	s_waitcnt lgkmcnt(0)
	ds_write_b128 v184, v[2:5] offset:28672
	ds_read_b128 v[2:5], v1 offset:64
	s_waitcnt lgkmcnt(0)
	ds_write_b128 v184, v[2:5] offset:29696
	ds_read_b128 v[2:5], v1 offset:128
	s_waitcnt lgkmcnt(0)
	ds_write_b128 v184, v[2:5] offset:30720
	ds_read_b128 v[2:5], v1 offset:192
	s_waitcnt lgkmcnt(0)
	ds_write_b128 v184, v[2:5] offset:31744
	s_mov_b64 s[44:45], 0x20000
	v_lshl_add_u64 v[168:169], v[130:131], 0, s[44:45]
	s_mov_b64 s[44:45], 0x22000
	v_lshl_add_u64 v[170:171], v[130:131], 0, s[44:45]
	s_mov_b64 s[44:45], 0x24000
	v_lshl_add_u64 v[172:173], v[130:131], 0, s[44:45]
	s_mov_b64 s[44:45], 0x26000
	v_lshl_add_u64 v[174:175], v[130:131], 0, s[44:45]
	s_mov_b64 s[44:45], 0x28000
	v_lshl_add_u64 v[176:177], v[130:131], 0, s[44:45]
	s_mov_b64 s[44:45], 0x2a000
	v_lshl_add_u64 v[178:179], v[130:131], 0, s[44:45]
	s_mov_b64 s[44:45], 0x2c000
	v_lshl_add_u64 v[180:181], v[130:131], 0, s[44:45]
	s_mov_b64 s[44:45], 0x2e000
	v_lshl_add_u64 v[2:3], v[168:169], 0, s[30:31]
	v_lshl_add_u64 v[4:5], v[170:171], 0, s[30:31]
	v_lshl_add_u64 v[10:11], v[172:173], 0, s[30:31]
	v_lshl_add_u64 v[12:13], v[174:175], 0, s[30:31]
	v_lshl_add_u64 v[18:19], v[176:177], 0, s[30:31]
	v_lshl_add_u64 v[20:21], v[178:179], 0, s[30:31]
	v_lshl_add_u64 v[182:183], v[130:131], 0, s[44:45]
	v_lshl_add_u64 v[42:43], v[180:181], 0, s[30:31]
	v_lshl_add_u64 v[44:45], v[182:183], 0, s[30:31]
	global_load_dwordx4 v[106:109], v[2:3], off nt
	global_load_dwordx4 v[98:101], v[4:5], off nt
	global_load_dwordx4 v[78:81], v[10:11], off nt
	global_load_dwordx4 v[66:69], v[12:13], off nt
	global_load_dwordx4 v[38:41], v[18:19], off nt
	s_nop 0
	global_load_dwordx4 v[18:21], v[20:21], off nt
	s_nop 0
	global_load_dwordx4 v[10:13], v[42:43], off nt
	global_load_dwordx4 v[2:5], v[44:45], off nt
	v_mov_b32_e32 v42, v198
	s_waitcnt vmcnt(23)
	s_waitcnt vmcnt(22)
	s_waitcnt vmcnt(21)
	s_waitcnt vmcnt(20)
	s_waitcnt vmcnt(19)
	s_waitcnt vmcnt(18)
	s_waitcnt vmcnt(17)
	s_waitcnt vmcnt(16)
	ds_read_b32 v232, v187 offset:0
	ds_read_b32 v234, v187 offset:8
	ds_read_b32 v236, v187 offset:16
	ds_read_b32 v238, v187 offset:24
	ds_read_b32 v240, v187 offset:32
	ds_read_b32 v242, v187 offset:40
	ds_read_b32 v244, v187 offset:48
	ds_read_b32 v246, v187 offset:56
	s_waitcnt lgkmcnt(0)
	v_pk_fma_f32 v[44:45], v[232:233], v[74:75], 0 op_sel_hi:[0,1,0] neg_lo:[1,0,0] neg_hi:[1,0,0]
	v_pk_fma_f32 v[42:43], v[232:233], v[76:77], 0 op_sel_hi:[0,1,0] neg_lo:[1,0,0] neg_hi:[1,0,0]
	v_cvt_pk_bf16_f32 v44, v44, v45
	v_cvt_pk_bf16_f32 v45, v42, v43
	ds_write_b64 v186, v[44:45]
	v_pk_fma_f32 v[44:45], v[234:235], v[62:63], 0 op_sel_hi:[0,1,0] neg_lo:[1,0,0] neg_hi:[1,0,0]
	v_pk_fma_f32 v[42:43], v[234:235], v[64:65], 0 op_sel_hi:[0,1,0] neg_lo:[1,0,0] neg_hi:[1,0,0]
	v_cvt_pk_bf16_f32 v44, v44, v45
	v_cvt_pk_bf16_f32 v45, v42, v43
	ds_write_b64 v186, v[44:45] offset:544
	v_pk_fma_f32 v[44:45], v[236:237], v[58:59], 0 op_sel_hi:[0,1,0] neg_lo:[1,0,0] neg_hi:[1,0,0]
	v_pk_fma_f32 v[42:43], v[236:237], v[60:61], 0 op_sel_hi:[0,1,0] neg_lo:[1,0,0] neg_hi:[1,0,0]
	v_cvt_pk_bf16_f32 v44, v44, v45
	v_cvt_pk_bf16_f32 v45, v42, v43
	ds_write_b64 v186, v[44:45] offset:1088
	v_pk_fma_f32 v[44:45], v[238:239], v[46:47], 0 op_sel_hi:[0,1,0] neg_lo:[1,0,0] neg_hi:[1,0,0]
	v_pk_fma_f32 v[42:43], v[238:239], v[48:49], 0 op_sel_hi:[0,1,0] neg_lo:[1,0,0] neg_hi:[1,0,0]
	v_cvt_pk_bf16_f32 v44, v44, v45
	v_cvt_pk_bf16_f32 v45, v42, v43
	ds_write_b64 v186, v[44:45] offset:1632
	v_pk_fma_f32 v[44:45], v[240:241], v[50:51], 0 op_sel_hi:[0,1,0] neg_lo:[1,0,0] neg_hi:[1,0,0]
	v_pk_fma_f32 v[42:43], v[240:241], v[52:53], 0 op_sel_hi:[0,1,0] neg_lo:[1,0,0] neg_hi:[1,0,0]
	v_cvt_pk_bf16_f32 v44, v44, v45
	v_cvt_pk_bf16_f32 v45, v42, v43
	ds_write_b64 v186, v[44:45] offset:2176
	v_pk_fma_f32 v[30:31], v[242:243], v[30:31], 0 op_sel_hi:[0,1,0] neg_lo:[1,0,0] neg_hi:[1,0,0]
	v_pk_fma_f32 v[32:33], v[242:243], v[32:33], 0 op_sel_hi:[0,1,0] neg_lo:[1,0,0] neg_hi:[1,0,0]
	v_cvt_pk_bf16_f32 v30, v30, v31
	v_cvt_pk_bf16_f32 v31, v32, v33
	ds_write_b64 v186, v[30:31] offset:2720
	v_pk_fma_f32 v[32:33], v[244:245], v[34:35], 0 op_sel_hi:[0,1,0] neg_lo:[1,0,0] neg_hi:[1,0,0]
	v_pk_fma_f32 v[30:31], v[244:245], v[36:37], 0 op_sel_hi:[0,1,0] neg_lo:[1,0,0] neg_hi:[1,0,0]
	v_cvt_pk_bf16_f32 v32, v32, v33
	v_cvt_pk_bf16_f32 v33, v30, v31
	ds_write_b64 v186, v[32:33] offset:3264
	v_pk_fma_f32 v[22:23], v[246:247], v[22:23], 0 op_sel_hi:[0,1,0] neg_lo:[1,0,0] neg_hi:[1,0,0]
	v_pk_fma_f32 v[24:25], v[246:247], v[24:25], 0 op_sel_hi:[0,1,0] neg_lo:[1,0,0] neg_hi:[1,0,0]
	v_cvt_pk_bf16_f32 v22, v22, v23
	v_cvt_pk_bf16_f32 v23, v24, v25
	ds_write_b64 v186, v[22:23] offset:3808
	ds_read_b128 a[0:3], v1
	ds_read_b128 a[4:7], v1 offset:64
	ds_read_b128 a[8:11], v1 offset:128
	ds_read_b128 a[12:15], v1 offset:192
	v_lshl_add_u64 v[22:23], v[130:131], 0, s[28:29]
	v_add_co_u32_e32 v24, vcc, s7, v22
	s_nop 1
	v_addc_co_u32_e32 v25, vcc, 0, v23, vcc
	global_load_dwordx4 v[102:105], v[22:23], off nt
	global_load_dwordx4 v[86:89], v[24:25], off nt
	v_add_co_u32_e32 v24, vcc, s36, v22
	s_nop 1
	v_addc_co_u32_e32 v25, vcc, 0, v23, vcc
	v_add_co_u32_e32 v30, vcc, s37, v22
	s_nop 1
	v_addc_co_u32_e32 v31, vcc, 0, v23, vcc
	global_load_dwordx4 v[74:77], v[24:25], off nt
	global_load_dwordx4 v[62:65], v[30:31], off nt
	v_add_co_u32_e32 v24, vcc, s38, v22
	s_nop 1
	v_addc_co_u32_e32 v25, vcc, 0, v23, vcc
	v_add_co_u32_e32 v30, vcc, s39, v22
	s_nop 1
	v_addc_co_u32_e32 v31, vcc, 0, v23, vcc
	global_load_dwordx4 v[58:61], v[24:25], off nt
	global_load_dwordx4 v[46:49], v[30:31], off nt
	v_add_co_u32_e32 v24, vcc, s41, v22
	s_nop 1
	v_addc_co_u32_e32 v25, vcc, 0, v23, vcc
	v_add_co_u32_e32 v22, vcc, s42, v22
	s_nop 1
	v_addc_co_u32_e32 v23, vcc, 0, v23, vcc
	global_load_dwordx4 v[42:45], v[24:25], off nt
	global_load_dwordx4 v[30:33], v[22:23], off nt
	v_mov_b32_e32 v22, v198
	s_waitcnt vmcnt(23)
	s_waitcnt vmcnt(22)
	s_waitcnt vmcnt(21)
	s_waitcnt vmcnt(20)
	s_waitcnt vmcnt(19)
	s_waitcnt vmcnt(18)
	s_waitcnt vmcnt(17)
	s_waitcnt vmcnt(16)
	ds_read_b32 v232, v187 offset:64
	ds_read_b32 v234, v187 offset:72
	ds_read_b32 v236, v187 offset:80
	ds_read_b32 v238, v187 offset:88
	ds_read_b32 v240, v187 offset:96
	ds_read_b32 v242, v187 offset:104
	ds_read_b32 v244, v187 offset:112
	ds_read_b32 v246, v187 offset:120
	s_waitcnt lgkmcnt(0)
	v_pk_fma_f32 v[24:25], v[232:233], v[94:95], 0 op_sel_hi:[0,1,0] neg_lo:[1,0,0] neg_hi:[1,0,0]
	v_pk_fma_f32 v[22:23], v[232:233], v[96:97], 0 op_sel_hi:[0,1,0] neg_lo:[1,0,0] neg_hi:[1,0,0]
	v_cvt_pk_bf16_f32 v24, v24, v25
	v_cvt_pk_bf16_f32 v25, v22, v23
	ds_write_b64 v186, v[24:25]
	v_pk_fma_f32 v[24:25], v[234:235], v[90:91], 0 op_sel_hi:[0,1,0] neg_lo:[1,0,0] neg_hi:[1,0,0]
	v_pk_fma_f32 v[22:23], v[234:235], v[92:93], 0 op_sel_hi:[0,1,0] neg_lo:[1,0,0] neg_hi:[1,0,0]
	v_cvt_pk_bf16_f32 v24, v24, v25
	v_cvt_pk_bf16_f32 v25, v22, v23
	ds_write_b64 v186, v[24:25] offset:544
	v_pk_fma_f32 v[24:25], v[236:237], v[82:83], 0 op_sel_hi:[0,1,0] neg_lo:[1,0,0] neg_hi:[1,0,0]
	v_pk_fma_f32 v[22:23], v[236:237], v[84:85], 0 op_sel_hi:[0,1,0] neg_lo:[1,0,0] neg_hi:[1,0,0]
	v_cvt_pk_bf16_f32 v24, v24, v25
	v_cvt_pk_bf16_f32 v25, v22, v23
	ds_write_b64 v186, v[24:25] offset:1088
	v_pk_fma_f32 v[24:25], v[238:239], v[70:71], 0 op_sel_hi:[0,1,0] neg_lo:[1,0,0] neg_hi:[1,0,0]
	v_pk_fma_f32 v[22:23], v[238:239], v[72:73], 0 op_sel_hi:[0,1,0] neg_lo:[1,0,0] neg_hi:[1,0,0]
	v_cvt_pk_bf16_f32 v24, v24, v25
	v_cvt_pk_bf16_f32 v25, v22, v23
	ds_write_b64 v186, v[24:25] offset:1632
	v_pk_fma_f32 v[24:25], v[240:241], v[54:55], 0 op_sel_hi:[0,1,0] neg_lo:[1,0,0] neg_hi:[1,0,0]
	v_pk_fma_f32 v[22:23], v[240:241], v[56:57], 0 op_sel_hi:[0,1,0] neg_lo:[1,0,0] neg_hi:[1,0,0]
	v_cvt_pk_bf16_f32 v24, v24, v25
	v_cvt_pk_bf16_f32 v25, v22, v23
	ds_write_b64 v186, v[24:25] offset:2176
	v_pk_fma_f32 v[24:25], v[242:243], v[26:27], 0 op_sel_hi:[0,1,0] neg_lo:[1,0,0] neg_hi:[1,0,0]
	v_pk_fma_f32 v[22:23], v[242:243], v[28:29], 0 op_sel_hi:[0,1,0] neg_lo:[1,0,0] neg_hi:[1,0,0]
	v_cvt_pk_bf16_f32 v24, v24, v25
	v_cvt_pk_bf16_f32 v25, v22, v23
	ds_write_b64 v186, v[24:25] offset:2720
	v_pk_fma_f32 v[14:15], v[244:245], v[14:15], 0 op_sel_hi:[0,1,0] neg_lo:[1,0,0] neg_hi:[1,0,0]
	v_pk_fma_f32 v[16:17], v[244:245], v[16:17], 0 op_sel_hi:[0,1,0] neg_lo:[1,0,0] neg_hi:[1,0,0]
	v_cvt_pk_bf16_f32 v14, v14, v15
	v_cvt_pk_bf16_f32 v15, v16, v17
	ds_write_b64 v186, v[14:15] offset:3264
	v_pk_fma_f32 v[6:7], v[246:247], v[6:7], 0 op_sel_hi:[0,1,0] neg_lo:[1,0,0] neg_hi:[1,0,0]
	v_pk_fma_f32 v[8:9], v[246:247], v[8:9], 0 op_sel_hi:[0,1,0] neg_lo:[1,0,0] neg_hi:[1,0,0]
	v_cvt_pk_bf16_f32 v6, v6, v7
	v_cvt_pk_bf16_f32 v7, v8, v9
	ds_write_b64 v186, v[6:7] offset:3808
	ds_read_b128 a[16:19], v1
	ds_read_b128 a[20:23], v1 offset:64
	ds_read_b128 a[24:27], v1 offset:128
	ds_read_b128 a[28:31], v1 offset:192
	v_lshl_add_u64 v[6:7], v[150:151], 0, s[28:29]
	v_lshl_add_u64 v[8:9], v[152:153], 0, s[28:29]
	v_lshl_add_u64 v[14:15], v[156:157], 0, s[28:29]
	v_lshl_add_u64 v[16:17], v[158:159], 0, s[28:29]
	v_lshl_add_u64 v[22:23], v[160:161], 0, s[28:29]
	v_lshl_add_u64 v[24:25], v[162:163], 0, s[28:29]
	v_lshl_add_u64 v[26:27], v[164:165], 0, s[28:29]
	v_lshl_add_u64 v[28:29], v[166:167], 0, s[28:29]
	global_load_dwordx4 v[110:113], v[6:7], off nt
	global_load_dwordx4 v[90:93], v[8:9], off nt
	global_load_dwordx4 v[70:73], v[14:15], off nt
	global_load_dwordx4 v[50:53], v[16:17], off nt
	global_load_dwordx4 v[34:37], v[22:23], off nt
	s_nop 0
	global_load_dwordx4 v[22:25], v[24:25], off nt
	s_nop 0
	global_load_dwordx4 v[14:17], v[26:27], off nt
	global_load_dwordx4 v[6:9], v[28:29], off nt
	s_waitcnt vmcnt(23)
	s_waitcnt vmcnt(22)
	s_waitcnt vmcnt(21)
	s_waitcnt vmcnt(20)
	s_waitcnt vmcnt(19)
	s_waitcnt vmcnt(18)
	s_waitcnt vmcnt(17)
	s_waitcnt vmcnt(16)
	ds_read_b32 v232, v187 offset:128
	ds_read_b32 v234, v187 offset:136
	ds_read_b32 v236, v187 offset:144
	ds_read_b32 v238, v187 offset:152
	ds_read_b32 v240, v187 offset:160
	ds_read_b32 v242, v187 offset:168
	ds_read_b32 v244, v187 offset:176
	ds_read_b32 v246, v187 offset:184
	s_waitcnt lgkmcnt(0)
	v_pk_fma_f32 v[28:29], v[232:233], v[106:107], 0 op_sel_hi:[0,1,0] neg_lo:[1,0,0] neg_hi:[1,0,0]
	v_pk_fma_f32 v[26:27], v[232:233], v[108:109], 0 op_sel_hi:[0,1,0] neg_lo:[1,0,0] neg_hi:[1,0,0]
	v_cvt_pk_bf16_f32 v28, v28, v29
	v_cvt_pk_bf16_f32 v29, v26, v27
	ds_write_b64 v186, v[28:29]
	v_pk_fma_f32 v[28:29], v[234:235], v[98:99], 0 op_sel_hi:[0,1,0] neg_lo:[1,0,0] neg_hi:[1,0,0]
	v_pk_fma_f32 v[26:27], v[234:235], v[100:101], 0 op_sel_hi:[0,1,0] neg_lo:[1,0,0] neg_hi:[1,0,0]
	v_cvt_pk_bf16_f32 v28, v28, v29
	v_cvt_pk_bf16_f32 v29, v26, v27
	ds_write_b64 v186, v[28:29] offset:544
	v_pk_fma_f32 v[28:29], v[236:237], v[78:79], 0 op_sel_hi:[0,1,0] neg_lo:[1,0,0] neg_hi:[1,0,0]
	v_pk_fma_f32 v[26:27], v[236:237], v[80:81], 0 op_sel_hi:[0,1,0] neg_lo:[1,0,0] neg_hi:[1,0,0]
	v_cvt_pk_bf16_f32 v28, v28, v29
	v_cvt_pk_bf16_f32 v29, v26, v27
	ds_write_b64 v186, v[28:29] offset:1088
	v_pk_fma_f32 v[28:29], v[238:239], v[66:67], 0 op_sel_hi:[0,1,0] neg_lo:[1,0,0] neg_hi:[1,0,0]
	v_pk_fma_f32 v[26:27], v[238:239], v[68:69], 0 op_sel_hi:[0,1,0] neg_lo:[1,0,0] neg_hi:[1,0,0]
	v_cvt_pk_bf16_f32 v28, v28, v29
	v_cvt_pk_bf16_f32 v29, v26, v27
	ds_write_b64 v186, v[28:29] offset:1632
	v_pk_fma_f32 v[28:29], v[240:241], v[38:39], 0 op_sel_hi:[0,1,0] neg_lo:[1,0,0] neg_hi:[1,0,0]
	v_pk_fma_f32 v[26:27], v[240:241], v[40:41], 0 op_sel_hi:[0,1,0] neg_lo:[1,0,0] neg_hi:[1,0,0]
	v_cvt_pk_bf16_f32 v28, v28, v29
	v_cvt_pk_bf16_f32 v29, v26, v27
	ds_write_b64 v186, v[28:29] offset:2176
	v_pk_fma_f32 v[18:19], v[242:243], v[18:19], 0 op_sel_hi:[0,1,0] neg_lo:[1,0,0] neg_hi:[1,0,0]
	v_pk_fma_f32 v[20:21], v[242:243], v[20:21], 0 op_sel_hi:[0,1,0] neg_lo:[1,0,0] neg_hi:[1,0,0]
	v_cvt_pk_bf16_f32 v18, v18, v19
	v_cvt_pk_bf16_f32 v19, v20, v21
	ds_write_b64 v186, v[18:19] offset:2720
	v_pk_fma_f32 v[10:11], v[244:245], v[10:11], 0 op_sel_hi:[0,1,0] neg_lo:[1,0,0] neg_hi:[1,0,0]
	v_pk_fma_f32 v[12:13], v[244:245], v[12:13], 0 op_sel_hi:[0,1,0] neg_lo:[1,0,0] neg_hi:[1,0,0]
	v_cvt_pk_bf16_f32 v10, v10, v11
	v_cvt_pk_bf16_f32 v11, v12, v13
	ds_write_b64 v186, v[10:11] offset:3264
	v_pk_fma_f32 v[2:3], v[246:247], v[2:3], 0 op_sel_hi:[0,1,0] neg_lo:[1,0,0] neg_hi:[1,0,0]
	v_pk_fma_f32 v[4:5], v[246:247], v[4:5], 0 op_sel_hi:[0,1,0] neg_lo:[1,0,0] neg_hi:[1,0,0]
	v_cvt_pk_bf16_f32 v2, v2, v3
	v_cvt_pk_bf16_f32 v3, v4, v5
	ds_write_b64 v186, v[2:3] offset:3808
	ds_read_b128 a[32:35], v1
	ds_read_b128 a[36:39], v1 offset:64
	ds_read_b128 a[40:43], v1 offset:128
	ds_read_b128 a[44:47], v1 offset:192
	v_lshl_add_u64 v[2:3], v[168:169], 0, s[28:29]
	v_lshl_add_u64 v[4:5], v[170:171], 0, s[28:29]
	v_lshl_add_u64 v[10:11], v[172:173], 0, s[28:29]
	v_lshl_add_u64 v[12:13], v[174:175], 0, s[28:29]
	v_lshl_add_u64 v[18:19], v[176:177], 0, s[28:29]
	v_lshl_add_u64 v[20:21], v[178:179], 0, s[28:29]
	v_lshl_add_u64 v[26:27], v[180:181], 0, s[28:29]
	v_lshl_add_u64 v[28:29], v[182:183], 0, s[28:29]
	global_load_dwordx4 v[106:109], v[2:3], off nt
	global_load_dwordx4 v[94:97], v[4:5], off nt
	global_load_dwordx4 v[66:69], v[10:11], off nt
	global_load_dwordx4 v[54:57], v[12:13], off nt
	global_load_dwordx4 v[38:41], v[18:19], off nt
	s_nop 0
	global_load_dwordx4 v[18:21], v[20:21], off nt
	s_nop 0
	global_load_dwordx4 v[10:13], v[26:27], off nt
	global_load_dwordx4 v[2:5], v[28:29], off nt
	v_mov_b32_e32 v26, v197
	s_waitcnt vmcnt(23)
	s_waitcnt vmcnt(22)
	s_waitcnt vmcnt(21)
	s_waitcnt vmcnt(20)
	s_waitcnt vmcnt(19)
	s_waitcnt vmcnt(18)
	s_waitcnt vmcnt(17)
	s_waitcnt vmcnt(16)
	ds_read_b32 v232, v187 offset:0
	ds_read_b32 v234, v187 offset:8
	ds_read_b32 v236, v187 offset:16
	ds_read_b32 v238, v187 offset:24
	ds_read_b32 v240, v187 offset:32
	ds_read_b32 v242, v187 offset:40
	ds_read_b32 v244, v187 offset:48
	ds_read_b32 v246, v187 offset:56
	s_waitcnt lgkmcnt(0)
	v_pk_fma_f32 v[28:29], v[232:233], v[102:103], 0 op_sel_hi:[0,1,0] neg_lo:[1,0,0] neg_hi:[1,0,0]
	v_pk_fma_f32 v[26:27], v[232:233], v[104:105], 0 op_sel_hi:[0,1,0] neg_lo:[1,0,0] neg_hi:[1,0,0]
	v_cvt_pk_bf16_f32 v28, v28, v29
	v_cvt_pk_bf16_f32 v29, v26, v27
	ds_write_b64 v186, v[28:29]
	v_pk_fma_f32 v[28:29], v[234:235], v[86:87], 0 op_sel_hi:[0,1,0] neg_lo:[1,0,0] neg_hi:[1,0,0]
	v_pk_fma_f32 v[26:27], v[234:235], v[88:89], 0 op_sel_hi:[0,1,0] neg_lo:[1,0,0] neg_hi:[1,0,0]
	v_cvt_pk_bf16_f32 v28, v28, v29
	v_cvt_pk_bf16_f32 v29, v26, v27
	ds_write_b64 v186, v[28:29] offset:544
	v_pk_fma_f32 v[28:29], v[236:237], v[74:75], 0 op_sel_hi:[0,1,0] neg_lo:[1,0,0] neg_hi:[1,0,0]
	v_pk_fma_f32 v[26:27], v[236:237], v[76:77], 0 op_sel_hi:[0,1,0] neg_lo:[1,0,0] neg_hi:[1,0,0]
	v_cvt_pk_bf16_f32 v28, v28, v29
	v_cvt_pk_bf16_f32 v29, v26, v27
	ds_write_b64 v186, v[28:29] offset:1088
	v_pk_fma_f32 v[28:29], v[238:239], v[62:63], 0 op_sel_hi:[0,1,0] neg_lo:[1,0,0] neg_hi:[1,0,0]
	v_pk_fma_f32 v[26:27], v[238:239], v[64:65], 0 op_sel_hi:[0,1,0] neg_lo:[1,0,0] neg_hi:[1,0,0]
	v_cvt_pk_bf16_f32 v28, v28, v29
	v_cvt_pk_bf16_f32 v29, v26, v27
	ds_write_b64 v186, v[28:29] offset:1632
	v_pk_fma_f32 v[28:29], v[240:241], v[58:59], 0 op_sel_hi:[0,1,0] neg_lo:[1,0,0] neg_hi:[1,0,0]
	v_pk_fma_f32 v[26:27], v[240:241], v[60:61], 0 op_sel_hi:[0,1,0] neg_lo:[1,0,0] neg_hi:[1,0,0]
	v_cvt_pk_bf16_f32 v28, v28, v29
	v_cvt_pk_bf16_f32 v29, v26, v27
	ds_write_b64 v186, v[28:29] offset:2176
	v_pk_fma_f32 v[28:29], v[242:243], v[46:47], 0 op_sel_hi:[0,1,0] neg_lo:[1,0,0] neg_hi:[1,0,0]
	v_pk_fma_f32 v[26:27], v[242:243], v[48:49], 0 op_sel_hi:[0,1,0] neg_lo:[1,0,0] neg_hi:[1,0,0]
	v_cvt_pk_bf16_f32 v28, v28, v29
	v_cvt_pk_bf16_f32 v29, v26, v27
	ds_write_b64 v186, v[28:29] offset:2720
	v_pk_fma_f32 v[28:29], v[244:245], v[42:43], 0 op_sel_hi:[0,1,0] neg_lo:[1,0,0] neg_hi:[1,0,0]
	v_pk_fma_f32 v[26:27], v[244:245], v[44:45], 0 op_sel_hi:[0,1,0] neg_lo:[1,0,0] neg_hi:[1,0,0]
	v_cvt_pk_bf16_f32 v28, v28, v29
	v_cvt_pk_bf16_f32 v29, v26, v27
	ds_write_b64 v186, v[28:29] offset:3264
	v_pk_fma_f32 v[28:29], v[246:247], v[30:31], 0 op_sel_hi:[0,1,0] neg_lo:[1,0,0] neg_hi:[1,0,0]
	v_pk_fma_f32 v[26:27], v[246:247], v[32:33], 0 op_sel_hi:[0,1,0] neg_lo:[1,0,0] neg_hi:[1,0,0]
	v_cvt_pk_bf16_f32 v28, v28, v29
	v_cvt_pk_bf16_f32 v29, v26, v27
	ds_write_b64 v186, v[28:29] offset:3808
	ds_read_b128 a[48:51], v1
	ds_read_b128 a[52:55], v1 offset:64
	ds_read_b128 a[56:59], v1 offset:128
	ds_read_b128 a[60:63], v1 offset:192
	v_lshl_add_u64 v[26:27], v[130:131], 0, s[26:27]
	v_add_co_u32_e32 v28, vcc, s7, v26
	s_nop 1
	v_addc_co_u32_e32 v29, vcc, 0, v27, vcc
	global_load_dwordx4 v[86:89], v[26:27], off nt
	global_load_dwordx4 v[82:85], v[28:29], off nt
	v_add_co_u32_e32 v28, vcc, s36, v26
	s_nop 1
	v_addc_co_u32_e32 v29, vcc, 0, v27, vcc
	v_add_co_u32_e32 v30, vcc, s37, v26
	s_nop 1
	v_addc_co_u32_e32 v31, vcc, 0, v27, vcc
	global_load_dwordx4 v[78:81], v[28:29], off nt
	global_load_dwordx4 v[58:61], v[30:31], off nt
	v_add_co_u32_e32 v28, vcc, s38, v26
	s_nop 1
	v_addc_co_u32_e32 v29, vcc, 0, v27, vcc
	v_add_co_u32_e32 v30, vcc, s39, v26
	s_nop 1
	v_addc_co_u32_e32 v31, vcc, 0, v27, vcc
	global_load_dwordx4 v[46:49], v[28:29], off nt
	global_load_dwordx4 v[42:45], v[30:31], off nt
	v_add_co_u32_e32 v28, vcc, s41, v26
	s_nop 1
	v_addc_co_u32_e32 v29, vcc, 0, v27, vcc
	v_add_co_u32_e32 v26, vcc, s42, v26
	s_nop 1
	v_addc_co_u32_e32 v27, vcc, 0, v27, vcc
	global_load_dwordx4 v[30:33], v[28:29], off nt
	s_nop 0
	global_load_dwordx4 v[26:29], v[26:27], off nt
	v_mov_b32_e32 v62, v197
	s_waitcnt vmcnt(23)
	s_waitcnt vmcnt(22)
	s_waitcnt vmcnt(21)
	s_waitcnt vmcnt(20)
	s_waitcnt vmcnt(19)
	s_waitcnt vmcnt(18)
	s_waitcnt vmcnt(17)
	s_waitcnt vmcnt(16)
	ds_read_b32 v232, v187 offset:64
	ds_read_b32 v234, v187 offset:72
	ds_read_b32 v236, v187 offset:80
	ds_read_b32 v238, v187 offset:88
	ds_read_b32 v240, v187 offset:96
	ds_read_b32 v242, v187 offset:104
	ds_read_b32 v244, v187 offset:112
	ds_read_b32 v246, v187 offset:120
	s_waitcnt lgkmcnt(0)
	v_pk_fma_f32 v[64:65], v[232:233], v[110:111], 0 op_sel_hi:[0,1,0] neg_lo:[1,0,0] neg_hi:[1,0,0]
	v_pk_fma_f32 v[62:63], v[232:233], v[112:113], 0 op_sel_hi:[0,1,0] neg_lo:[1,0,0] neg_hi:[1,0,0]
	v_cvt_pk_bf16_f32 v64, v64, v65
	v_cvt_pk_bf16_f32 v65, v62, v63
	ds_write_b64 v186, v[64:65]
	v_pk_fma_f32 v[64:65], v[234:235], v[90:91], 0 op_sel_hi:[0,1,0] neg_lo:[1,0,0] neg_hi:[1,0,0]
	v_pk_fma_f32 v[62:63], v[234:235], v[92:93], 0 op_sel_hi:[0,1,0] neg_lo:[1,0,0] neg_hi:[1,0,0]
	v_cvt_pk_bf16_f32 v64, v64, v65
	v_cvt_pk_bf16_f32 v65, v62, v63
	ds_write_b64 v186, v[64:65] offset:544
	v_pk_fma_f32 v[64:65], v[236:237], v[70:71], 0 op_sel_hi:[0,1,0] neg_lo:[1,0,0] neg_hi:[1,0,0]
	v_pk_fma_f32 v[62:63], v[236:237], v[72:73], 0 op_sel_hi:[0,1,0] neg_lo:[1,0,0] neg_hi:[1,0,0]
	v_cvt_pk_bf16_f32 v64, v64, v65
	v_cvt_pk_bf16_f32 v65, v62, v63
	ds_write_b64 v186, v[64:65] offset:1088
	v_pk_fma_f32 v[50:51], v[238:239], v[50:51], 0 op_sel_hi:[0,1,0] neg_lo:[1,0,0] neg_hi:[1,0,0]
	v_pk_fma_f32 v[52:53], v[238:239], v[52:53], 0 op_sel_hi:[0,1,0] neg_lo:[1,0,0] neg_hi:[1,0,0]
	v_cvt_pk_bf16_f32 v50, v50, v51
	v_cvt_pk_bf16_f32 v51, v52, v53
	ds_write_b64 v186, v[50:51] offset:1632
	v_pk_fma_f32 v[34:35], v[240:241], v[34:35], 0 op_sel_hi:[0,1,0] neg_lo:[1,0,0] neg_hi:[1,0,0]
	v_pk_fma_f32 v[36:37], v[240:241], v[36:37], 0 op_sel_hi:[0,1,0] neg_lo:[1,0,0] neg_hi:[1,0,0]
	v_cvt_pk_bf16_f32 v34, v34, v35
	v_cvt_pk_bf16_f32 v35, v36, v37
	ds_write_b64 v186, v[34:35] offset:2176
	v_pk_fma_f32 v[22:23], v[242:243], v[22:23], 0 op_sel_hi:[0,1,0] neg_lo:[1,0,0] neg_hi:[1,0,0]
	v_pk_fma_f32 v[24:25], v[242:243], v[24:25], 0 op_sel_hi:[0,1,0] neg_lo:[1,0,0] neg_hi:[1,0,0]
	v_cvt_pk_bf16_f32 v22, v22, v23
	v_cvt_pk_bf16_f32 v23, v24, v25
	ds_write_b64 v186, v[22:23] offset:2720
	v_pk_fma_f32 v[14:15], v[244:245], v[14:15], 0 op_sel_hi:[0,1,0] neg_lo:[1,0,0] neg_hi:[1,0,0]
	v_pk_fma_f32 v[16:17], v[244:245], v[16:17], 0 op_sel_hi:[0,1,0] neg_lo:[1,0,0] neg_hi:[1,0,0]
	v_cvt_pk_bf16_f32 v14, v14, v15
	v_cvt_pk_bf16_f32 v15, v16, v17
	ds_write_b64 v186, v[14:15] offset:3264
	v_pk_fma_f32 v[6:7], v[246:247], v[6:7], 0 op_sel_hi:[0,1,0] neg_lo:[1,0,0] neg_hi:[1,0,0]
	v_pk_fma_f32 v[8:9], v[246:247], v[8:9], 0 op_sel_hi:[0,1,0] neg_lo:[1,0,0] neg_hi:[1,0,0]
	v_cvt_pk_bf16_f32 v6, v6, v7
	v_cvt_pk_bf16_f32 v7, v8, v9
	ds_write_b64 v186, v[6:7] offset:3808
	ds_read_b128 a[64:67], v1
	ds_read_b128 a[68:71], v1 offset:64
	ds_read_b128 a[72:75], v1 offset:128
	ds_read_b128 a[76:79], v1 offset:192
	v_lshl_add_u64 v[6:7], v[150:151], 0, s[26:27]
	v_lshl_add_u64 v[8:9], v[152:153], 0, s[26:27]
	v_lshl_add_u64 v[14:15], v[156:157], 0, s[26:27]
	v_lshl_add_u64 v[16:17], v[158:159], 0, s[26:27]
	v_lshl_add_u64 v[22:23], v[160:161], 0, s[26:27]
	v_lshl_add_u64 v[24:25], v[162:163], 0, s[26:27]
	v_lshl_add_u64 v[70:71], v[164:165], 0, s[26:27]
	v_lshl_add_u64 v[72:73], v[166:167], 0, s[26:27]
	global_load_dwordx4 v[110:113], v[6:7], off nt
	global_load_dwordx4 v[98:101], v[8:9], off nt
	global_load_dwordx4 v[62:65], v[14:15], off nt
	global_load_dwordx4 v[50:53], v[16:17], off nt
	global_load_dwordx4 v[34:37], v[22:23], off nt
	s_nop 0
	global_load_dwordx4 v[22:25], v[24:25], off nt
	s_nop 0
	global_load_dwordx4 v[14:17], v[70:71], off nt
	global_load_dwordx4 v[6:9], v[72:73], off nt
	s_waitcnt vmcnt(23)
	s_waitcnt vmcnt(22)
	s_waitcnt vmcnt(21)
	s_waitcnt vmcnt(20)
	s_waitcnt vmcnt(19)
	s_waitcnt vmcnt(18)
	s_waitcnt vmcnt(17)
	s_waitcnt vmcnt(16)
	ds_read_b32 v232, v187 offset:128
	ds_read_b32 v234, v187 offset:136
	ds_read_b32 v236, v187 offset:144
	ds_read_b32 v238, v187 offset:152
	ds_read_b32 v240, v187 offset:160
	ds_read_b32 v242, v187 offset:168
	ds_read_b32 v244, v187 offset:176
	ds_read_b32 v246, v187 offset:184
	s_waitcnt lgkmcnt(0)
	v_pk_fma_f32 v[72:73], v[232:233], v[106:107], 0 op_sel_hi:[0,1,0] neg_lo:[1,0,0] neg_hi:[1,0,0]
	v_pk_fma_f32 v[70:71], v[232:233], v[108:109], 0 op_sel_hi:[0,1,0] neg_lo:[1,0,0] neg_hi:[1,0,0]
	v_cvt_pk_bf16_f32 v72, v72, v73
	v_cvt_pk_bf16_f32 v73, v70, v71
	ds_write_b64 v186, v[72:73]
	v_pk_fma_f32 v[72:73], v[234:235], v[94:95], 0 op_sel_hi:[0,1,0] neg_lo:[1,0,0] neg_hi:[1,0,0]
	v_pk_fma_f32 v[70:71], v[234:235], v[96:97], 0 op_sel_hi:[0,1,0] neg_lo:[1,0,0] neg_hi:[1,0,0]
	v_cvt_pk_bf16_f32 v72, v72, v73
	v_cvt_pk_bf16_f32 v73, v70, v71
	ds_write_b64 v186, v[72:73] offset:544
	v_pk_fma_f32 v[66:67], v[236:237], v[66:67], 0 op_sel_hi:[0,1,0] neg_lo:[1,0,0] neg_hi:[1,0,0]
	v_pk_fma_f32 v[68:69], v[236:237], v[68:69], 0 op_sel_hi:[0,1,0] neg_lo:[1,0,0] neg_hi:[1,0,0]
	v_cvt_pk_bf16_f32 v66, v66, v67
	v_cvt_pk_bf16_f32 v67, v68, v69
	ds_write_b64 v186, v[66:67] offset:1088
	v_pk_fma_f32 v[54:55], v[238:239], v[54:55], 0 op_sel_hi:[0,1,0] neg_lo:[1,0,0] neg_hi:[1,0,0]
	v_pk_fma_f32 v[56:57], v[238:239], v[56:57], 0 op_sel_hi:[0,1,0] neg_lo:[1,0,0] neg_hi:[1,0,0]
	v_cvt_pk_bf16_f32 v54, v54, v55
	v_cvt_pk_bf16_f32 v55, v56, v57
	ds_write_b64 v186, v[54:55] offset:1632
	v_pk_fma_f32 v[38:39], v[240:241], v[38:39], 0 op_sel_hi:[0,1,0] neg_lo:[1,0,0] neg_hi:[1,0,0]
	v_pk_fma_f32 v[40:41], v[240:241], v[40:41], 0 op_sel_hi:[0,1,0] neg_lo:[1,0,0] neg_hi:[1,0,0]
	v_cvt_pk_bf16_f32 v38, v38, v39
	v_cvt_pk_bf16_f32 v39, v40, v41
	ds_write_b64 v186, v[38:39] offset:2176
	v_pk_fma_f32 v[18:19], v[242:243], v[18:19], 0 op_sel_hi:[0,1,0] neg_lo:[1,0,0] neg_hi:[1,0,0]
	v_pk_fma_f32 v[20:21], v[242:243], v[20:21], 0 op_sel_hi:[0,1,0] neg_lo:[1,0,0] neg_hi:[1,0,0]
	v_cvt_pk_bf16_f32 v18, v18, v19
	v_cvt_pk_bf16_f32 v19, v20, v21
	ds_write_b64 v186, v[18:19] offset:2720
	v_pk_fma_f32 v[10:11], v[244:245], v[10:11], 0 op_sel_hi:[0,1,0] neg_lo:[1,0,0] neg_hi:[1,0,0]
	v_pk_fma_f32 v[12:13], v[244:245], v[12:13], 0 op_sel_hi:[0,1,0] neg_lo:[1,0,0] neg_hi:[1,0,0]
	v_cvt_pk_bf16_f32 v10, v10, v11
	v_cvt_pk_bf16_f32 v11, v12, v13
	ds_write_b64 v186, v[10:11] offset:3264
	v_pk_fma_f32 v[2:3], v[246:247], v[2:3], 0 op_sel_hi:[0,1,0] neg_lo:[1,0,0] neg_hi:[1,0,0]
	v_pk_fma_f32 v[4:5], v[246:247], v[4:5], 0 op_sel_hi:[0,1,0] neg_lo:[1,0,0] neg_hi:[1,0,0]
	v_cvt_pk_bf16_f32 v2, v2, v3
	v_cvt_pk_bf16_f32 v3, v4, v5
	ds_write_b64 v186, v[2:3] offset:3808
	ds_read_b128 a[80:83], v1
	ds_read_b128 a[84:87], v1 offset:64
	ds_read_b128 a[88:91], v1 offset:128
	ds_read_b128 a[92:95], v1 offset:192
	v_lshl_add_u64 v[2:3], v[168:169], 0, s[26:27]
	v_lshl_add_u64 v[4:5], v[170:171], 0, s[26:27]
	v_lshl_add_u64 v[10:11], v[172:173], 0, s[26:27]
	v_lshl_add_u64 v[12:13], v[174:175], 0, s[26:27]
	v_lshl_add_u64 v[18:19], v[176:177], 0, s[26:27]
	v_lshl_add_u64 v[20:21], v[178:179], 0, s[26:27]
	v_lshl_add_u64 v[66:67], v[180:181], 0, s[26:27]
	v_lshl_add_u64 v[68:69], v[182:183], 0, s[26:27]
	global_load_dwordx4 v[106:109], v[2:3], off nt
	global_load_dwordx4 v[94:97], v[4:5], off nt
	global_load_dwordx4 v[74:77], v[10:11], off nt
	global_load_dwordx4 v[54:57], v[12:13], off nt
	global_load_dwordx4 v[38:41], v[18:19], off nt
	s_nop 0
	global_load_dwordx4 v[18:21], v[20:21], off nt
	s_nop 0
	global_load_dwordx4 v[10:13], v[66:67], off nt
	global_load_dwordx4 v[2:5], v[68:69], off nt
	v_mov_b32_e32 v66, v196
	s_waitcnt vmcnt(23)
	s_waitcnt vmcnt(22)
	s_waitcnt vmcnt(21)
	s_waitcnt vmcnt(20)
	s_waitcnt vmcnt(19)
	s_waitcnt vmcnt(18)
	s_waitcnt vmcnt(17)
	s_waitcnt vmcnt(16)
	ds_read_b32 v232, v187 offset:0
	ds_read_b32 v234, v187 offset:8
	ds_read_b32 v236, v187 offset:16
	ds_read_b32 v238, v187 offset:24
	ds_read_b32 v240, v187 offset:32
	ds_read_b32 v242, v187 offset:40
	ds_read_b32 v244, v187 offset:48
	ds_read_b32 v246, v187 offset:56
	s_waitcnt lgkmcnt(0)
	v_pk_fma_f32 v[68:69], v[232:233], v[86:87], 0 op_sel_hi:[0,1,0] neg_lo:[1,0,0] neg_hi:[1,0,0]
	v_pk_fma_f32 v[66:67], v[232:233], v[88:89], 0 op_sel_hi:[0,1,0] neg_lo:[1,0,0] neg_hi:[1,0,0]
	v_cvt_pk_bf16_f32 v68, v68, v69
	v_cvt_pk_bf16_f32 v69, v66, v67
	ds_write_b64 v186, v[68:69]
	v_pk_fma_f32 v[68:69], v[234:235], v[82:83], 0 op_sel_hi:[0,1,0] neg_lo:[1,0,0] neg_hi:[1,0,0]
	v_pk_fma_f32 v[66:67], v[234:235], v[84:85], 0 op_sel_hi:[0,1,0] neg_lo:[1,0,0] neg_hi:[1,0,0]
	v_cvt_pk_bf16_f32 v68, v68, v69
	v_cvt_pk_bf16_f32 v69, v66, v67
	ds_write_b64 v186, v[68:69] offset:544
	v_pk_fma_f32 v[68:69], v[236:237], v[78:79], 0 op_sel_hi:[0,1,0] neg_lo:[1,0,0] neg_hi:[1,0,0]
	v_pk_fma_f32 v[66:67], v[236:237], v[80:81], 0 op_sel_hi:[0,1,0] neg_lo:[1,0,0] neg_hi:[1,0,0]
	v_cvt_pk_bf16_f32 v68, v68, v69
	v_cvt_pk_bf16_f32 v69, v66, v67
	ds_write_b64 v186, v[68:69] offset:1088
	v_pk_fma_f32 v[58:59], v[238:239], v[58:59], 0 op_sel_hi:[0,1,0] neg_lo:[1,0,0] neg_hi:[1,0,0]
	v_pk_fma_f32 v[60:61], v[238:239], v[60:61], 0 op_sel_hi:[0,1,0] neg_lo:[1,0,0] neg_hi:[1,0,0]
	v_cvt_pk_bf16_f32 v58, v58, v59
	v_cvt_pk_bf16_f32 v59, v60, v61
	ds_write_b64 v186, v[58:59] offset:1632
	v_pk_fma_f32 v[46:47], v[240:241], v[46:47], 0 op_sel_hi:[0,1,0] neg_lo:[1,0,0] neg_hi:[1,0,0]
	v_pk_fma_f32 v[48:49], v[240:241], v[48:49], 0 op_sel_hi:[0,1,0] neg_lo:[1,0,0] neg_hi:[1,0,0]
	v_cvt_pk_bf16_f32 v46, v46, v47
	v_cvt_pk_bf16_f32 v47, v48, v49
	ds_write_b64 v186, v[46:47] offset:2176
	v_pk_fma_f32 v[42:43], v[242:243], v[42:43], 0 op_sel_hi:[0,1,0] neg_lo:[1,0,0] neg_hi:[1,0,0]
	v_pk_fma_f32 v[44:45], v[242:243], v[44:45], 0 op_sel_hi:[0,1,0] neg_lo:[1,0,0] neg_hi:[1,0,0]
	v_cvt_pk_bf16_f32 v42, v42, v43
	v_cvt_pk_bf16_f32 v43, v44, v45
	ds_write_b64 v186, v[42:43] offset:2720
	v_pk_fma_f32 v[30:31], v[244:245], v[30:31], 0 op_sel_hi:[0,1,0] neg_lo:[1,0,0] neg_hi:[1,0,0]
	v_pk_fma_f32 v[32:33], v[244:245], v[32:33], 0 op_sel_hi:[0,1,0] neg_lo:[1,0,0] neg_hi:[1,0,0]
	v_cvt_pk_bf16_f32 v30, v30, v31
	v_cvt_pk_bf16_f32 v31, v32, v33
	ds_write_b64 v186, v[30:31] offset:3264
	v_pk_fma_f32 v[26:27], v[246:247], v[26:27], 0 op_sel_hi:[0,1,0] neg_lo:[1,0,0] neg_hi:[1,0,0]
	v_pk_fma_f32 v[28:29], v[246:247], v[28:29], 0 op_sel_hi:[0,1,0] neg_lo:[1,0,0] neg_hi:[1,0,0]
	v_cvt_pk_bf16_f32 v26, v26, v27
	v_cvt_pk_bf16_f32 v27, v28, v29
	ds_write_b64 v186, v[26:27] offset:3808
	ds_read_b128 a[96:99], v1
	ds_read_b128 a[100:103], v1 offset:64
	ds_read_b128 a[104:107], v1 offset:128
	ds_read_b128 a[108:111], v1 offset:192
	v_lshl_add_u64 v[26:27], v[130:131], 0, s[24:25]
	v_add_co_u32_e32 v28, vcc, s7, v26
	s_nop 1
	v_addc_co_u32_e32 v29, vcc, 0, v27, vcc
	global_load_dwordx4 v[102:105], v[26:27], off nt
	global_load_dwordx4 v[90:93], v[28:29], off nt
	v_add_co_u32_e32 v28, vcc, s36, v26
	s_nop 1
	v_addc_co_u32_e32 v29, vcc, 0, v27, vcc
	v_add_co_u32_e32 v30, vcc, s37, v26
	s_nop 1
	v_addc_co_u32_e32 v31, vcc, 0, v27, vcc
	global_load_dwordx4 v[86:89], v[28:29], off nt
	global_load_dwordx4 v[70:73], v[30:31], off nt
	v_add_co_u32_e32 v28, vcc, s38, v26
	s_nop 1
	v_addc_co_u32_e32 v29, vcc, 0, v27, vcc
	v_add_co_u32_e32 v30, vcc, s39, v26
	s_nop 1
	v_addc_co_u32_e32 v31, vcc, 0, v27, vcc
	global_load_dwordx4 v[66:69], v[28:29], off nt
	global_load_dwordx4 v[46:49], v[30:31], off nt
	v_add_co_u32_e32 v28, vcc, s41, v26
	s_nop 1
	v_addc_co_u32_e32 v29, vcc, 0, v27, vcc
	v_add_co_u32_e32 v26, vcc, s42, v26
	s_nop 1
	v_addc_co_u32_e32 v27, vcc, 0, v27, vcc
	global_load_dwordx4 v[42:45], v[28:29], off nt
	global_load_dwordx4 v[30:33], v[26:27], off nt
	v_mov_b32_e32 v26, v196
	s_waitcnt vmcnt(23)
	s_waitcnt vmcnt(22)
	s_waitcnt vmcnt(21)
	s_waitcnt vmcnt(20)
	s_waitcnt vmcnt(19)
	s_waitcnt vmcnt(18)
	s_waitcnt vmcnt(17)
	s_waitcnt vmcnt(16)
	ds_read_b32 v232, v187 offset:64
	ds_read_b32 v234, v187 offset:72
	ds_read_b32 v236, v187 offset:80
	ds_read_b32 v238, v187 offset:88
	ds_read_b32 v240, v187 offset:96
	ds_read_b32 v242, v187 offset:104
	ds_read_b32 v244, v187 offset:112
	ds_read_b32 v246, v187 offset:120
	s_waitcnt lgkmcnt(0)
	v_pk_fma_f32 v[28:29], v[232:233], v[110:111], 0 op_sel_hi:[0,1,0] neg_lo:[1,0,0] neg_hi:[1,0,0]
	v_pk_fma_f32 v[26:27], v[232:233], v[112:113], 0 op_sel_hi:[0,1,0] neg_lo:[1,0,0] neg_hi:[1,0,0]
	v_cvt_pk_bf16_f32 v28, v28, v29
	v_cvt_pk_bf16_f32 v29, v26, v27
	ds_write_b64 v186, v[28:29]
	v_pk_fma_f32 v[28:29], v[234:235], v[98:99], 0 op_sel_hi:[0,1,0] neg_lo:[1,0,0] neg_hi:[1,0,0]
	v_pk_fma_f32 v[26:27], v[234:235], v[100:101], 0 op_sel_hi:[0,1,0] neg_lo:[1,0,0] neg_hi:[1,0,0]
	v_cvt_pk_bf16_f32 v28, v28, v29
	v_cvt_pk_bf16_f32 v29, v26, v27
	ds_write_b64 v186, v[28:29] offset:544
	v_pk_fma_f32 v[28:29], v[236:237], v[62:63], 0 op_sel_hi:[0,1,0] neg_lo:[1,0,0] neg_hi:[1,0,0]
	v_pk_fma_f32 v[26:27], v[236:237], v[64:65], 0 op_sel_hi:[0,1,0] neg_lo:[1,0,0] neg_hi:[1,0,0]
	v_cvt_pk_bf16_f32 v28, v28, v29
	v_cvt_pk_bf16_f32 v29, v26, v27
	ds_write_b64 v186, v[28:29] offset:1088
	v_pk_fma_f32 v[28:29], v[238:239], v[50:51], 0 op_sel_hi:[0,1,0] neg_lo:[1,0,0] neg_hi:[1,0,0]
	v_pk_fma_f32 v[26:27], v[238:239], v[52:53], 0 op_sel_hi:[0,1,0] neg_lo:[1,0,0] neg_hi:[1,0,0]
	v_cvt_pk_bf16_f32 v28, v28, v29
	v_cvt_pk_bf16_f32 v29, v26, v27
	ds_write_b64 v186, v[28:29] offset:1632
	v_pk_fma_f32 v[28:29], v[240:241], v[34:35], 0 op_sel_hi:[0,1,0] neg_lo:[1,0,0] neg_hi:[1,0,0]
	v_pk_fma_f32 v[26:27], v[240:241], v[36:37], 0 op_sel_hi:[0,1,0] neg_lo:[1,0,0] neg_hi:[1,0,0]
	v_cvt_pk_bf16_f32 v28, v28, v29
	v_cvt_pk_bf16_f32 v29, v26, v27
	ds_write_b64 v186, v[28:29] offset:2176
	v_pk_fma_f32 v[22:23], v[242:243], v[22:23], 0 op_sel_hi:[0,1,0] neg_lo:[1,0,0] neg_hi:[1,0,0]
	v_pk_fma_f32 v[24:25], v[242:243], v[24:25], 0 op_sel_hi:[0,1,0] neg_lo:[1,0,0] neg_hi:[1,0,0]
	v_cvt_pk_bf16_f32 v22, v22, v23
	v_cvt_pk_bf16_f32 v23, v24, v25
	ds_write_b64 v186, v[22:23] offset:2720
	v_pk_fma_f32 v[14:15], v[244:245], v[14:15], 0 op_sel_hi:[0,1,0] neg_lo:[1,0,0] neg_hi:[1,0,0]
	v_pk_fma_f32 v[16:17], v[244:245], v[16:17], 0 op_sel_hi:[0,1,0] neg_lo:[1,0,0] neg_hi:[1,0,0]
	v_cvt_pk_bf16_f32 v14, v14, v15
	v_cvt_pk_bf16_f32 v15, v16, v17
	ds_write_b64 v186, v[14:15] offset:3264
	v_pk_fma_f32 v[6:7], v[246:247], v[6:7], 0 op_sel_hi:[0,1,0] neg_lo:[1,0,0] neg_hi:[1,0,0]
	v_pk_fma_f32 v[8:9], v[246:247], v[8:9], 0 op_sel_hi:[0,1,0] neg_lo:[1,0,0] neg_hi:[1,0,0]
	v_cvt_pk_bf16_f32 v6, v6, v7
	v_cvt_pk_bf16_f32 v7, v8, v9
	ds_write_b64 v186, v[6:7] offset:3808
	ds_read_b128 a[112:115], v1
	ds_read_b128 a[116:119], v1 offset:64
	ds_read_b128 a[120:123], v1 offset:128
	ds_read_b128 a[124:127], v1 offset:192
	v_lshl_add_u64 v[6:7], v[150:151], 0, s[24:25]
	v_lshl_add_u64 v[8:9], v[152:153], 0, s[24:25]
	v_lshl_add_u64 v[14:15], v[156:157], 0, s[24:25]
	v_lshl_add_u64 v[16:17], v[158:159], 0, s[24:25]
	v_lshl_add_u64 v[22:23], v[160:161], 0, s[24:25]
	v_lshl_add_u64 v[24:25], v[162:163], 0, s[24:25]
	v_lshl_add_u64 v[26:27], v[164:165], 0, s[24:25]
	v_lshl_add_u64 v[28:29], v[166:167], 0, s[24:25]
	global_load_dwordx4 v[110:113], v[6:7], off nt
	global_load_dwordx4 v[98:101], v[8:9], off nt
	global_load_dwordx4 v[78:81], v[14:15], off nt
	global_load_dwordx4 v[58:61], v[16:17], off nt
	global_load_dwordx4 v[34:37], v[22:23], off nt
	s_nop 0
	global_load_dwordx4 v[22:25], v[24:25], off nt
	s_nop 0
	global_load_dwordx4 v[14:17], v[26:27], off nt
	global_load_dwordx4 v[6:9], v[28:29], off nt
	s_waitcnt vmcnt(23)
	s_waitcnt vmcnt(22)
	s_waitcnt vmcnt(21)
	s_waitcnt vmcnt(20)
	s_waitcnt vmcnt(19)
	s_waitcnt vmcnt(18)
	s_waitcnt vmcnt(17)
	s_waitcnt vmcnt(16)
	ds_read_b32 v232, v187 offset:128
	ds_read_b32 v234, v187 offset:136
	ds_read_b32 v236, v187 offset:144
	ds_read_b32 v238, v187 offset:152
	ds_read_b32 v240, v187 offset:160
	ds_read_b32 v242, v187 offset:168
	ds_read_b32 v244, v187 offset:176
	ds_read_b32 v246, v187 offset:184
	s_waitcnt lgkmcnt(0)
	v_pk_fma_f32 v[28:29], v[232:233], v[106:107], 0 op_sel_hi:[0,1,0] neg_lo:[1,0,0] neg_hi:[1,0,0]
	v_pk_fma_f32 v[26:27], v[232:233], v[108:109], 0 op_sel_hi:[0,1,0] neg_lo:[1,0,0] neg_hi:[1,0,0]
	v_cvt_pk_bf16_f32 v28, v28, v29
	v_cvt_pk_bf16_f32 v29, v26, v27
	ds_write_b64 v186, v[28:29]
	v_pk_fma_f32 v[28:29], v[234:235], v[94:95], 0 op_sel_hi:[0,1,0] neg_lo:[1,0,0] neg_hi:[1,0,0]
	v_pk_fma_f32 v[26:27], v[234:235], v[96:97], 0 op_sel_hi:[0,1,0] neg_lo:[1,0,0] neg_hi:[1,0,0]
	v_cvt_pk_bf16_f32 v28, v28, v29
	v_cvt_pk_bf16_f32 v29, v26, v27
	ds_write_b64 v186, v[28:29] offset:544
	v_pk_fma_f32 v[28:29], v[236:237], v[74:75], 0 op_sel_hi:[0,1,0] neg_lo:[1,0,0] neg_hi:[1,0,0]
	v_pk_fma_f32 v[26:27], v[236:237], v[76:77], 0 op_sel_hi:[0,1,0] neg_lo:[1,0,0] neg_hi:[1,0,0]
	v_cvt_pk_bf16_f32 v28, v28, v29
	v_cvt_pk_bf16_f32 v29, v26, v27
	ds_write_b64 v186, v[28:29] offset:1088
	v_pk_fma_f32 v[28:29], v[238:239], v[54:55], 0 op_sel_hi:[0,1,0] neg_lo:[1,0,0] neg_hi:[1,0,0]
	v_pk_fma_f32 v[26:27], v[238:239], v[56:57], 0 op_sel_hi:[0,1,0] neg_lo:[1,0,0] neg_hi:[1,0,0]
	v_cvt_pk_bf16_f32 v28, v28, v29
	v_cvt_pk_bf16_f32 v29, v26, v27
	ds_write_b64 v186, v[28:29] offset:1632
	v_pk_fma_f32 v[28:29], v[240:241], v[38:39], 0 op_sel_hi:[0,1,0] neg_lo:[1,0,0] neg_hi:[1,0,0]
	v_pk_fma_f32 v[26:27], v[240:241], v[40:41], 0 op_sel_hi:[0,1,0] neg_lo:[1,0,0] neg_hi:[1,0,0]
	v_cvt_pk_bf16_f32 v28, v28, v29
	v_cvt_pk_bf16_f32 v29, v26, v27
	ds_write_b64 v186, v[28:29] offset:2176
	v_pk_fma_f32 v[18:19], v[242:243], v[18:19], 0 op_sel_hi:[0,1,0] neg_lo:[1,0,0] neg_hi:[1,0,0]
	v_pk_fma_f32 v[20:21], v[242:243], v[20:21], 0 op_sel_hi:[0,1,0] neg_lo:[1,0,0] neg_hi:[1,0,0]
	v_cvt_pk_bf16_f32 v18, v18, v19
	v_cvt_pk_bf16_f32 v19, v20, v21
	ds_write_b64 v186, v[18:19] offset:2720
	v_pk_fma_f32 v[10:11], v[244:245], v[10:11], 0 op_sel_hi:[0,1,0] neg_lo:[1,0,0] neg_hi:[1,0,0]
	v_pk_fma_f32 v[12:13], v[244:245], v[12:13], 0 op_sel_hi:[0,1,0] neg_lo:[1,0,0] neg_hi:[1,0,0]
	v_cvt_pk_bf16_f32 v10, v10, v11
	v_cvt_pk_bf16_f32 v11, v12, v13
	ds_write_b64 v186, v[10:11] offset:3264
	v_pk_fma_f32 v[2:3], v[246:247], v[2:3], 0 op_sel_hi:[0,1,0] neg_lo:[1,0,0] neg_hi:[1,0,0]
	v_pk_fma_f32 v[4:5], v[246:247], v[4:5], 0 op_sel_hi:[0,1,0] neg_lo:[1,0,0] neg_hi:[1,0,0]
	v_cvt_pk_bf16_f32 v2, v2, v3
	v_cvt_pk_bf16_f32 v3, v4, v5
	ds_write_b64 v186, v[2:3] offset:3808
	ds_read_b128 a[128:131], v1
	ds_read_b128 a[132:135], v1 offset:64
	ds_read_b128 a[136:139], v1 offset:128
	ds_read_b128 a[140:143], v1 offset:192
	v_lshl_add_u64 v[2:3], v[168:169], 0, s[24:25]
	v_lshl_add_u64 v[4:5], v[170:171], 0, s[24:25]
	v_lshl_add_u64 v[10:11], v[172:173], 0, s[24:25]
	v_lshl_add_u64 v[12:13], v[174:175], 0, s[24:25]
	v_lshl_add_u64 v[18:19], v[176:177], 0, s[24:25]
	v_lshl_add_u64 v[20:21], v[178:179], 0, s[24:25]
	v_lshl_add_u64 v[50:51], v[180:181], 0, s[24:25]
	v_lshl_add_u64 v[52:53], v[182:183], 0, s[24:25]
	global_load_dwordx4 v[114:117], v[2:3], off nt
	global_load_dwordx4 v[94:97], v[4:5], off nt
	global_load_dwordx4 v[82:85], v[10:11], off nt
	global_load_dwordx4 v[62:65], v[12:13], off nt
	global_load_dwordx4 v[38:41], v[18:19], off nt
	global_load_dwordx4 v[26:29], v[20:21], off nt
	s_nop 0
	global_load_dwordx4 v[10:13], v[50:51], off nt
	global_load_dwordx4 v[2:5], v[52:53], off nt
	v_mov_b32_e32 v18, v195
	s_waitcnt vmcnt(23)
	s_waitcnt vmcnt(22)
	s_waitcnt vmcnt(21)
	s_waitcnt vmcnt(20)
	s_waitcnt vmcnt(19)
	s_waitcnt vmcnt(18)
	s_waitcnt vmcnt(17)
	s_waitcnt vmcnt(16)
	ds_read_b32 v232, v187 offset:0
	ds_read_b32 v234, v187 offset:8
	ds_read_b32 v236, v187 offset:16
	ds_read_b32 v238, v187 offset:24
	ds_read_b32 v240, v187 offset:32
	ds_read_b32 v242, v187 offset:40
	ds_read_b32 v244, v187 offset:48
	ds_read_b32 v246, v187 offset:56
	s_waitcnt lgkmcnt(0)
	v_pk_fma_f32 v[20:21], v[232:233], v[102:103], 0 op_sel_hi:[0,1,0] neg_lo:[1,0,0] neg_hi:[1,0,0]
	v_pk_fma_f32 v[18:19], v[232:233], v[104:105], 0 op_sel_hi:[0,1,0] neg_lo:[1,0,0] neg_hi:[1,0,0]
	v_cvt_pk_bf16_f32 v20, v20, v21
	v_cvt_pk_bf16_f32 v21, v18, v19
	ds_write_b64 v186, v[20:21]
	v_pk_fma_f32 v[20:21], v[234:235], v[90:91], 0 op_sel_hi:[0,1,0] neg_lo:[1,0,0] neg_hi:[1,0,0]
	v_pk_fma_f32 v[18:19], v[234:235], v[92:93], 0 op_sel_hi:[0,1,0] neg_lo:[1,0,0] neg_hi:[1,0,0]
	v_cvt_pk_bf16_f32 v20, v20, v21
	v_cvt_pk_bf16_f32 v21, v18, v19
	ds_write_b64 v186, v[20:21] offset:544
	v_pk_fma_f32 v[20:21], v[236:237], v[86:87], 0 op_sel_hi:[0,1,0] neg_lo:[1,0,0] neg_hi:[1,0,0]
	v_pk_fma_f32 v[18:19], v[236:237], v[88:89], 0 op_sel_hi:[0,1,0] neg_lo:[1,0,0] neg_hi:[1,0,0]
	v_cvt_pk_bf16_f32 v20, v20, v21
	v_cvt_pk_bf16_f32 v21, v18, v19
	ds_write_b64 v186, v[20:21] offset:1088
	v_pk_fma_f32 v[20:21], v[238:239], v[70:71], 0 op_sel_hi:[0,1,0] neg_lo:[1,0,0] neg_hi:[1,0,0]
	v_pk_fma_f32 v[18:19], v[238:239], v[72:73], 0 op_sel_hi:[0,1,0] neg_lo:[1,0,0] neg_hi:[1,0,0]
	v_cvt_pk_bf16_f32 v20, v20, v21
	v_cvt_pk_bf16_f32 v21, v18, v19
	ds_write_b64 v186, v[20:21] offset:1632
	v_pk_fma_f32 v[20:21], v[240:241], v[66:67], 0 op_sel_hi:[0,1,0] neg_lo:[1,0,0] neg_hi:[1,0,0]
	v_pk_fma_f32 v[18:19], v[240:241], v[68:69], 0 op_sel_hi:[0,1,0] neg_lo:[1,0,0] neg_hi:[1,0,0]
	v_cvt_pk_bf16_f32 v20, v20, v21
	v_cvt_pk_bf16_f32 v21, v18, v19
	ds_write_b64 v186, v[20:21] offset:2176
	v_pk_fma_f32 v[20:21], v[242:243], v[46:47], 0 op_sel_hi:[0,1,0] neg_lo:[1,0,0] neg_hi:[1,0,0]
	v_pk_fma_f32 v[18:19], v[242:243], v[48:49], 0 op_sel_hi:[0,1,0] neg_lo:[1,0,0] neg_hi:[1,0,0]
	v_cvt_pk_bf16_f32 v20, v20, v21
	v_cvt_pk_bf16_f32 v21, v18, v19
	ds_write_b64 v186, v[20:21] offset:2720
	v_pk_fma_f32 v[20:21], v[244:245], v[42:43], 0 op_sel_hi:[0,1,0] neg_lo:[1,0,0] neg_hi:[1,0,0]
	v_pk_fma_f32 v[18:19], v[244:245], v[44:45], 0 op_sel_hi:[0,1,0] neg_lo:[1,0,0] neg_hi:[1,0,0]
	v_cvt_pk_bf16_f32 v20, v20, v21
	v_cvt_pk_bf16_f32 v21, v18, v19
	ds_write_b64 v186, v[20:21] offset:3264
	v_pk_fma_f32 v[20:21], v[246:247], v[30:31], 0 op_sel_hi:[0,1,0] neg_lo:[1,0,0] neg_hi:[1,0,0]
	v_pk_fma_f32 v[18:19], v[246:247], v[32:33], 0 op_sel_hi:[0,1,0] neg_lo:[1,0,0] neg_hi:[1,0,0]
	v_cvt_pk_bf16_f32 v20, v20, v21
	v_cvt_pk_bf16_f32 v21, v18, v19
	ds_write_b64 v186, v[20:21] offset:3808
	ds_read_b128 a[144:147], v1
	ds_read_b128 a[148:151], v1 offset:64
	ds_read_b128 a[152:155], v1 offset:128
	ds_read_b128 a[156:159], v1 offset:192
	v_lshl_add_u64 v[18:19], v[130:131], 0, s[22:23]
	v_add_co_u32_e32 v20, vcc, s7, v18
	s_nop 1
	v_addc_co_u32_e32 v21, vcc, 0, v19, vcc
	global_load_dwordx4 v[106:109], v[18:19], off nt
	global_load_dwordx4 v[90:93], v[20:21], off nt
	v_add_co_u32_e32 v20, vcc, s36, v18
	s_nop 1
	v_addc_co_u32_e32 v21, vcc, 0, v19, vcc
	v_add_co_u32_e32 v30, vcc, s37, v18
	s_nop 1
	v_addc_co_u32_e32 v31, vcc, 0, v19, vcc
	global_load_dwordx4 v[86:89], v[20:21], off nt
	global_load_dwordx4 v[74:77], v[30:31], off nt
	v_add_co_u32_e32 v20, vcc, s38, v18
	s_nop 1
	v_addc_co_u32_e32 v21, vcc, 0, v19, vcc
	v_add_co_u32_e32 v30, vcc, s39, v18
	s_nop 1
	v_addc_co_u32_e32 v31, vcc, 0, v19, vcc
	global_load_dwordx4 v[70:73], v[20:21], off nt
	global_load_dwordx4 v[54:57], v[30:31], off nt
	v_add_co_u32_e32 v20, vcc, s41, v18
	s_nop 1
	v_addc_co_u32_e32 v21, vcc, 0, v19, vcc
	v_add_co_u32_e32 v18, vcc, s42, v18
	s_nop 1
	v_addc_co_u32_e32 v19, vcc, 0, v19, vcc
	global_load_dwordx4 v[50:53], v[20:21], off nt
	global_load_dwordx4 v[46:49], v[18:19], off nt
	v_mov_b32_e32 v18, v195
	s_waitcnt vmcnt(23)
	s_waitcnt vmcnt(22)
	s_waitcnt vmcnt(21)
	s_waitcnt vmcnt(20)
	s_waitcnt vmcnt(19)
	s_waitcnt vmcnt(18)
	s_waitcnt vmcnt(17)
	s_waitcnt vmcnt(16)
	ds_read_b32 v232, v187 offset:64
	ds_read_b32 v234, v187 offset:72
	ds_read_b32 v236, v187 offset:80
	ds_read_b32 v238, v187 offset:88
	ds_read_b32 v240, v187 offset:96
	ds_read_b32 v242, v187 offset:104
	ds_read_b32 v244, v187 offset:112
	ds_read_b32 v246, v187 offset:120
	s_waitcnt lgkmcnt(0)
	v_pk_fma_f32 v[20:21], v[232:233], v[110:111], 0 op_sel_hi:[0,1,0] neg_lo:[1,0,0] neg_hi:[1,0,0]
	v_pk_fma_f32 v[18:19], v[232:233], v[112:113], 0 op_sel_hi:[0,1,0] neg_lo:[1,0,0] neg_hi:[1,0,0]
	v_cvt_pk_bf16_f32 v20, v20, v21
	v_cvt_pk_bf16_f32 v21, v18, v19
	ds_write_b64 v186, v[20:21]
	v_pk_fma_f32 v[20:21], v[234:235], v[98:99], 0 op_sel_hi:[0,1,0] neg_lo:[1,0,0] neg_hi:[1,0,0]
	v_pk_fma_f32 v[18:19], v[234:235], v[100:101], 0 op_sel_hi:[0,1,0] neg_lo:[1,0,0] neg_hi:[1,0,0]
	v_cvt_pk_bf16_f32 v20, v20, v21
	v_cvt_pk_bf16_f32 v21, v18, v19
	ds_write_b64 v186, v[20:21] offset:544
	v_pk_fma_f32 v[20:21], v[236:237], v[78:79], 0 op_sel_hi:[0,1,0] neg_lo:[1,0,0] neg_hi:[1,0,0]
	v_pk_fma_f32 v[18:19], v[236:237], v[80:81], 0 op_sel_hi:[0,1,0] neg_lo:[1,0,0] neg_hi:[1,0,0]
	v_cvt_pk_bf16_f32 v20, v20, v21
	v_cvt_pk_bf16_f32 v21, v18, v19
	ds_write_b64 v186, v[20:21] offset:1088
	v_pk_fma_f32 v[20:21], v[238:239], v[58:59], 0 op_sel_hi:[0,1,0] neg_lo:[1,0,0] neg_hi:[1,0,0]
	v_pk_fma_f32 v[18:19], v[238:239], v[60:61], 0 op_sel_hi:[0,1,0] neg_lo:[1,0,0] neg_hi:[1,0,0]
	v_cvt_pk_bf16_f32 v20, v20, v21
	v_cvt_pk_bf16_f32 v21, v18, v19
	ds_write_b64 v186, v[20:21] offset:1632
	v_pk_fma_f32 v[20:21], v[240:241], v[34:35], 0 op_sel_hi:[0,1,0] neg_lo:[1,0,0] neg_hi:[1,0,0]
	v_pk_fma_f32 v[18:19], v[240:241], v[36:37], 0 op_sel_hi:[0,1,0] neg_lo:[1,0,0] neg_hi:[1,0,0]
	v_cvt_pk_bf16_f32 v20, v20, v21
	v_cvt_pk_bf16_f32 v21, v18, v19
	ds_write_b64 v186, v[20:21] offset:2176
	v_pk_fma_f32 v[20:21], v[242:243], v[22:23], 0 op_sel_hi:[0,1,0] neg_lo:[1,0,0] neg_hi:[1,0,0]
	v_pk_fma_f32 v[18:19], v[242:243], v[24:25], 0 op_sel_hi:[0,1,0] neg_lo:[1,0,0] neg_hi:[1,0,0]
	v_cvt_pk_bf16_f32 v20, v20, v21
	v_cvt_pk_bf16_f32 v21, v18, v19
	ds_write_b64 v186, v[20:21] offset:2720
	v_pk_fma_f32 v[14:15], v[244:245], v[14:15], 0 op_sel_hi:[0,1,0] neg_lo:[1,0,0] neg_hi:[1,0,0]
	v_pk_fma_f32 v[16:17], v[244:245], v[16:17], 0 op_sel_hi:[0,1,0] neg_lo:[1,0,0] neg_hi:[1,0,0]
	v_cvt_pk_bf16_f32 v14, v14, v15
	v_cvt_pk_bf16_f32 v15, v16, v17
	ds_write_b64 v186, v[14:15] offset:3264
	v_pk_fma_f32 v[6:7], v[246:247], v[6:7], 0 op_sel_hi:[0,1,0] neg_lo:[1,0,0] neg_hi:[1,0,0]
	v_pk_fma_f32 v[8:9], v[246:247], v[8:9], 0 op_sel_hi:[0,1,0] neg_lo:[1,0,0] neg_hi:[1,0,0]
	v_cvt_pk_bf16_f32 v6, v6, v7
	v_cvt_pk_bf16_f32 v7, v8, v9
	ds_write_b64 v186, v[6:7] offset:3808
	ds_read_b128 a[160:163], v1
	ds_read_b128 a[164:167], v1 offset:64
	ds_read_b128 a[168:171], v1 offset:128
	ds_read_b128 a[172:175], v1 offset:192
	v_lshl_add_u64 v[6:7], v[150:151], 0, s[22:23]
	v_lshl_add_u64 v[18:19], v[160:161], 0, s[22:23]
	v_lshl_add_u64 v[20:21], v[162:163], 0, s[22:23]
	v_lshl_add_u64 v[22:23], v[164:165], 0, s[22:23]
	v_lshl_add_u64 v[8:9], v[152:153], 0, s[22:23]
	v_lshl_add_u64 v[14:15], v[156:157], 0, s[22:23]
	v_lshl_add_u64 v[16:17], v[158:159], 0, s[22:23]
	v_lshl_add_u64 v[34:35], v[166:167], 0, s[22:23]
	global_load_dwordx4 v[110:113], v[6:7], off nt
	global_load_dwordx4 v[98:101], v[8:9], off nt
	global_load_dwordx4 v[78:81], v[14:15], off nt
	global_load_dwordx4 v[66:69], v[16:17], off nt
	global_load_dwordx4 v[58:61], v[18:19], off nt
	global_load_dwordx4 v[30:33], v[20:21], off nt
	s_nop 0
	global_load_dwordx4 v[22:25], v[22:23], off nt
	s_nop 0
	global_load_dwordx4 v[18:21], v[34:35], off nt
	s_waitcnt vmcnt(23)
	s_waitcnt vmcnt(22)
	s_waitcnt vmcnt(21)
	s_waitcnt vmcnt(20)
	s_waitcnt vmcnt(19)
	s_waitcnt vmcnt(18)
	s_waitcnt vmcnt(17)
	s_waitcnt vmcnt(16)
	ds_read_b32 v232, v187 offset:128
	ds_read_b32 v234, v187 offset:136
	ds_read_b32 v236, v187 offset:144
	ds_read_b32 v238, v187 offset:152
	ds_read_b32 v240, v187 offset:160
	ds_read_b32 v242, v187 offset:168
	ds_read_b32 v244, v187 offset:176
	ds_read_b32 v246, v187 offset:184
	s_waitcnt lgkmcnt(0)
	v_pk_fma_f32 v[8:9], v[232:233], v[114:115], 0 op_sel_hi:[0,1,0] neg_lo:[1,0,0] neg_hi:[1,0,0]
	v_pk_fma_f32 v[6:7], v[232:233], v[116:117], 0 op_sel_hi:[0,1,0] neg_lo:[1,0,0] neg_hi:[1,0,0]
	v_cvt_pk_bf16_f32 v8, v8, v9
	v_cvt_pk_bf16_f32 v9, v6, v7
	ds_write_b64 v186, v[8:9]
	v_pk_fma_f32 v[8:9], v[234:235], v[94:95], 0 op_sel_hi:[0,1,0] neg_lo:[1,0,0] neg_hi:[1,0,0]
	v_pk_fma_f32 v[6:7], v[234:235], v[96:97], 0 op_sel_hi:[0,1,0] neg_lo:[1,0,0] neg_hi:[1,0,0]
	v_cvt_pk_bf16_f32 v8, v8, v9
	v_cvt_pk_bf16_f32 v9, v6, v7
	ds_write_b64 v186, v[8:9] offset:544
	v_pk_fma_f32 v[8:9], v[236:237], v[82:83], 0 op_sel_hi:[0,1,0] neg_lo:[1,0,0] neg_hi:[1,0,0]
	v_pk_fma_f32 v[6:7], v[236:237], v[84:85], 0 op_sel_hi:[0,1,0] neg_lo:[1,0,0] neg_hi:[1,0,0]
	v_cvt_pk_bf16_f32 v8, v8, v9
	v_cvt_pk_bf16_f32 v9, v6, v7
	ds_write_b64 v186, v[8:9] offset:1088
	v_pk_fma_f32 v[8:9], v[238:239], v[62:63], 0 op_sel_hi:[0,1,0] neg_lo:[1,0,0] neg_hi:[1,0,0]
	v_pk_fma_f32 v[6:7], v[238:239], v[64:65], 0 op_sel_hi:[0,1,0] neg_lo:[1,0,0] neg_hi:[1,0,0]
	v_cvt_pk_bf16_f32 v8, v8, v9
	v_cvt_pk_bf16_f32 v9, v6, v7
	ds_write_b64 v186, v[8:9] offset:1632
	v_pk_fma_f32 v[8:9], v[240:241], v[38:39], 0 op_sel_hi:[0,1,0] neg_lo:[1,0,0] neg_hi:[1,0,0]
	v_pk_fma_f32 v[6:7], v[240:241], v[40:41], 0 op_sel_hi:[0,1,0] neg_lo:[1,0,0] neg_hi:[1,0,0]
	v_cvt_pk_bf16_f32 v8, v8, v9
	v_cvt_pk_bf16_f32 v9, v6, v7
	ds_write_b64 v186, v[8:9] offset:2176
	v_pk_fma_f32 v[8:9], v[242:243], v[26:27], 0 op_sel_hi:[0,1,0] neg_lo:[1,0,0] neg_hi:[1,0,0]
	v_pk_fma_f32 v[6:7], v[242:243], v[28:29], 0 op_sel_hi:[0,1,0] neg_lo:[1,0,0] neg_hi:[1,0,0]
	v_cvt_pk_bf16_f32 v8, v8, v9
	v_cvt_pk_bf16_f32 v9, v6, v7
	ds_write_b64 v186, v[8:9] offset:2720
	v_pk_fma_f32 v[8:9], v[244:245], v[10:11], 0 op_sel_hi:[0,1,0] neg_lo:[1,0,0] neg_hi:[1,0,0]
	v_pk_fma_f32 v[6:7], v[244:245], v[12:13], 0 op_sel_hi:[0,1,0] neg_lo:[1,0,0] neg_hi:[1,0,0]
	v_cvt_pk_bf16_f32 v8, v8, v9
	v_cvt_pk_bf16_f32 v9, v6, v7
	ds_write_b64 v186, v[8:9] offset:3264
	v_pk_fma_f32 v[2:3], v[246:247], v[2:3], 0 op_sel_hi:[0,1,0] neg_lo:[1,0,0] neg_hi:[1,0,0]
	v_pk_fma_f32 v[4:5], v[246:247], v[4:5], 0 op_sel_hi:[0,1,0] neg_lo:[1,0,0] neg_hi:[1,0,0]
	v_cvt_pk_bf16_f32 v2, v2, v3
	v_cvt_pk_bf16_f32 v3, v4, v5
	ds_write_b64 v186, v[2:3] offset:3808
	ds_read_b128 a[176:179], v1
	ds_read_b128 a[180:183], v1 offset:64
	ds_read_b128 a[184:187], v1 offset:128
	ds_read_b128 a[188:191], v1 offset:192
	v_lshl_add_u64 v[2:3], v[168:169], 0, s[22:23]
	v_lshl_add_u64 v[4:5], v[170:171], 0, s[22:23]
	v_lshl_add_u64 v[6:7], v[172:173], 0, s[22:23]
	v_lshl_add_u64 v[8:9], v[174:175], 0, s[22:23]
	v_lshl_add_u64 v[10:11], v[176:177], 0, s[22:23]
	v_lshl_add_u64 v[12:13], v[178:179], 0, s[22:23]
	v_lshl_add_u64 v[14:15], v[180:181], 0, s[22:23]
	v_lshl_add_u64 v[16:17], v[182:183], 0, s[22:23]
	global_load_dwordx4 v[114:117], v[2:3], off nt
	global_load_dwordx4 v[102:105], v[4:5], off nt
	global_load_dwordx4 v[94:97], v[6:7], off nt
	global_load_dwordx4 v[82:85], v[8:9], off nt
	global_load_dwordx4 v[62:65], v[10:11], off nt
	global_load_dwordx4 v[42:45], v[12:13], off nt
	global_load_dwordx4 v[38:41], v[14:15], off nt
	global_load_dwordx4 v[34:37], v[16:17], off nt
	v_mov_b32_e32 v2, v194
	s_waitcnt vmcnt(23)
	s_waitcnt vmcnt(22)
	s_waitcnt vmcnt(21)
	s_waitcnt vmcnt(20)
	s_waitcnt vmcnt(19)
	s_waitcnt vmcnt(18)
	s_waitcnt vmcnt(17)
	s_waitcnt vmcnt(16)
	ds_read_b32 v232, v187 offset:0
	ds_read_b32 v234, v187 offset:8
	ds_read_b32 v236, v187 offset:16
	ds_read_b32 v238, v187 offset:24
	ds_read_b32 v240, v187 offset:32
	ds_read_b32 v242, v187 offset:40
	ds_read_b32 v244, v187 offset:48
	ds_read_b32 v246, v187 offset:56
	s_waitcnt lgkmcnt(0)
	v_pk_fma_f32 v[4:5], v[232:233], v[106:107], 0 op_sel_hi:[0,1,0] neg_lo:[1,0,0] neg_hi:[1,0,0]
	v_pk_fma_f32 v[2:3], v[232:233], v[108:109], 0 op_sel_hi:[0,1,0] neg_lo:[1,0,0] neg_hi:[1,0,0]
	v_cvt_pk_bf16_f32 v4, v4, v5
	v_cvt_pk_bf16_f32 v5, v2, v3
	ds_write_b64 v186, v[4:5]
	v_pk_fma_f32 v[4:5], v[234:235], v[90:91], 0 op_sel_hi:[0,1,0] neg_lo:[1,0,0] neg_hi:[1,0,0]
	v_pk_fma_f32 v[2:3], v[234:235], v[92:93], 0 op_sel_hi:[0,1,0] neg_lo:[1,0,0] neg_hi:[1,0,0]
	v_cvt_pk_bf16_f32 v4, v4, v5
	v_cvt_pk_bf16_f32 v5, v2, v3
	ds_write_b64 v186, v[4:5] offset:544
	v_pk_fma_f32 v[4:5], v[236:237], v[86:87], 0 op_sel_hi:[0,1,0] neg_lo:[1,0,0] neg_hi:[1,0,0]
	v_pk_fma_f32 v[2:3], v[236:237], v[88:89], 0 op_sel_hi:[0,1,0] neg_lo:[1,0,0] neg_hi:[1,0,0]
	v_cvt_pk_bf16_f32 v4, v4, v5
	v_cvt_pk_bf16_f32 v5, v2, v3
	ds_write_b64 v186, v[4:5] offset:1088
	v_pk_fma_f32 v[4:5], v[238:239], v[74:75], 0 op_sel_hi:[0,1,0] neg_lo:[1,0,0] neg_hi:[1,0,0]
	v_pk_fma_f32 v[2:3], v[238:239], v[76:77], 0 op_sel_hi:[0,1,0] neg_lo:[1,0,0] neg_hi:[1,0,0]
	v_cvt_pk_bf16_f32 v4, v4, v5
	v_cvt_pk_bf16_f32 v5, v2, v3
	ds_write_b64 v186, v[4:5] offset:1632
	v_pk_fma_f32 v[4:5], v[240:241], v[70:71], 0 op_sel_hi:[0,1,0] neg_lo:[1,0,0] neg_hi:[1,0,0]
	v_pk_fma_f32 v[2:3], v[240:241], v[72:73], 0 op_sel_hi:[0,1,0] neg_lo:[1,0,0] neg_hi:[1,0,0]
	v_cvt_pk_bf16_f32 v4, v4, v5
	v_cvt_pk_bf16_f32 v5, v2, v3
	ds_write_b64 v186, v[4:5] offset:2176
	v_pk_fma_f32 v[4:5], v[242:243], v[54:55], 0 op_sel_hi:[0,1,0] neg_lo:[1,0,0] neg_hi:[1,0,0]
	v_pk_fma_f32 v[2:3], v[242:243], v[56:57], 0 op_sel_hi:[0,1,0] neg_lo:[1,0,0] neg_hi:[1,0,0]
	v_cvt_pk_bf16_f32 v4, v4, v5
	v_cvt_pk_bf16_f32 v5, v2, v3
	ds_write_b64 v186, v[4:5] offset:2720
	v_pk_fma_f32 v[4:5], v[244:245], v[50:51], 0 op_sel_hi:[0,1,0] neg_lo:[1,0,0] neg_hi:[1,0,0]
	v_pk_fma_f32 v[2:3], v[244:245], v[52:53], 0 op_sel_hi:[0,1,0] neg_lo:[1,0,0] neg_hi:[1,0,0]
	v_cvt_pk_bf16_f32 v4, v4, v5
	v_cvt_pk_bf16_f32 v5, v2, v3
	ds_write_b64 v186, v[4:5] offset:3264
	v_pk_fma_f32 v[4:5], v[246:247], v[46:47], 0 op_sel_hi:[0,1,0] neg_lo:[1,0,0] neg_hi:[1,0,0]
	v_pk_fma_f32 v[2:3], v[246:247], v[48:49], 0 op_sel_hi:[0,1,0] neg_lo:[1,0,0] neg_hi:[1,0,0]
	v_cvt_pk_bf16_f32 v4, v4, v5
	v_cvt_pk_bf16_f32 v5, v2, v3
	ds_write_b64 v186, v[4:5] offset:3808
	ds_read_b128 a[192:195], v1
	ds_read_b128 a[196:199], v1 offset:64
	ds_read_b128 a[200:203], v1 offset:128
	ds_read_b128 a[204:207], v1 offset:192
	v_lshl_add_u64 v[118:119], v[130:131], 0, s[20:21]
	v_add_co_u32_e32 v126, vcc, s7, v118
	s_nop 1
	v_addc_co_u32_e32 v127, vcc, 0, v119, vcc
	v_add_co_u32_e32 v128, vcc, s36, v118
	global_load_dwordx4 v[90:93], v[118:119], off nt
	global_load_dwordx4 v[86:89], v[126:127], off nt
	v_addc_co_u32_e32 v129, vcc, 0, v119, vcc
	v_add_co_u32_e32 v134, vcc, s37, v118
	s_nop 1
	v_addc_co_u32_e32 v135, vcc, 0, v119, vcc
	v_add_co_u32_e32 v136, vcc, s38, v118
	global_load_dwordx4 v[54:57], v[128:129], off nt
	global_load_dwordx4 v[50:53], v[134:135], off nt
	v_addc_co_u32_e32 v137, vcc, 0, v119, vcc
	v_add_co_u32_e32 v138, vcc, s39, v118
	s_nop 1
	v_addc_co_u32_e32 v139, vcc, 0, v119, vcc
	v_add_co_u32_e32 v140, vcc, s41, v118
	global_load_dwordx4 v[14:17], v[136:137], off nt
	global_load_dwordx4 v[10:13], v[138:139], off nt
	v_addc_co_u32_e32 v141, vcc, 0, v119, vcc
	v_add_co_u32_e32 v142, vcc, s42, v118
	s_nop 1
	v_addc_co_u32_e32 v143, vcc, 0, v119, vcc
	global_load_dwordx4 v[6:9], v[140:141], off nt
	global_load_dwordx4 v[2:5], v[142:143], off nt
	v_mov_b32_e32 v26, v194
	s_waitcnt vmcnt(23)
	s_waitcnt vmcnt(22)
	s_waitcnt vmcnt(21)
	s_waitcnt vmcnt(20)
	s_waitcnt vmcnt(19)
	s_waitcnt vmcnt(18)
	s_waitcnt vmcnt(17)
	s_waitcnt vmcnt(16)
	ds_read_b32 v232, v187 offset:64
	ds_read_b32 v234, v187 offset:72
	ds_read_b32 v236, v187 offset:80
	ds_read_b32 v238, v187 offset:88
	ds_read_b32 v240, v187 offset:96
	ds_read_b32 v242, v187 offset:104
	ds_read_b32 v244, v187 offset:112
	ds_read_b32 v246, v187 offset:120
	s_waitcnt lgkmcnt(0)
	v_pk_fma_f32 v[28:29], v[232:233], v[110:111], 0 op_sel_hi:[0,1,0] neg_lo:[1,0,0] neg_hi:[1,0,0]
	v_pk_fma_f32 v[26:27], v[232:233], v[112:113], 0 op_sel_hi:[0,1,0] neg_lo:[1,0,0] neg_hi:[1,0,0]
	v_cvt_pk_bf16_f32 v28, v28, v29
	v_cvt_pk_bf16_f32 v29, v26, v27
	ds_write_b64 v186, v[28:29]
	v_pk_fma_f32 v[28:29], v[234:235], v[98:99], 0 op_sel_hi:[0,1,0] neg_lo:[1,0,0] neg_hi:[1,0,0]
	v_pk_fma_f32 v[26:27], v[234:235], v[100:101], 0 op_sel_hi:[0,1,0] neg_lo:[1,0,0] neg_hi:[1,0,0]
	v_cvt_pk_bf16_f32 v28, v28, v29
	v_cvt_pk_bf16_f32 v29, v26, v27
	ds_write_b64 v186, v[28:29] offset:544
	v_pk_fma_f32 v[28:29], v[236:237], v[78:79], 0 op_sel_hi:[0,1,0] neg_lo:[1,0,0] neg_hi:[1,0,0]
	v_pk_fma_f32 v[26:27], v[236:237], v[80:81], 0 op_sel_hi:[0,1,0] neg_lo:[1,0,0] neg_hi:[1,0,0]
	v_cvt_pk_bf16_f32 v28, v28, v29
	v_cvt_pk_bf16_f32 v29, v26, v27
	ds_write_b64 v186, v[28:29] offset:1088
	v_pk_fma_f32 v[28:29], v[238:239], v[66:67], 0 op_sel_hi:[0,1,0] neg_lo:[1,0,0] neg_hi:[1,0,0]
	v_pk_fma_f32 v[26:27], v[238:239], v[68:69], 0 op_sel_hi:[0,1,0] neg_lo:[1,0,0] neg_hi:[1,0,0]
	v_cvt_pk_bf16_f32 v28, v28, v29
	v_cvt_pk_bf16_f32 v29, v26, v27
	ds_write_b64 v186, v[28:29] offset:1632
	v_pk_fma_f32 v[28:29], v[240:241], v[58:59], 0 op_sel_hi:[0,1,0] neg_lo:[1,0,0] neg_hi:[1,0,0]
	v_pk_fma_f32 v[26:27], v[240:241], v[60:61], 0 op_sel_hi:[0,1,0] neg_lo:[1,0,0] neg_hi:[1,0,0]
	v_cvt_pk_bf16_f32 v28, v28, v29
	v_cvt_pk_bf16_f32 v29, v26, v27
	ds_write_b64 v186, v[28:29] offset:2176
	v_pk_fma_f32 v[28:29], v[242:243], v[30:31], 0 op_sel_hi:[0,1,0] neg_lo:[1,0,0] neg_hi:[1,0,0]
	v_pk_fma_f32 v[26:27], v[242:243], v[32:33], 0 op_sel_hi:[0,1,0] neg_lo:[1,0,0] neg_hi:[1,0,0]
	v_cvt_pk_bf16_f32 v28, v28, v29
	v_cvt_pk_bf16_f32 v29, v26, v27
	ds_write_b64 v186, v[28:29] offset:2720
	v_pk_fma_f32 v[22:23], v[244:245], v[22:23], 0 op_sel_hi:[0,1,0] neg_lo:[1,0,0] neg_hi:[1,0,0]
	v_pk_fma_f32 v[24:25], v[244:245], v[24:25], 0 op_sel_hi:[0,1,0] neg_lo:[1,0,0] neg_hi:[1,0,0]
	v_cvt_pk_bf16_f32 v22, v22, v23
	v_cvt_pk_bf16_f32 v23, v24, v25
	ds_write_b64 v186, v[22:23] offset:3264
	v_pk_fma_f32 v[18:19], v[246:247], v[18:19], 0 op_sel_hi:[0,1,0] neg_lo:[1,0,0] neg_hi:[1,0,0]
	v_pk_fma_f32 v[20:21], v[246:247], v[20:21], 0 op_sel_hi:[0,1,0] neg_lo:[1,0,0] neg_hi:[1,0,0]
	v_cvt_pk_bf16_f32 v18, v18, v19
	v_cvt_pk_bf16_f32 v19, v20, v21
	ds_write_b64 v186, v[18:19] offset:3808
	ds_read_b128 a[208:211], v1
	ds_read_b128 a[212:215], v1 offset:64
	ds_read_b128 a[216:219], v1 offset:128
	ds_read_b128 a[220:223], v1 offset:192
	v_lshl_add_u64 v[18:19], v[150:151], 0, s[20:21]
	v_lshl_add_u64 v[20:21], v[152:153], 0, s[20:21]
	v_lshl_add_u64 v[22:23], v[156:157], 0, s[20:21]
	v_lshl_add_u64 v[24:25], v[158:159], 0, s[20:21]
	v_lshl_add_u64 v[26:27], v[160:161], 0, s[20:21]
	v_lshl_add_u64 v[28:29], v[162:163], 0, s[20:21]
	v_lshl_add_u64 v[46:47], v[164:165], 0, s[20:21]
	v_lshl_add_u64 v[48:49], v[166:167], 0, s[20:21]
	global_load_dwordx4 v[78:81], v[18:19], off nt
	global_load_dwordx4 v[74:77], v[20:21], off nt
	global_load_dwordx4 v[70:73], v[22:23], off nt
	global_load_dwordx4 v[66:69], v[24:25], off nt
	global_load_dwordx4 v[30:33], v[26:27], off nt
	s_nop 0
	global_load_dwordx4 v[26:29], v[28:29], off nt
	s_nop 0
	global_load_dwordx4 v[22:25], v[46:47], off nt
	global_load_dwordx4 v[18:21], v[48:49], off nt
	s_waitcnt vmcnt(23)
	s_waitcnt vmcnt(22)
	s_waitcnt vmcnt(21)
	s_waitcnt vmcnt(20)
	s_waitcnt vmcnt(19)
	s_waitcnt vmcnt(18)
	s_waitcnt vmcnt(17)
	s_waitcnt vmcnt(16)
	ds_read_b32 v232, v187 offset:128
	ds_read_b32 v234, v187 offset:136
	ds_read_b32 v236, v187 offset:144
	ds_read_b32 v238, v187 offset:152
	ds_read_b32 v240, v187 offset:160
	ds_read_b32 v242, v187 offset:168
	ds_read_b32 v244, v187 offset:176
	ds_read_b32 v246, v187 offset:184
	s_waitcnt lgkmcnt(0)
	v_pk_fma_f32 v[48:49], v[232:233], v[114:115], 0 op_sel_hi:[0,1,0] neg_lo:[1,0,0] neg_hi:[1,0,0]
	v_pk_fma_f32 v[46:47], v[232:233], v[116:117], 0 op_sel_hi:[0,1,0] neg_lo:[1,0,0] neg_hi:[1,0,0]
	v_cvt_pk_bf16_f32 v48, v48, v49
	v_cvt_pk_bf16_f32 v49, v46, v47
	ds_write_b64 v186, v[48:49]
	v_pk_fma_f32 v[48:49], v[234:235], v[102:103], 0 op_sel_hi:[0,1,0] neg_lo:[1,0,0] neg_hi:[1,0,0]
	v_pk_fma_f32 v[46:47], v[234:235], v[104:105], 0 op_sel_hi:[0,1,0] neg_lo:[1,0,0] neg_hi:[1,0,0]
	v_cvt_pk_bf16_f32 v48, v48, v49
	v_cvt_pk_bf16_f32 v49, v46, v47
	ds_write_b64 v186, v[48:49] offset:544
	v_pk_fma_f32 v[48:49], v[236:237], v[94:95], 0 op_sel_hi:[0,1,0] neg_lo:[1,0,0] neg_hi:[1,0,0]
	v_pk_fma_f32 v[46:47], v[236:237], v[96:97], 0 op_sel_hi:[0,1,0] neg_lo:[1,0,0] neg_hi:[1,0,0]
	v_cvt_pk_bf16_f32 v48, v48, v49
	v_cvt_pk_bf16_f32 v49, v46, v47
	ds_write_b64 v186, v[48:49] offset:1088
	v_pk_fma_f32 v[48:49], v[238:239], v[82:83], 0 op_sel_hi:[0,1,0] neg_lo:[1,0,0] neg_hi:[1,0,0]
	v_pk_fma_f32 v[46:47], v[238:239], v[84:85], 0 op_sel_hi:[0,1,0] neg_lo:[1,0,0] neg_hi:[1,0,0]
	v_cvt_pk_bf16_f32 v48, v48, v49
	v_cvt_pk_bf16_f32 v49, v46, v47
	ds_write_b64 v186, v[48:49] offset:1632
	v_pk_fma_f32 v[48:49], v[240:241], v[62:63], 0 op_sel_hi:[0,1,0] neg_lo:[1,0,0] neg_hi:[1,0,0]
	v_pk_fma_f32 v[46:47], v[240:241], v[64:65], 0 op_sel_hi:[0,1,0] neg_lo:[1,0,0] neg_hi:[1,0,0]
	v_cvt_pk_bf16_f32 v48, v48, v49
	v_cvt_pk_bf16_f32 v49, v46, v47
	ds_write_b64 v186, v[48:49] offset:2176
	v_pk_fma_f32 v[42:43], v[242:243], v[42:43], 0 op_sel_hi:[0,1,0] neg_lo:[1,0,0] neg_hi:[1,0,0]
	v_pk_fma_f32 v[44:45], v[242:243], v[44:45], 0 op_sel_hi:[0,1,0] neg_lo:[1,0,0] neg_hi:[1,0,0]
	v_cvt_pk_bf16_f32 v42, v42, v43
	v_cvt_pk_bf16_f32 v43, v44, v45
	ds_write_b64 v186, v[42:43] offset:2720
	v_pk_fma_f32 v[38:39], v[244:245], v[38:39], 0 op_sel_hi:[0,1,0] neg_lo:[1,0,0] neg_hi:[1,0,0]
	v_pk_fma_f32 v[40:41], v[244:245], v[40:41], 0 op_sel_hi:[0,1,0] neg_lo:[1,0,0] neg_hi:[1,0,0]
	v_cvt_pk_bf16_f32 v38, v38, v39
	v_cvt_pk_bf16_f32 v39, v40, v41
	ds_write_b64 v186, v[38:39] offset:3264
	v_pk_fma_f32 v[34:35], v[246:247], v[34:35], 0 op_sel_hi:[0,1,0] neg_lo:[1,0,0] neg_hi:[1,0,0]
	v_pk_fma_f32 v[36:37], v[246:247], v[36:37], 0 op_sel_hi:[0,1,0] neg_lo:[1,0,0] neg_hi:[1,0,0]
	v_cvt_pk_bf16_f32 v34, v34, v35
	v_cvt_pk_bf16_f32 v35, v36, v37
	ds_write_b64 v186, v[34:35] offset:3808
	ds_read_b128 a[224:227], v1
	ds_read_b128 a[228:231], v1 offset:64
	ds_read_b128 a[232:235], v1 offset:128
	ds_read_b128 a[236:239], v1 offset:192
	v_lshl_add_u64 v[34:35], v[168:169], 0, s[20:21]
	v_lshl_add_u64 v[36:37], v[170:171], 0, s[20:21]
	v_lshl_add_u64 v[38:39], v[172:173], 0, s[20:21]
	v_lshl_add_u64 v[40:41], v[174:175], 0, s[20:21]
	v_lshl_add_u64 v[42:43], v[176:177], 0, s[20:21]
	v_lshl_add_u64 v[44:45], v[178:179], 0, s[20:21]
	v_lshl_add_u64 v[58:59], v[180:181], 0, s[20:21]
	v_lshl_add_u64 v[60:61], v[182:183], 0, s[20:21]
	global_load_dwordx4 v[122:125], v[34:35], off nt
	global_load_dwordx4 v[106:109], v[36:37], off nt
	global_load_dwordx4 v[94:97], v[38:39], off nt
	global_load_dwordx4 v[82:85], v[40:41], off nt
	global_load_dwordx4 v[46:49], v[42:43], off nt
	s_nop 0
	global_load_dwordx4 v[42:45], v[44:45], off nt
	s_nop 0
	global_load_dwordx4 v[38:41], v[58:59], off nt
	global_load_dwordx4 v[34:37], v[60:61], off nt
	v_mov_b32_e32 v98, v133
	s_waitcnt vmcnt(23)
	s_waitcnt vmcnt(22)
	s_waitcnt vmcnt(21)
	s_waitcnt vmcnt(20)
	s_waitcnt vmcnt(19)
	s_waitcnt vmcnt(18)
	s_waitcnt vmcnt(17)
	s_waitcnt vmcnt(16)
	ds_read_b32 v232, v187 offset:0
	ds_read_b32 v234, v187 offset:8
	ds_read_b32 v236, v187 offset:16
	ds_read_b32 v238, v187 offset:24
	ds_read_b32 v240, v187 offset:32
	ds_read_b32 v242, v187 offset:40
	ds_read_b32 v244, v187 offset:48
	ds_read_b32 v246, v187 offset:56
	v_add_u32_e32 v99, 1, v98
	v_cmp_eq_u32_e32 vcc, v98, v132
	s_nop 1
	v_cndmask_b32_e64 v60, 0, 1.0, vcc
	v_cmp_eq_u32_e32 vcc, v99, v132
	s_nop 1
	v_cndmask_b32_e64 v61, 0, 1.0, vcc
	s_waitcnt lgkmcnt(0)
	v_pk_fma_f32 v[62:63], v[232:233], v[90:91], v[60:61] op_sel_hi:[0,1,1] neg_lo:[1,0,0] neg_hi:[1,0,0]
	v_add_u32_e32 v90, 3, v98
	v_add_u32_e32 v91, 2, v98
	v_cmp_eq_u32_e32 vcc, v90, v132
	v_cvt_pk_bf16_f32 v62, v62, v63
	s_nop 0
	v_cndmask_b32_e64 v65, 0, 1.0, vcc
	v_cmp_eq_u32_e32 vcc, v91, v132
	s_nop 1
	v_cndmask_b32_e64 v64, 0, 1.0, vcc
	v_pk_fma_f32 v[58:59], v[232:233], v[92:93], v[64:65] op_sel_hi:[0,1,1] neg_lo:[1,0,0] neg_hi:[1,0,0]
	v_cvt_pk_bf16_f32 v63, v58, v59
	ds_write_b64 v186, v[62:63]
	v_cmp_eq_u32_e32 vcc, v98, v193
	s_nop 1
	v_cndmask_b32_e64 v62, 0, 1.0, vcc
	v_cmp_eq_u32_e32 vcc, v99, v193
	s_nop 1
	v_cndmask_b32_e64 v63, 0, 1.0, vcc
	v_cmp_eq_u32_e32 vcc, v90, v193
	v_pk_fma_f32 v[62:63], v[234:235], v[86:87], v[62:63] op_sel_hi:[0,1,1] neg_lo:[1,0,0] neg_hi:[1,0,0]
	v_cvt_pk_bf16_f32 v62, v62, v63
	v_cndmask_b32_e64 v61, 0, 1.0, vcc
	v_pk_fma_f32 v[58:59], v[234:235], v[88:89], v[60:61] op_sel_hi:[0,1,1] neg_lo:[1,0,0] neg_hi:[1,0,0]
	v_cvt_pk_bf16_f32 v63, v58, v59
	ds_write_b64 v186, v[62:63] offset:544
	v_cmp_eq_u32_e32 vcc, v98, v192
	s_nop 1
	v_cndmask_b32_e64 v60, 0, 1.0, vcc
	v_cmp_eq_u32_e32 vcc, v99, v192
	s_nop 1
	v_cndmask_b32_e64 v61, 0, 1.0, vcc
	v_cmp_eq_u32_e32 vcc, v90, v192
	v_pk_fma_f32 v[54:55], v[236:237], v[54:55], v[60:61] op_sel_hi:[0,1,1] neg_lo:[1,0,0] neg_hi:[1,0,0]
	v_cvt_pk_bf16_f32 v54, v54, v55
	v_cndmask_b32_e64 v61, 0, 1.0, vcc
	v_cmp_eq_u32_e32 vcc, v91, v192
	s_nop 1
	v_cndmask_b32_e64 v60, 0, 1.0, vcc
	v_pk_fma_f32 v[56:57], v[236:237], v[56:57], v[60:61] op_sel_hi:[0,1,1] neg_lo:[1,0,0] neg_hi:[1,0,0]
	v_cvt_pk_bf16_f32 v55, v56, v57
	ds_write_b64 v186, v[54:55] offset:1088
	v_cmp_eq_u32_e32 vcc, v98, v190
	s_nop 1
	v_cndmask_b32_e64 v56, 0, 1.0, vcc
	v_cmp_eq_u32_e32 vcc, v99, v190
	s_nop 1
	v_cndmask_b32_e64 v57, 0, 1.0, vcc
	v_cmp_eq_u32_e32 vcc, v90, v190
	v_pk_fma_f32 v[50:51], v[238:239], v[50:51], v[56:57] op_sel_hi:[0,1,1] neg_lo:[1,0,0] neg_hi:[1,0,0]
	v_cvt_pk_bf16_f32 v50, v50, v51
	v_cndmask_b32_e64 v57, 0, 1.0, vcc
	v_cmp_eq_u32_e32 vcc, v91, v190
	s_nop 1
	v_cndmask_b32_e64 v56, 0, 1.0, vcc
	v_pk_fma_f32 v[52:53], v[238:239], v[52:53], v[56:57] op_sel_hi:[0,1,1] neg_lo:[1,0,0] neg_hi:[1,0,0]
	v_cvt_pk_bf16_f32 v51, v52, v53
	ds_write_b64 v186, v[50:51] offset:1632
	v_cmp_eq_u32_e32 vcc, v98, v149
	s_nop 1
	v_cndmask_b32_e64 v52, 0, 1.0, vcc
	v_cmp_eq_u32_e32 vcc, v99, v149
	s_nop 1
	v_cndmask_b32_e64 v53, 0, 1.0, vcc
	v_cmp_eq_u32_e32 vcc, v90, v149
	v_pk_fma_f32 v[14:15], v[240:241], v[14:15], v[52:53] op_sel_hi:[0,1,1] neg_lo:[1,0,0] neg_hi:[1,0,0]
	v_cvt_pk_bf16_f32 v14, v14, v15
	v_cndmask_b32_e64 v53, 0, 1.0, vcc
	v_cmp_eq_u32_e32 vcc, v91, v149
	s_nop 1
	v_cndmask_b32_e64 v52, 0, 1.0, vcc
	v_pk_fma_f32 v[16:17], v[240:241], v[16:17], v[52:53] op_sel_hi:[0,1,1] neg_lo:[1,0,0] neg_hi:[1,0,0]
	v_cvt_pk_bf16_f32 v15, v16, v17
	ds_write_b64 v186, v[14:15] offset:2176
	v_cmp_eq_u32_e32 vcc, v98, v148
	s_nop 1
	v_cndmask_b32_e64 v16, 0, 1.0, vcc
	v_cmp_eq_u32_e32 vcc, v99, v148
	s_nop 1
	v_cndmask_b32_e64 v17, 0, 1.0, vcc
	v_cmp_eq_u32_e32 vcc, v90, v148
	v_pk_fma_f32 v[10:11], v[242:243], v[10:11], v[16:17] op_sel_hi:[0,1,1] neg_lo:[1,0,0] neg_hi:[1,0,0]
	v_cvt_pk_bf16_f32 v10, v10, v11
	v_cndmask_b32_e64 v17, 0, 1.0, vcc
	v_cmp_eq_u32_e32 vcc, v91, v148
	s_nop 1
	v_cndmask_b32_e64 v16, 0, 1.0, vcc
	v_pk_fma_f32 v[12:13], v[242:243], v[12:13], v[16:17] op_sel_hi:[0,1,1] neg_lo:[1,0,0] neg_hi:[1,0,0]
	v_cvt_pk_bf16_f32 v11, v12, v13
	ds_write_b64 v186, v[10:11] offset:2720
	v_cmp_eq_u32_e32 vcc, v98, v147
	s_nop 1
	v_cndmask_b32_e64 v12, 0, 1.0, vcc
	v_cmp_eq_u32_e32 vcc, v99, v147
	s_nop 1
	v_cndmask_b32_e64 v13, 0, 1.0, vcc
	v_cmp_eq_u32_e32 vcc, v90, v147
	v_pk_fma_f32 v[6:7], v[244:245], v[6:7], v[12:13] op_sel_hi:[0,1,1] neg_lo:[1,0,0] neg_hi:[1,0,0]
	v_cvt_pk_bf16_f32 v6, v6, v7
	v_cndmask_b32_e64 v13, 0, 1.0, vcc
	v_cmp_eq_u32_e32 vcc, v91, v147
	s_nop 1
	v_cndmask_b32_e64 v12, 0, 1.0, vcc
	v_pk_fma_f32 v[8:9], v[244:245], v[8:9], v[12:13] op_sel_hi:[0,1,1] neg_lo:[1,0,0] neg_hi:[1,0,0]
	v_cvt_pk_bf16_f32 v7, v8, v9
	ds_write_b64 v186, v[6:7] offset:3264
	v_cmp_eq_u32_e32 vcc, v98, v146
	s_nop 1
	v_cndmask_b32_e64 v8, 0, 1.0, vcc
	v_cmp_eq_u32_e32 vcc, v99, v146
	s_nop 1
	v_cndmask_b32_e64 v9, 0, 1.0, vcc
	v_cmp_eq_u32_e32 vcc, v90, v146
	v_pk_fma_f32 v[2:3], v[246:247], v[2:3], v[8:9] op_sel_hi:[0,1,1] neg_lo:[1,0,0] neg_hi:[1,0,0]
	v_cvt_pk_bf16_f32 v2, v2, v3
	v_cndmask_b32_e64 v9, 0, 1.0, vcc
	v_cmp_eq_u32_e32 vcc, v91, v146
	s_nop 1
	v_cndmask_b32_e64 v8, 0, 1.0, vcc
	v_pk_fma_f32 v[4:5], v[246:247], v[4:5], v[8:9] op_sel_hi:[0,1,1] neg_lo:[1,0,0] neg_hi:[1,0,0]
	v_cvt_pk_bf16_f32 v3, v4, v5
	ds_write_b64 v186, v[2:3] offset:3808
	ds_read_b128 v[2:5], v1
	ds_read_b128 v[6:9], v1 offset:64
	ds_read_b128 v[10:13], v1 offset:128
	ds_read_b128 v[14:17], v1 offset:192
	global_load_dwordx4 v[118:121], v[118:119], off offset:512 nt
	s_nop 0
	global_load_dwordx4 v[110:113], v[126:127], off offset:512 nt
	global_load_dwordx4 v[98:101], v[128:129], off offset:512 nt
	global_load_dwordx4 v[86:89], v[134:135], off offset:512 nt
	global_load_dwordx4 v[62:65], v[136:137], off offset:512 nt
	global_load_dwordx4 v[58:61], v[138:139], off offset:512 nt
	global_load_dwordx4 v[54:57], v[140:141], off offset:512 nt
	global_load_dwordx4 v[50:53], v[142:143], off offset:512 nt
	v_mov_b32_e32 v91, v133
	s_waitcnt vmcnt(23)
	s_waitcnt vmcnt(22)
	s_waitcnt vmcnt(21)
	s_waitcnt vmcnt(20)
	s_waitcnt vmcnt(19)
	s_waitcnt vmcnt(18)
	s_waitcnt vmcnt(17)
	s_waitcnt vmcnt(16)
	ds_read_b32 v232, v187 offset:64
	ds_read_b32 v234, v187 offset:72
	ds_read_b32 v236, v187 offset:80
	ds_read_b32 v238, v187 offset:88
	ds_read_b32 v240, v187 offset:96
	ds_read_b32 v242, v187 offset:104
	ds_read_b32 v244, v187 offset:112
	ds_read_b32 v246, v187 offset:120
	v_or_b32_e32 v138, 16, v132
	v_add_u32_e32 v102, 1, v91
	v_cmp_eq_u32_e32 vcc, v91, v138
	v_add_u32_e32 v103, 3, v91
	v_add_u32_e32 v104, 2, v91
	v_cndmask_b32_e64 v92, 0, 1.0, vcc
	v_cmp_eq_u32_e32 vcc, v102, v138
	v_or_b32_e32 v139, 18, v132
	v_or_b32_e32 v140, 20, v132
	v_cndmask_b32_e64 v93, 0, 1.0, vcc
	v_cmp_eq_u32_e32 vcc, v103, v138
	s_waitcnt lgkmcnt(0)
	v_pk_fma_f32 v[78:79], v[232:233], v[78:79], v[92:93] op_sel_hi:[0,1,1] neg_lo:[1,0,0] neg_hi:[1,0,0]
	v_cvt_pk_bf16_f32 v78, v78, v79
	v_cndmask_b32_e64 v93, 0, 1.0, vcc
	v_cmp_eq_u32_e32 vcc, v104, v138
	v_or_b32_e32 v141, 22, v132
	v_or_b32_e32 v142, 24, v132
	v_cndmask_b32_e64 v92, 0, 1.0, vcc
	v_pk_fma_f32 v[80:81], v[232:233], v[80:81], v[92:93] op_sel_hi:[0,1,1] neg_lo:[1,0,0] neg_hi:[1,0,0]
	v_cvt_pk_bf16_f32 v79, v80, v81
	ds_write_b64 v186, v[78:79]
	v_cmp_eq_u32_e32 vcc, v91, v139
	v_or_b32_e32 v143, 26, v132
	v_or_b32_e32 v144, 28, v132
	v_cndmask_b32_e64 v80, 0, 1.0, vcc
	v_cmp_eq_u32_e32 vcc, v102, v139
	v_or_b32_e32 v145, 30, v132
	s_nop 0
	v_cndmask_b32_e64 v81, 0, 1.0, vcc
	v_cmp_eq_u32_e32 vcc, v103, v139
	v_pk_fma_f32 v[74:75], v[234:235], v[74:75], v[80:81] op_sel_hi:[0,1,1] neg_lo:[1,0,0] neg_hi:[1,0,0]
	v_cvt_pk_bf16_f32 v74, v74, v75
	v_cndmask_b32_e64 v81, 0, 1.0, vcc
	v_cmp_eq_u32_e32 vcc, v104, v139
	s_nop 1
	v_cndmask_b32_e64 v80, 0, 1.0, vcc
	v_pk_fma_f32 v[76:77], v[234:235], v[76:77], v[80:81] op_sel_hi:[0,1,1] neg_lo:[1,0,0] neg_hi:[1,0,0]
	v_cvt_pk_bf16_f32 v75, v76, v77
	ds_write_b64 v186, v[74:75] offset:544
	v_cmp_eq_u32_e32 vcc, v91, v140
	s_nop 1
	v_cndmask_b32_e64 v76, 0, 1.0, vcc
	v_cmp_eq_u32_e32 vcc, v102, v140
	s_nop 1
	v_cndmask_b32_e64 v77, 0, 1.0, vcc
	v_cmp_eq_u32_e32 vcc, v103, v140
	v_pk_fma_f32 v[70:71], v[236:237], v[70:71], v[76:77] op_sel_hi:[0,1,1] neg_lo:[1,0,0] neg_hi:[1,0,0]
	v_cvt_pk_bf16_f32 v70, v70, v71
	v_cndmask_b32_e64 v77, 0, 1.0, vcc
	v_cmp_eq_u32_e32 vcc, v104, v140
	s_nop 1
	v_cndmask_b32_e64 v76, 0, 1.0, vcc
	v_pk_fma_f32 v[72:73], v[236:237], v[72:73], v[76:77] op_sel_hi:[0,1,1] neg_lo:[1,0,0] neg_hi:[1,0,0]
	v_cvt_pk_bf16_f32 v71, v72, v73
	ds_write_b64 v186, v[70:71] offset:1088
	v_cmp_eq_u32_e32 vcc, v91, v141
	s_nop 1
	v_cndmask_b32_e64 v72, 0, 1.0, vcc
	v_cmp_eq_u32_e32 vcc, v102, v141
	s_nop 1
	v_cndmask_b32_e64 v73, 0, 1.0, vcc
	v_cmp_eq_u32_e32 vcc, v103, v141
	v_pk_fma_f32 v[66:67], v[238:239], v[66:67], v[72:73] op_sel_hi:[0,1,1] neg_lo:[1,0,0] neg_hi:[1,0,0]
	v_cvt_pk_bf16_f32 v66, v66, v67
	v_cndmask_b32_e64 v73, 0, 1.0, vcc
	v_cmp_eq_u32_e32 vcc, v104, v141
	s_nop 1
	v_cndmask_b32_e64 v72, 0, 1.0, vcc
	v_pk_fma_f32 v[68:69], v[238:239], v[68:69], v[72:73] op_sel_hi:[0,1,1] neg_lo:[1,0,0] neg_hi:[1,0,0]
	v_cvt_pk_bf16_f32 v67, v68, v69
	ds_write_b64 v186, v[66:67] offset:1632
	v_cmp_eq_u32_e32 vcc, v91, v142
	s_nop 1
	v_cndmask_b32_e64 v68, 0, 1.0, vcc
	v_cmp_eq_u32_e32 vcc, v102, v142
	s_nop 1
	v_cndmask_b32_e64 v69, 0, 1.0, vcc
	v_cmp_eq_u32_e32 vcc, v103, v142
	v_pk_fma_f32 v[30:31], v[240:241], v[30:31], v[68:69] op_sel_hi:[0,1,1] neg_lo:[1,0,0] neg_hi:[1,0,0]
	v_cvt_pk_bf16_f32 v30, v30, v31
	v_cndmask_b32_e64 v69, 0, 1.0, vcc
	v_cmp_eq_u32_e32 vcc, v104, v142
	s_nop 1
	v_cndmask_b32_e64 v68, 0, 1.0, vcc
	v_pk_fma_f32 v[32:33], v[240:241], v[32:33], v[68:69] op_sel_hi:[0,1,1] neg_lo:[1,0,0] neg_hi:[1,0,0]
	v_cvt_pk_bf16_f32 v31, v32, v33
	ds_write_b64 v186, v[30:31] offset:2176
	v_cmp_eq_u32_e32 vcc, v91, v143
	s_nop 1
	v_cndmask_b32_e64 v32, 0, 1.0, vcc
	v_cmp_eq_u32_e32 vcc, v102, v143
	s_nop 1
	v_cndmask_b32_e64 v33, 0, 1.0, vcc
	v_cmp_eq_u32_e32 vcc, v103, v143
	v_pk_fma_f32 v[26:27], v[242:243], v[26:27], v[32:33] op_sel_hi:[0,1,1] neg_lo:[1,0,0] neg_hi:[1,0,0]
	v_cvt_pk_bf16_f32 v26, v26, v27
	v_cndmask_b32_e64 v33, 0, 1.0, vcc
	v_cmp_eq_u32_e32 vcc, v104, v143
	s_nop 1
	v_cndmask_b32_e64 v32, 0, 1.0, vcc
	v_pk_fma_f32 v[28:29], v[242:243], v[28:29], v[32:33] op_sel_hi:[0,1,1] neg_lo:[1,0,0] neg_hi:[1,0,0]
	v_cvt_pk_bf16_f32 v27, v28, v29
	ds_write_b64 v186, v[26:27] offset:2720
	v_cmp_eq_u32_e32 vcc, v91, v144
	s_nop 1
	v_cndmask_b32_e64 v28, 0, 1.0, vcc
	v_cmp_eq_u32_e32 vcc, v102, v144
	s_nop 1
	v_cndmask_b32_e64 v29, 0, 1.0, vcc
	v_cmp_eq_u32_e32 vcc, v103, v144
	v_pk_fma_f32 v[22:23], v[244:245], v[22:23], v[28:29] op_sel_hi:[0,1,1] neg_lo:[1,0,0] neg_hi:[1,0,0]
	v_cvt_pk_bf16_f32 v22, v22, v23
	v_cndmask_b32_e64 v29, 0, 1.0, vcc
	v_cmp_eq_u32_e32 vcc, v104, v144
	s_nop 1
	v_cndmask_b32_e64 v28, 0, 1.0, vcc
	v_pk_fma_f32 v[24:25], v[244:245], v[24:25], v[28:29] op_sel_hi:[0,1,1] neg_lo:[1,0,0] neg_hi:[1,0,0]
	v_cvt_pk_bf16_f32 v23, v24, v25
	ds_write_b64 v186, v[22:23] offset:3264
	v_cmp_eq_u32_e32 vcc, v91, v145
	s_nop 1
	v_cndmask_b32_e64 v24, 0, 1.0, vcc
	v_cmp_eq_u32_e32 vcc, v102, v145
	s_nop 1
	v_cndmask_b32_e64 v25, 0, 1.0, vcc
	v_cmp_eq_u32_e32 vcc, v103, v145
	v_pk_fma_f32 v[18:19], v[246:247], v[18:19], v[24:25] op_sel_hi:[0,1,1] neg_lo:[1,0,0] neg_hi:[1,0,0]
	v_cvt_pk_bf16_f32 v18, v18, v19
	v_cndmask_b32_e64 v25, 0, 1.0, vcc
	v_cmp_eq_u32_e32 vcc, v104, v145
	s_nop 1
	v_cndmask_b32_e64 v24, 0, 1.0, vcc
	v_pk_fma_f32 v[20:21], v[246:247], v[20:21], v[24:25] op_sel_hi:[0,1,1] neg_lo:[1,0,0] neg_hi:[1,0,0]
	v_cvt_pk_bf16_f32 v19, v20, v21
	ds_write_b64 v186, v[18:19] offset:3808
	ds_read_b128 v[18:21], v1
	ds_read_b128 v[22:25], v1 offset:64
	ds_read_b128 v[26:29], v1 offset:128
	ds_read_b128 v[30:33], v1 offset:192
	v_lshl_add_u64 v[66:67], v[150:151], 0, s[8:9]
	v_lshl_add_u64 v[68:69], v[152:153], 0, s[8:9]
	v_lshl_add_u64 v[70:71], v[156:157], 0, s[8:9]
	v_lshl_add_u64 v[72:73], v[158:159], 0, s[8:9]
	v_lshl_add_u64 v[74:75], v[160:161], 0, s[8:9]
	v_lshl_add_u64 v[76:77], v[162:163], 0, s[8:9]
	v_lshl_add_u64 v[134:135], v[164:165], 0, s[8:9]
	v_lshl_add_u64 v[136:137], v[166:167], 0, s[8:9]
	global_load_dwordx4 v[126:129], v[66:67], off nt
	global_load_dwordx4 v[114:117], v[68:69], off nt
	global_load_dwordx4 v[102:105], v[70:71], off nt
	global_load_dwordx4 v[90:93], v[72:73], off nt
	global_load_dwordx4 v[78:81], v[74:75], off nt
	s_nop 0
	global_load_dwordx4 v[74:77], v[76:77], off nt
	s_nop 0
	global_load_dwordx4 v[70:73], v[134:135], off nt
	global_load_dwordx4 v[66:69], v[136:137], off nt
	s_waitcnt vmcnt(23)
	s_waitcnt vmcnt(22)
	s_waitcnt vmcnt(21)
	s_waitcnt vmcnt(20)
	s_waitcnt vmcnt(19)
	s_waitcnt vmcnt(18)
	s_waitcnt vmcnt(17)
	s_waitcnt vmcnt(16)
	ds_read_b32 v232, v187 offset:128
	ds_read_b32 v234, v187 offset:136
	ds_read_b32 v236, v187 offset:144
	ds_read_b32 v238, v187 offset:152
	ds_read_b32 v240, v187 offset:160
	ds_read_b32 v242, v187 offset:168
	ds_read_b32 v244, v187 offset:176
	ds_read_b32 v246, v187 offset:184
	v_or_b32_e32 v194, 32, v132
	v_add_u32_e32 v135, 1, v133
	v_cmp_eq_u32_e32 vcc, v133, v194
	v_add_u32_e32 v202, 3, v133
	v_add_u32_e32 v203, 2, v133
	v_cndmask_b32_e64 v136, 0, 1.0, vcc
	v_cmp_eq_u32_e32 vcc, v135, v194
	v_or_b32_e32 v195, 34, v132
	v_or_b32_e32 v196, 36, v132
	v_cndmask_b32_e64 v137, 0, 1.0, vcc
	v_cmp_eq_u32_e32 vcc, v202, v194
	s_waitcnt lgkmcnt(0)
	v_pk_fma_f32 v[122:123], v[232:233], v[122:123], v[136:137] op_sel_hi:[0,1,1] neg_lo:[1,0,0] neg_hi:[1,0,0]
	v_cvt_pk_bf16_f32 v122, v122, v123
	v_cndmask_b32_e64 v137, 0, 1.0, vcc
	v_cmp_eq_u32_e32 vcc, v203, v194
	v_or_b32_e32 v197, 38, v132
	v_or_b32_e32 v198, 40, v132
	v_cndmask_b32_e64 v136, 0, 1.0, vcc
	v_pk_fma_f32 v[124:125], v[232:233], v[124:125], v[136:137] op_sel_hi:[0,1,1] neg_lo:[1,0,0] neg_hi:[1,0,0]
	v_cvt_pk_bf16_f32 v123, v124, v125
	ds_write_b64 v186, v[122:123]
	v_cmp_eq_u32_e32 vcc, v133, v195
	v_or_b32_e32 v199, 42, v132
	v_or_b32_e32 v200, 44, v132
	v_cndmask_b32_e64 v124, 0, 1.0, vcc
	v_cmp_eq_u32_e32 vcc, v135, v195
	v_or_b32_e32 v201, 46, v132
	s_nop 0
	v_cndmask_b32_e64 v125, 0, 1.0, vcc
	v_cmp_eq_u32_e32 vcc, v202, v195
	v_pk_fma_f32 v[106:107], v[234:235], v[106:107], v[124:125] op_sel_hi:[0,1,1] neg_lo:[1,0,0] neg_hi:[1,0,0]
	v_cvt_pk_bf16_f32 v106, v106, v107
	v_cndmask_b32_e64 v125, 0, 1.0, vcc
	v_cmp_eq_u32_e32 vcc, v203, v195
	s_nop 1
	v_cndmask_b32_e64 v124, 0, 1.0, vcc
	v_pk_fma_f32 v[108:109], v[234:235], v[108:109], v[124:125] op_sel_hi:[0,1,1] neg_lo:[1,0,0] neg_hi:[1,0,0]
	v_cvt_pk_bf16_f32 v107, v108, v109
	ds_write_b64 v186, v[106:107] offset:544
	v_cmp_eq_u32_e32 vcc, v133, v196
	s_nop 1
	v_cndmask_b32_e64 v108, 0, 1.0, vcc
	v_cmp_eq_u32_e32 vcc, v135, v196
	s_nop 1
	v_cndmask_b32_e64 v109, 0, 1.0, vcc
	v_cmp_eq_u32_e32 vcc, v202, v196
	v_pk_fma_f32 v[94:95], v[236:237], v[94:95], v[108:109] op_sel_hi:[0,1,1] neg_lo:[1,0,0] neg_hi:[1,0,0]
	v_cvt_pk_bf16_f32 v94, v94, v95
	v_cndmask_b32_e64 v109, 0, 1.0, vcc
	v_cmp_eq_u32_e32 vcc, v203, v196
	s_nop 1
	v_cndmask_b32_e64 v108, 0, 1.0, vcc
	v_pk_fma_f32 v[96:97], v[236:237], v[96:97], v[108:109] op_sel_hi:[0,1,1] neg_lo:[1,0,0] neg_hi:[1,0,0]
	v_cvt_pk_bf16_f32 v95, v96, v97
	ds_write_b64 v186, v[94:95] offset:1088
	v_cmp_eq_u32_e32 vcc, v133, v197
	s_nop 1
	v_cndmask_b32_e64 v96, 0, 1.0, vcc
	v_cmp_eq_u32_e32 vcc, v135, v197
	s_nop 1
	v_cndmask_b32_e64 v97, 0, 1.0, vcc
	v_cmp_eq_u32_e32 vcc, v202, v197
	v_pk_fma_f32 v[82:83], v[238:239], v[82:83], v[96:97] op_sel_hi:[0,1,1] neg_lo:[1,0,0] neg_hi:[1,0,0]
	v_cvt_pk_bf16_f32 v82, v82, v83
	v_cndmask_b32_e64 v97, 0, 1.0, vcc
	v_cmp_eq_u32_e32 vcc, v203, v197
	s_nop 1
	v_cndmask_b32_e64 v96, 0, 1.0, vcc
	v_pk_fma_f32 v[84:85], v[238:239], v[84:85], v[96:97] op_sel_hi:[0,1,1] neg_lo:[1,0,0] neg_hi:[1,0,0]
	v_cvt_pk_bf16_f32 v83, v84, v85
	ds_write_b64 v186, v[82:83] offset:1632
	v_cmp_eq_u32_e32 vcc, v133, v198
	s_nop 1
	v_cndmask_b32_e64 v84, 0, 1.0, vcc
	v_cmp_eq_u32_e32 vcc, v135, v198
	s_nop 1
	v_cndmask_b32_e64 v85, 0, 1.0, vcc
	v_cmp_eq_u32_e32 vcc, v202, v198
	v_pk_fma_f32 v[46:47], v[240:241], v[46:47], v[84:85] op_sel_hi:[0,1,1] neg_lo:[1,0,0] neg_hi:[1,0,0]
	v_cvt_pk_bf16_f32 v46, v46, v47
	v_cndmask_b32_e64 v85, 0, 1.0, vcc
	v_cmp_eq_u32_e32 vcc, v203, v198
	s_nop 1
	v_cndmask_b32_e64 v84, 0, 1.0, vcc
	v_pk_fma_f32 v[48:49], v[240:241], v[48:49], v[84:85] op_sel_hi:[0,1,1] neg_lo:[1,0,0] neg_hi:[1,0,0]
	v_cvt_pk_bf16_f32 v47, v48, v49
	ds_write_b64 v186, v[46:47] offset:2176
	v_cmp_eq_u32_e32 vcc, v133, v199
	s_nop 1
	v_cndmask_b32_e64 v48, 0, 1.0, vcc
	v_cmp_eq_u32_e32 vcc, v135, v199
	s_nop 1
	v_cndmask_b32_e64 v49, 0, 1.0, vcc
	v_cmp_eq_u32_e32 vcc, v202, v199
	v_pk_fma_f32 v[42:43], v[242:243], v[42:43], v[48:49] op_sel_hi:[0,1,1] neg_lo:[1,0,0] neg_hi:[1,0,0]
	v_cvt_pk_bf16_f32 v42, v42, v43
	v_cndmask_b32_e64 v49, 0, 1.0, vcc
	v_cmp_eq_u32_e32 vcc, v203, v199
	s_nop 1
	v_cndmask_b32_e64 v48, 0, 1.0, vcc
	v_pk_fma_f32 v[44:45], v[242:243], v[44:45], v[48:49] op_sel_hi:[0,1,1] neg_lo:[1,0,0] neg_hi:[1,0,0]
	v_cvt_pk_bf16_f32 v43, v44, v45
	ds_write_b64 v186, v[42:43] offset:2720
	v_cmp_eq_u32_e32 vcc, v133, v200
	s_nop 1
	v_cndmask_b32_e64 v44, 0, 1.0, vcc
	v_cmp_eq_u32_e32 vcc, v135, v200
	s_nop 1
	v_cndmask_b32_e64 v45, 0, 1.0, vcc
	v_cmp_eq_u32_e32 vcc, v202, v200
	v_pk_fma_f32 v[38:39], v[244:245], v[38:39], v[44:45] op_sel_hi:[0,1,1] neg_lo:[1,0,0] neg_hi:[1,0,0]
	v_cvt_pk_bf16_f32 v38, v38, v39
	v_cndmask_b32_e64 v45, 0, 1.0, vcc
	v_cmp_eq_u32_e32 vcc, v203, v200
	s_nop 1
	v_cndmask_b32_e64 v44, 0, 1.0, vcc
	v_pk_fma_f32 v[40:41], v[244:245], v[40:41], v[44:45] op_sel_hi:[0,1,1] neg_lo:[1,0,0] neg_hi:[1,0,0]
	v_cvt_pk_bf16_f32 v39, v40, v41
	ds_write_b64 v186, v[38:39] offset:3264
	v_cmp_eq_u32_e32 vcc, v133, v201
	s_nop 1
	v_cndmask_b32_e64 v40, 0, 1.0, vcc
	v_cmp_eq_u32_e32 vcc, v135, v201
	s_nop 1
	v_cndmask_b32_e64 v41, 0, 1.0, vcc
	v_cmp_eq_u32_e32 vcc, v202, v201
	v_pk_fma_f32 v[34:35], v[246:247], v[34:35], v[40:41] op_sel_hi:[0,1,1] neg_lo:[1,0,0] neg_hi:[1,0,0]
	v_cvt_pk_bf16_f32 v34, v34, v35
	v_cndmask_b32_e64 v41, 0, 1.0, vcc
	v_cmp_eq_u32_e32 vcc, v203, v201
	s_nop 1
	v_cndmask_b32_e64 v40, 0, 1.0, vcc
	v_pk_fma_f32 v[36:37], v[246:247], v[36:37], v[40:41] op_sel_hi:[0,1,1] neg_lo:[1,0,0] neg_hi:[1,0,0]
	v_cvt_pk_bf16_f32 v35, v36, v37
	ds_write_b64 v186, v[34:35] offset:3808
	ds_read_b128 v[34:37], v1
	ds_read_b128 v[38:41], v1 offset:64
	ds_read_b128 v[42:45], v1 offset:128
	ds_read_b128 v[46:49], v1 offset:192
	v_mov_b32_e32 v106, v189
	s_waitcnt vmcnt(15)
	s_waitcnt vmcnt(14)
	s_waitcnt vmcnt(13)
	s_waitcnt vmcnt(12)
	s_waitcnt vmcnt(11)
	s_waitcnt vmcnt(10)
	s_waitcnt vmcnt(9)
	s_waitcnt vmcnt(8)
	ds_read_b32 v232, v187 offset:0
	ds_read_b32 v234, v187 offset:8
	ds_read_b32 v236, v187 offset:16
	ds_read_b32 v238, v187 offset:24
	ds_read_b32 v240, v187 offset:32
	ds_read_b32 v242, v187 offset:40
	ds_read_b32 v244, v187 offset:48
	ds_read_b32 v246, v187 offset:56
	v_add_u32_e32 v107, 1, v106
	v_cmp_eq_u32_e32 vcc, v106, v132
	v_add_u32_e32 v108, 3, v106
	v_add_u32_e32 v109, 2, v106
	v_cndmask_b32_e64 v84, 0, 1.0, vcc
	v_cmp_eq_u32_e32 vcc, v107, v132
	s_nop 1
	v_cndmask_b32_e64 v85, 0, 1.0, vcc
	v_cmp_eq_u32_e32 vcc, v108, v132
	s_waitcnt lgkmcnt(0)
	v_pk_fma_f32 v[94:95], v[232:233], v[118:119], v[84:85] op_sel_hi:[0,1,1] neg_lo:[1,0,0] neg_hi:[1,0,0]
	v_cvt_pk_bf16_f32 v94, v94, v95
	v_cndmask_b32_e64 v97, 0, 1.0, vcc
	v_cmp_eq_u32_e32 vcc, v109, v132
	s_nop 1
	v_cndmask_b32_e64 v96, 0, 1.0, vcc
	v_pk_fma_f32 v[82:83], v[232:233], v[120:121], v[96:97] op_sel_hi:[0,1,1] neg_lo:[1,0,0] neg_hi:[1,0,0]
	v_cvt_pk_bf16_f32 v95, v82, v83
	ds_write_b64 v186, v[94:95]
	v_cmp_eq_u32_e32 vcc, v106, v193
	s_nop 1
	v_cndmask_b32_e64 v94, 0, 1.0, vcc
	v_cmp_eq_u32_e32 vcc, v107, v193
	s_nop 1
	v_cndmask_b32_e64 v95, 0, 1.0, vcc
	v_cmp_eq_u32_e32 vcc, v108, v193
	v_pk_fma_f32 v[94:95], v[234:235], v[110:111], v[94:95] op_sel_hi:[0,1,1] neg_lo:[1,0,0] neg_hi:[1,0,0]
	v_cvt_pk_bf16_f32 v94, v94, v95
	v_cndmask_b32_e64 v85, 0, 1.0, vcc
	v_pk_fma_f32 v[82:83], v[234:235], v[112:113], v[84:85] op_sel_hi:[0,1,1] neg_lo:[1,0,0] neg_hi:[1,0,0]
	v_cvt_pk_bf16_f32 v95, v82, v83
	ds_write_b64 v186, v[94:95] offset:544
	v_cmp_eq_u32_e32 vcc, v106, v192
	s_nop 1
	v_cndmask_b32_e64 v84, 0, 1.0, vcc
	v_cmp_eq_u32_e32 vcc, v107, v192
	s_nop 1
	v_cndmask_b32_e64 v85, 0, 1.0, vcc
	v_cmp_eq_u32_e32 vcc, v108, v192
	v_pk_fma_f32 v[84:85], v[236:237], v[98:99], v[84:85] op_sel_hi:[0,1,1] neg_lo:[1,0,0] neg_hi:[1,0,0]
	v_cvt_pk_bf16_f32 v84, v84, v85
	v_cndmask_b32_e64 v95, 0, 1.0, vcc
	v_cmp_eq_u32_e32 vcc, v109, v192
	s_nop 1
	v_cndmask_b32_e64 v94, 0, 1.0, vcc
	v_pk_fma_f32 v[82:83], v[236:237], v[100:101], v[94:95] op_sel_hi:[0,1,1] neg_lo:[1,0,0] neg_hi:[1,0,0]
	v_cvt_pk_bf16_f32 v85, v82, v83
	ds_write_b64 v186, v[84:85] offset:1088
	v_cmp_eq_u32_e32 vcc, v106, v190
	s_nop 1
	v_cndmask_b32_e64 v84, 0, 1.0, vcc
	v_cmp_eq_u32_e32 vcc, v107, v190
	s_nop 1
	v_cndmask_b32_e64 v85, 0, 1.0, vcc
	v_cmp_eq_u32_e32 vcc, v108, v190
	v_pk_fma_f32 v[84:85], v[238:239], v[86:87], v[84:85] op_sel_hi:[0,1,1] neg_lo:[1,0,0] neg_hi:[1,0,0]
	v_cvt_pk_bf16_f32 v84, v84, v85
	v_cndmask_b32_e64 v87, 0, 1.0, vcc
	v_cmp_eq_u32_e32 vcc, v109, v190
	s_nop 1
	v_cndmask_b32_e64 v86, 0, 1.0, vcc
	v_pk_fma_f32 v[82:83], v[238:239], v[88:89], v[86:87] op_sel_hi:[0,1,1] neg_lo:[1,0,0] neg_hi:[1,0,0]
	v_cvt_pk_bf16_f32 v85, v82, v83
	ds_write_b64 v186, v[84:85] offset:1632
	v_cmp_eq_u32_e32 vcc, v106, v149
	s_nop 1
	v_cndmask_b32_e64 v84, 0, 1.0, vcc
	v_cmp_eq_u32_e32 vcc, v107, v149
	s_nop 1
	v_cndmask_b32_e64 v85, 0, 1.0, vcc
	v_cmp_eq_u32_e32 vcc, v108, v149
	v_pk_fma_f32 v[62:63], v[240:241], v[62:63], v[84:85] op_sel_hi:[0,1,1] neg_lo:[1,0,0] neg_hi:[1,0,0]
	v_cvt_pk_bf16_f32 v62, v62, v63
	v_cndmask_b32_e64 v85, 0, 1.0, vcc
	v_cmp_eq_u32_e32 vcc, v109, v149
	s_nop 1
	v_cndmask_b32_e64 v84, 0, 1.0, vcc
	v_pk_fma_f32 v[64:65], v[240:241], v[64:65], v[84:85] op_sel_hi:[0,1,1] neg_lo:[1,0,0] neg_hi:[1,0,0]
	v_cvt_pk_bf16_f32 v63, v64, v65
	ds_write_b64 v186, v[62:63] offset:2176
	v_cmp_eq_u32_e32 vcc, v106, v148
	s_nop 1
	v_cndmask_b32_e64 v64, 0, 1.0, vcc
	v_cmp_eq_u32_e32 vcc, v107, v148
	s_nop 1
	v_cndmask_b32_e64 v65, 0, 1.0, vcc
	v_cmp_eq_u32_e32 vcc, v108, v148
	v_pk_fma_f32 v[58:59], v[242:243], v[58:59], v[64:65] op_sel_hi:[0,1,1] neg_lo:[1,0,0] neg_hi:[1,0,0]
	v_cvt_pk_bf16_f32 v58, v58, v59
	v_cndmask_b32_e64 v65, 0, 1.0, vcc
	v_cmp_eq_u32_e32 vcc, v109, v148
	s_nop 1
	v_cndmask_b32_e64 v64, 0, 1.0, vcc
	v_pk_fma_f32 v[60:61], v[242:243], v[60:61], v[64:65] op_sel_hi:[0,1,1] neg_lo:[1,0,0] neg_hi:[1,0,0]
	v_cvt_pk_bf16_f32 v59, v60, v61
	ds_write_b64 v186, v[58:59] offset:2720
	v_cmp_eq_u32_e32 vcc, v106, v147
	s_nop 1
	v_cndmask_b32_e64 v60, 0, 1.0, vcc
	v_cmp_eq_u32_e32 vcc, v107, v147
	s_nop 1
	v_cndmask_b32_e64 v61, 0, 1.0, vcc
	v_cmp_eq_u32_e32 vcc, v108, v147
	v_pk_fma_f32 v[54:55], v[244:245], v[54:55], v[60:61] op_sel_hi:[0,1,1] neg_lo:[1,0,0] neg_hi:[1,0,0]
	v_cvt_pk_bf16_f32 v54, v54, v55
	v_cndmask_b32_e64 v61, 0, 1.0, vcc
	v_cmp_eq_u32_e32 vcc, v109, v147
	s_nop 1
	v_cndmask_b32_e64 v60, 0, 1.0, vcc
	v_pk_fma_f32 v[56:57], v[244:245], v[56:57], v[60:61] op_sel_hi:[0,1,1] neg_lo:[1,0,0] neg_hi:[1,0,0]
	v_cvt_pk_bf16_f32 v55, v56, v57
	ds_write_b64 v186, v[54:55] offset:3264
	v_cmp_eq_u32_e32 vcc, v106, v146
	s_nop 1
	v_cndmask_b32_e64 v56, 0, 1.0, vcc
	v_cmp_eq_u32_e32 vcc, v107, v146
	s_nop 1
	v_cndmask_b32_e64 v57, 0, 1.0, vcc
	v_cmp_eq_u32_e32 vcc, v108, v146
	v_pk_fma_f32 v[50:51], v[246:247], v[50:51], v[56:57] op_sel_hi:[0,1,1] neg_lo:[1,0,0] neg_hi:[1,0,0]
	v_cvt_pk_bf16_f32 v50, v50, v51
	v_cndmask_b32_e64 v57, 0, 1.0, vcc
	v_cmp_eq_u32_e32 vcc, v109, v146
	s_nop 1
	v_cndmask_b32_e64 v56, 0, 1.0, vcc
	v_pk_fma_f32 v[52:53], v[246:247], v[52:53], v[56:57] op_sel_hi:[0,1,1] neg_lo:[1,0,0] neg_hi:[1,0,0]
	v_cvt_pk_bf16_f32 v51, v52, v53
	ds_write_b64 v186, v[50:51] offset:3808
	ds_read_b128 v[50:53], v1
	ds_read_b128 v[54:57], v1 offset:64
	ds_read_b128 v[58:61], v1 offset:128
	ds_read_b128 v[62:65], v1 offset:192
	v_lshl_add_u64 v[82:83], v[168:169], 0, s[8:9]
	v_lshl_add_u64 v[84:85], v[170:171], 0, s[8:9]
	v_lshl_add_u64 v[86:87], v[172:173], 0, s[8:9]
	v_lshl_add_u64 v[88:89], v[174:175], 0, s[8:9]
	v_lshl_add_u64 v[94:95], v[176:177], 0, s[8:9]
	v_lshl_add_u64 v[96:97], v[178:179], 0, s[8:9]
	v_lshl_add_u64 v[122:123], v[180:181], 0, s[8:9]
	v_lshl_add_u64 v[124:125], v[182:183], 0, s[8:9]
	global_load_dwordx4 v[134:137], v[82:83], off nt
	global_load_dwordx4 v[118:121], v[84:85], off nt
	global_load_dwordx4 v[110:113], v[86:87], off nt
	global_load_dwordx4 v[106:109], v[88:89], off nt
	global_load_dwordx4 v[98:101], v[94:95], off nt
	s_nop 0
	global_load_dwordx4 v[94:97], v[96:97], off nt
	s_nop 0
	global_load_dwordx4 v[86:89], v[122:123], off nt
	global_load_dwordx4 v[82:85], v[124:125], off nt
	v_mov_b32_e32 v132, v189
	s_waitcnt vmcnt(15)
	s_waitcnt vmcnt(14)
	s_waitcnt vmcnt(13)
	s_waitcnt vmcnt(12)
	s_waitcnt vmcnt(11)
	s_waitcnt vmcnt(10)
	s_waitcnt vmcnt(9)
	s_waitcnt vmcnt(8)
	ds_read_b32 v232, v187 offset:64
	ds_read_b32 v234, v187 offset:72
	ds_read_b32 v236, v187 offset:80
	ds_read_b32 v238, v187 offset:88
	ds_read_b32 v240, v187 offset:96
	ds_read_b32 v242, v187 offset:104
	ds_read_b32 v244, v187 offset:112
	ds_read_b32 v246, v187 offset:120
	v_add_u32_e32 v133, 1, v132
	v_cmp_eq_u32_e32 vcc, v132, v138
	v_add_u32_e32 v146, 3, v132
	v_add_u32_e32 v147, 2, v132
	v_cndmask_b32_e64 v124, 0, 1.0, vcc
	v_cmp_eq_u32_e32 vcc, v133, v138
	s_nop 1
	v_cndmask_b32_e64 v125, 0, 1.0, vcc
	v_cmp_eq_u32_e32 vcc, v146, v138
	s_waitcnt lgkmcnt(0)
	v_pk_fma_f32 v[124:125], v[232:233], v[126:127], v[124:125] op_sel_hi:[0,1,1] neg_lo:[1,0,0] neg_hi:[1,0,0]
	v_cvt_pk_bf16_f32 v124, v124, v125
	v_cndmask_b32_e64 v127, 0, 1.0, vcc
	v_cmp_eq_u32_e32 vcc, v147, v138
	s_nop 1
	v_cndmask_b32_e64 v126, 0, 1.0, vcc
	v_pk_fma_f32 v[122:123], v[232:233], v[128:129], v[126:127] op_sel_hi:[0,1,1] neg_lo:[1,0,0] neg_hi:[1,0,0]
	v_cvt_pk_bf16_f32 v125, v122, v123
	ds_write_b64 v186, v[124:125]
	v_cmp_eq_u32_e32 vcc, v132, v139
	s_nop 1
	v_cndmask_b32_e64 v124, 0, 1.0, vcc
	v_cmp_eq_u32_e32 vcc, v133, v139
	s_nop 1
	v_cndmask_b32_e64 v125, 0, 1.0, vcc
	v_cmp_eq_u32_e32 vcc, v146, v139
	v_pk_fma_f32 v[114:115], v[234:235], v[114:115], v[124:125] op_sel_hi:[0,1,1] neg_lo:[1,0,0] neg_hi:[1,0,0]
	v_cvt_pk_bf16_f32 v114, v114, v115
	v_cndmask_b32_e64 v125, 0, 1.0, vcc
	v_cmp_eq_u32_e32 vcc, v147, v139
	s_nop 1
	v_cndmask_b32_e64 v124, 0, 1.0, vcc
	v_pk_fma_f32 v[116:117], v[234:235], v[116:117], v[124:125] op_sel_hi:[0,1,1] neg_lo:[1,0,0] neg_hi:[1,0,0]
	v_cvt_pk_bf16_f32 v115, v116, v117
	ds_write_b64 v186, v[114:115] offset:544
	v_cmp_eq_u32_e32 vcc, v132, v140
	s_nop 1
	v_cndmask_b32_e64 v116, 0, 1.0, vcc
	v_cmp_eq_u32_e32 vcc, v133, v140
	s_nop 1
	v_cndmask_b32_e64 v117, 0, 1.0, vcc
	v_cmp_eq_u32_e32 vcc, v146, v140
	v_pk_fma_f32 v[102:103], v[236:237], v[102:103], v[116:117] op_sel_hi:[0,1,1] neg_lo:[1,0,0] neg_hi:[1,0,0]
	v_cvt_pk_bf16_f32 v102, v102, v103
	v_cndmask_b32_e64 v117, 0, 1.0, vcc
	v_cmp_eq_u32_e32 vcc, v147, v140
	s_nop 1
	v_cndmask_b32_e64 v116, 0, 1.0, vcc
	v_pk_fma_f32 v[104:105], v[236:237], v[104:105], v[116:117] op_sel_hi:[0,1,1] neg_lo:[1,0,0] neg_hi:[1,0,0]
	v_cvt_pk_bf16_f32 v103, v104, v105
	ds_write_b64 v186, v[102:103] offset:1088
	v_cmp_eq_u32_e32 vcc, v132, v141
	s_nop 1
	v_cndmask_b32_e64 v104, 0, 1.0, vcc
	v_cmp_eq_u32_e32 vcc, v133, v141
	s_nop 1
	v_cndmask_b32_e64 v105, 0, 1.0, vcc
	v_cmp_eq_u32_e32 vcc, v146, v141
	v_pk_fma_f32 v[90:91], v[238:239], v[90:91], v[104:105] op_sel_hi:[0,1,1] neg_lo:[1,0,0] neg_hi:[1,0,0]
	v_cvt_pk_bf16_f32 v90, v90, v91
	v_cndmask_b32_e64 v105, 0, 1.0, vcc
	v_cmp_eq_u32_e32 vcc, v147, v141
	s_nop 1
	v_cndmask_b32_e64 v104, 0, 1.0, vcc
	v_pk_fma_f32 v[92:93], v[238:239], v[92:93], v[104:105] op_sel_hi:[0,1,1] neg_lo:[1,0,0] neg_hi:[1,0,0]
	v_cvt_pk_bf16_f32 v91, v92, v93
	ds_write_b64 v186, v[90:91] offset:1632
	v_cmp_eq_u32_e32 vcc, v132, v142
	s_nop 1
	v_cndmask_b32_e64 v92, 0, 1.0, vcc
	v_cmp_eq_u32_e32 vcc, v133, v142
	s_nop 1
	v_cndmask_b32_e64 v93, 0, 1.0, vcc
	v_cmp_eq_u32_e32 vcc, v146, v142
	v_pk_fma_f32 v[78:79], v[240:241], v[78:79], v[92:93] op_sel_hi:[0,1,1] neg_lo:[1,0,0] neg_hi:[1,0,0]
	v_cvt_pk_bf16_f32 v78, v78, v79
	v_cndmask_b32_e64 v93, 0, 1.0, vcc
	v_cmp_eq_u32_e32 vcc, v147, v142
	s_nop 1
	v_cndmask_b32_e64 v92, 0, 1.0, vcc
	v_pk_fma_f32 v[80:81], v[240:241], v[80:81], v[92:93] op_sel_hi:[0,1,1] neg_lo:[1,0,0] neg_hi:[1,0,0]
	v_cvt_pk_bf16_f32 v79, v80, v81
	ds_write_b64 v186, v[78:79] offset:2176
	v_cmp_eq_u32_e32 vcc, v132, v143
	s_nop 1
	v_cndmask_b32_e64 v80, 0, 1.0, vcc
	v_cmp_eq_u32_e32 vcc, v133, v143
	s_nop 1
	v_cndmask_b32_e64 v81, 0, 1.0, vcc
	v_cmp_eq_u32_e32 vcc, v146, v143
	v_pk_fma_f32 v[74:75], v[242:243], v[74:75], v[80:81] op_sel_hi:[0,1,1] neg_lo:[1,0,0] neg_hi:[1,0,0]
	v_cvt_pk_bf16_f32 v74, v74, v75
	v_cndmask_b32_e64 v81, 0, 1.0, vcc
	v_cmp_eq_u32_e32 vcc, v147, v143
	s_nop 1
	v_cndmask_b32_e64 v80, 0, 1.0, vcc
	v_pk_fma_f32 v[76:77], v[242:243], v[76:77], v[80:81] op_sel_hi:[0,1,1] neg_lo:[1,0,0] neg_hi:[1,0,0]
	v_cvt_pk_bf16_f32 v75, v76, v77
	ds_write_b64 v186, v[74:75] offset:2720
	v_cmp_eq_u32_e32 vcc, v132, v144
	s_nop 1
	v_cndmask_b32_e64 v76, 0, 1.0, vcc
	v_cmp_eq_u32_e32 vcc, v133, v144
	s_nop 1
	v_cndmask_b32_e64 v77, 0, 1.0, vcc
	v_cmp_eq_u32_e32 vcc, v146, v144
	v_pk_fma_f32 v[70:71], v[244:245], v[70:71], v[76:77] op_sel_hi:[0,1,1] neg_lo:[1,0,0] neg_hi:[1,0,0]
	v_cvt_pk_bf16_f32 v70, v70, v71
	v_cndmask_b32_e64 v77, 0, 1.0, vcc
	v_cmp_eq_u32_e32 vcc, v147, v144
	s_nop 1
	v_cndmask_b32_e64 v76, 0, 1.0, vcc
	v_pk_fma_f32 v[72:73], v[244:245], v[72:73], v[76:77] op_sel_hi:[0,1,1] neg_lo:[1,0,0] neg_hi:[1,0,0]
	v_cvt_pk_bf16_f32 v71, v72, v73
	ds_write_b64 v186, v[70:71] offset:3264
	v_cmp_eq_u32_e32 vcc, v132, v145
	s_nop 1
	v_cndmask_b32_e64 v72, 0, 1.0, vcc
	v_cmp_eq_u32_e32 vcc, v133, v145
	s_nop 1
	v_cndmask_b32_e64 v73, 0, 1.0, vcc
	v_cmp_eq_u32_e32 vcc, v146, v145
	v_pk_fma_f32 v[66:67], v[246:247], v[66:67], v[72:73] op_sel_hi:[0,1,1] neg_lo:[1,0,0] neg_hi:[1,0,0]
	v_cvt_pk_bf16_f32 v66, v66, v67
	v_cndmask_b32_e64 v73, 0, 1.0, vcc
	v_cmp_eq_u32_e32 vcc, v147, v145
	s_nop 1
	v_cndmask_b32_e64 v72, 0, 1.0, vcc
	v_pk_fma_f32 v[68:69], v[246:247], v[68:69], v[72:73] op_sel_hi:[0,1,1] neg_lo:[1,0,0] neg_hi:[1,0,0]
	v_cvt_pk_bf16_f32 v67, v68, v69
	ds_write_b64 v186, v[66:67] offset:3808
	ds_read_b128 v[66:69], v1
	ds_read_b128 v[70:73], v1 offset:64
	ds_read_b128 v[74:77], v1 offset:128
	ds_read_b128 v[78:81], v1 offset:192
	v_lshl_add_u64 v[90:91], v[130:131], 0, s[0:1]
	v_add_co_u32_e32 v92, vcc, s7, v90
	s_nop 1
	v_addc_co_u32_e32 v93, vcc, 0, v91, vcc
	global_load_dwordx4 v[146:149], v[90:91], off nt
	global_load_dwordx4 v[142:145], v[92:93], off nt
	v_add_co_u32_e32 v92, vcc, s36, v90
	s_nop 1
	v_addc_co_u32_e32 v93, vcc, 0, v91, vcc
	v_add_co_u32_e32 v102, vcc, s37, v90
	s_nop 1
	v_addc_co_u32_e32 v103, vcc, 0, v91, vcc
	global_load_dwordx4 v[138:141], v[92:93], off nt
	global_load_dwordx4 v[130:133], v[102:103], off nt
	v_add_co_u32_e32 v92, vcc, s38, v90
	s_nop 1
	v_addc_co_u32_e32 v93, vcc, 0, v91, vcc
	v_add_co_u32_e32 v102, vcc, s39, v90
	s_nop 1
	v_addc_co_u32_e32 v103, vcc, 0, v91, vcc
	global_load_dwordx4 v[126:129], v[92:93], off nt
	global_load_dwordx4 v[122:125], v[102:103], off nt
	v_add_co_u32_e32 v92, vcc, s41, v90
	s_nop 1
	v_addc_co_u32_e32 v93, vcc, 0, v91, vcc
	v_add_co_u32_e32 v90, vcc, s42, v90
	s_nop 1
	v_addc_co_u32_e32 v91, vcc, 0, v91, vcc
	global_load_dwordx4 v[114:117], v[92:93], off nt
	global_load_dwordx4 v[102:105], v[90:91], off nt
	s_waitcnt vmcnt(15)
	s_waitcnt vmcnt(14)
	s_waitcnt vmcnt(13)
	s_waitcnt vmcnt(12)
	s_waitcnt vmcnt(11)
	s_waitcnt vmcnt(10)
	s_waitcnt vmcnt(9)
	s_waitcnt vmcnt(8)
	ds_read_b32 v232, v187 offset:128
	ds_read_b32 v234, v187 offset:136
	ds_read_b32 v236, v187 offset:144
	ds_read_b32 v238, v187 offset:152
	ds_read_b32 v240, v187 offset:160
	ds_read_b32 v242, v187 offset:168
	ds_read_b32 v244, v187 offset:176
	ds_read_b32 v246, v187 offset:184
	v_add_u32_e32 v190, 1, v189
	v_cmp_eq_u32_e32 vcc, v189, v194
	v_add_u32_e32 v192, 3, v189
	v_add_u32_e32 v193, 2, v189
	v_cndmask_b32_e64 v92, 0, 1.0, vcc
	v_cmp_eq_u32_e32 vcc, v190, v194
	s_nop 1
	v_cndmask_b32_e64 v93, 0, 1.0, vcc
	v_cmp_eq_u32_e32 vcc, v192, v194
	s_waitcnt lgkmcnt(0)
	v_pk_fma_f32 v[92:93], v[232:233], v[134:135], v[92:93] op_sel_hi:[0,1,1] neg_lo:[1,0,0] neg_hi:[1,0,0]
	v_cvt_pk_bf16_f32 v92, v92, v93
	v_cndmask_b32_e64 v135, 0, 1.0, vcc
	v_cmp_eq_u32_e32 vcc, v193, v194
	s_nop 1
	v_cndmask_b32_e64 v134, 0, 1.0, vcc
	v_pk_fma_f32 v[90:91], v[232:233], v[136:137], v[134:135] op_sel_hi:[0,1,1] neg_lo:[1,0,0] neg_hi:[1,0,0]
	v_cvt_pk_bf16_f32 v93, v90, v91
	ds_write_b64 v186, v[92:93]
	v_cmp_eq_u32_e32 vcc, v189, v195
	s_nop 1
	v_cndmask_b32_e64 v92, 0, 1.0, vcc
	v_cmp_eq_u32_e32 vcc, v190, v195
	s_nop 1
	v_cndmask_b32_e64 v93, 0, 1.0, vcc
	v_cmp_eq_u32_e32 vcc, v192, v195
	v_pk_fma_f32 v[92:93], v[234:235], v[118:119], v[92:93] op_sel_hi:[0,1,1] neg_lo:[1,0,0] neg_hi:[1,0,0]
	v_cvt_pk_bf16_f32 v92, v92, v93
	v_cndmask_b32_e64 v119, 0, 1.0, vcc
	v_cmp_eq_u32_e32 vcc, v193, v195
	s_nop 1
	v_cndmask_b32_e64 v118, 0, 1.0, vcc
	v_pk_fma_f32 v[90:91], v[234:235], v[120:121], v[118:119] op_sel_hi:[0,1,1] neg_lo:[1,0,0] neg_hi:[1,0,0]
	v_cvt_pk_bf16_f32 v93, v90, v91
	ds_write_b64 v186, v[92:93] offset:544
	v_cmp_eq_u32_e32 vcc, v189, v196
	s_nop 1
	v_cndmask_b32_e64 v92, 0, 1.0, vcc
	v_cmp_eq_u32_e32 vcc, v190, v196
	s_nop 1
	v_cndmask_b32_e64 v93, 0, 1.0, vcc
	v_cmp_eq_u32_e32 vcc, v192, v196
	v_pk_fma_f32 v[92:93], v[236:237], v[110:111], v[92:93] op_sel_hi:[0,1,1] neg_lo:[1,0,0] neg_hi:[1,0,0]
	v_cvt_pk_bf16_f32 v92, v92, v93
	v_cndmask_b32_e64 v111, 0, 1.0, vcc
	v_cmp_eq_u32_e32 vcc, v193, v196
	s_nop 1
	v_cndmask_b32_e64 v110, 0, 1.0, vcc
	v_pk_fma_f32 v[90:91], v[236:237], v[112:113], v[110:111] op_sel_hi:[0,1,1] neg_lo:[1,0,0] neg_hi:[1,0,0]
	v_cvt_pk_bf16_f32 v93, v90, v91
	ds_write_b64 v186, v[92:93] offset:1088
	v_cmp_eq_u32_e32 vcc, v189, v197
	s_nop 1
	v_cndmask_b32_e64 v92, 0, 1.0, vcc
	v_cmp_eq_u32_e32 vcc, v190, v197
	s_nop 1
	v_cndmask_b32_e64 v93, 0, 1.0, vcc
	v_cmp_eq_u32_e32 vcc, v192, v197
	v_pk_fma_f32 v[92:93], v[238:239], v[106:107], v[92:93] op_sel_hi:[0,1,1] neg_lo:[1,0,0] neg_hi:[1,0,0]
	v_cvt_pk_bf16_f32 v92, v92, v93
	v_cndmask_b32_e64 v107, 0, 1.0, vcc
	v_cmp_eq_u32_e32 vcc, v193, v197
	s_nop 1
	v_cndmask_b32_e64 v106, 0, 1.0, vcc
	v_pk_fma_f32 v[90:91], v[238:239], v[108:109], v[106:107] op_sel_hi:[0,1,1] neg_lo:[1,0,0] neg_hi:[1,0,0]
	v_cvt_pk_bf16_f32 v93, v90, v91
	ds_write_b64 v186, v[92:93] offset:1632
	v_cmp_eq_u32_e32 vcc, v189, v198
	s_nop 1
	v_cndmask_b32_e64 v92, 0, 1.0, vcc
	v_cmp_eq_u32_e32 vcc, v190, v198
	s_nop 1
	v_cndmask_b32_e64 v93, 0, 1.0, vcc
	v_cmp_eq_u32_e32 vcc, v192, v198
	v_pk_fma_f32 v[92:93], v[240:241], v[98:99], v[92:93] op_sel_hi:[0,1,1] neg_lo:[1,0,0] neg_hi:[1,0,0]
	v_cvt_pk_bf16_f32 v92, v92, v93
	v_cndmask_b32_e64 v99, 0, 1.0, vcc
	v_cmp_eq_u32_e32 vcc, v193, v198
	s_nop 1
	v_cndmask_b32_e64 v98, 0, 1.0, vcc
	v_pk_fma_f32 v[90:91], v[240:241], v[100:101], v[98:99] op_sel_hi:[0,1,1] neg_lo:[1,0,0] neg_hi:[1,0,0]
	v_cvt_pk_bf16_f32 v93, v90, v91
	ds_write_b64 v186, v[92:93] offset:2176
	v_cmp_eq_u32_e32 vcc, v189, v199
	s_nop 1
	v_cndmask_b32_e64 v92, 0, 1.0, vcc
	v_cmp_eq_u32_e32 vcc, v190, v199
	s_nop 1
	v_cndmask_b32_e64 v93, 0, 1.0, vcc
	v_cmp_eq_u32_e32 vcc, v192, v199
	v_pk_fma_f32 v[92:93], v[242:243], v[94:95], v[92:93] op_sel_hi:[0,1,1] neg_lo:[1,0,0] neg_hi:[1,0,0]
	v_cvt_pk_bf16_f32 v92, v92, v93
	v_cndmask_b32_e64 v95, 0, 1.0, vcc
	v_cmp_eq_u32_e32 vcc, v193, v199
	s_nop 1
	v_cndmask_b32_e64 v94, 0, 1.0, vcc
	v_pk_fma_f32 v[90:91], v[242:243], v[96:97], v[94:95] op_sel_hi:[0,1,1] neg_lo:[1,0,0] neg_hi:[1,0,0]
	v_cvt_pk_bf16_f32 v93, v90, v91
	ds_write_b64 v186, v[92:93] offset:2720
	v_cmp_eq_u32_e32 vcc, v189, v200
	s_nop 1
	v_cndmask_b32_e64 v92, 0, 1.0, vcc
	v_cmp_eq_u32_e32 vcc, v190, v200
	s_nop 1
	v_cndmask_b32_e64 v93, 0, 1.0, vcc
	v_cmp_eq_u32_e32 vcc, v192, v200
	v_pk_fma_f32 v[86:87], v[244:245], v[86:87], v[92:93] op_sel_hi:[0,1,1] neg_lo:[1,0,0] neg_hi:[1,0,0]
	v_cvt_pk_bf16_f32 v86, v86, v87
	v_cndmask_b32_e64 v93, 0, 1.0, vcc
	v_cmp_eq_u32_e32 vcc, v193, v200
	s_nop 1
	v_cndmask_b32_e64 v92, 0, 1.0, vcc
	v_pk_fma_f32 v[88:89], v[244:245], v[88:89], v[92:93] op_sel_hi:[0,1,1] neg_lo:[1,0,0] neg_hi:[1,0,0]
	v_cvt_pk_bf16_f32 v87, v88, v89
	ds_write_b64 v186, v[86:87] offset:3264
	v_cmp_eq_u32_e32 vcc, v189, v201
	s_nop 1
	v_cndmask_b32_e64 v88, 0, 1.0, vcc
	v_cmp_eq_u32_e32 vcc, v190, v201
	s_nop 1
	v_cndmask_b32_e64 v89, 0, 1.0, vcc
	v_cmp_eq_u32_e32 vcc, v192, v201
	v_pk_fma_f32 v[82:83], v[246:247], v[82:83], v[88:89] op_sel_hi:[0,1,1] neg_lo:[1,0,0] neg_hi:[1,0,0]
	v_cvt_pk_bf16_f32 v82, v82, v83
	v_cndmask_b32_e64 v89, 0, 1.0, vcc
	v_cmp_eq_u32_e32 vcc, v193, v201
	s_nop 1
	v_cndmask_b32_e64 v88, 0, 1.0, vcc
	v_pk_fma_f32 v[84:85], v[246:247], v[84:85], v[88:89] op_sel_hi:[0,1,1] neg_lo:[1,0,0] neg_hi:[1,0,0]
	v_cvt_pk_bf16_f32 v83, v84, v85
	ds_write_b64 v186, v[82:83] offset:3808
	ds_read_b128 v[82:85], v1
	ds_read_b128 v[86:89], v1 offset:64
	ds_read_b128 v[90:93], v1 offset:128
	ds_read_b128 v[94:97], v1 offset:192
	v_lshl_add_u64 v[98:99], v[150:151], 0, s[0:1]
	v_lshl_add_u64 v[192:193], v[164:165], 0, s[0:1]
	v_lshl_add_u64 v[196:197], v[166:167], 0, s[0:1]
	v_lshl_add_u64 v[100:101], v[152:153], 0, s[0:1]
	v_lshl_add_u64 v[106:107], v[156:157], 0, s[0:1]
	v_lshl_add_u64 v[108:109], v[158:159], 0, s[0:1]
	v_lshl_add_u64 v[110:111], v[160:161], 0, s[0:1]
	v_lshl_add_u64 v[112:113], v[162:163], 0, s[0:1]
	global_load_dwordx4 v[118:121], v[98:99], off nt
	global_load_dwordx4 v[134:137], v[100:101], off nt
	global_load_dwordx4 v[150:153], v[106:107], off nt
	global_load_dwordx4 v[156:159], v[108:109], off nt
	global_load_dwordx4 v[160:163], v[110:111], off nt
	global_load_dwordx4 v[164:167], v[112:113], off nt
	s_nop 0
	global_load_dwordx4 v[192:195], v[192:193], off nt
	s_nop 0
	global_load_dwordx4 v[196:199], v[196:197], off nt
	v_mov_b32_e32 v98, v188
	s_waitcnt vmcnt(15)
	s_waitcnt vmcnt(14)
	s_waitcnt vmcnt(13)
	s_waitcnt vmcnt(12)
	s_waitcnt vmcnt(11)
	s_waitcnt vmcnt(10)
	s_waitcnt vmcnt(9)
	s_waitcnt vmcnt(8)
	ds_read_b32 v232, v187 offset:0
	ds_read_b32 v234, v187 offset:8
	ds_read_b32 v236, v187 offset:16
	ds_read_b32 v238, v187 offset:24
	ds_read_b32 v240, v187 offset:32
	ds_read_b32 v242, v187 offset:40
	ds_read_b32 v244, v187 offset:48
	ds_read_b32 v246, v187 offset:56
	s_waitcnt lgkmcnt(0)
	v_pk_fma_f32 v[100:101], v[232:233], v[146:147], 0 op_sel_hi:[0,1,0] neg_lo:[1,0,0] neg_hi:[1,0,0]
	v_pk_fma_f32 v[98:99], v[232:233], v[148:149], 0 op_sel_hi:[0,1,0] neg_lo:[1,0,0] neg_hi:[1,0,0]
	v_cvt_pk_bf16_f32 v100, v100, v101
	v_cvt_pk_bf16_f32 v101, v98, v99
	ds_write_b64 v186, v[100:101]
	v_pk_fma_f32 v[100:101], v[234:235], v[142:143], 0 op_sel_hi:[0,1,0] neg_lo:[1,0,0] neg_hi:[1,0,0]
	v_pk_fma_f32 v[98:99], v[234:235], v[144:145], 0 op_sel_hi:[0,1,0] neg_lo:[1,0,0] neg_hi:[1,0,0]
	v_cvt_pk_bf16_f32 v100, v100, v101
	v_cvt_pk_bf16_f32 v101, v98, v99
	ds_write_b64 v186, v[100:101] offset:544
	v_pk_fma_f32 v[100:101], v[236:237], v[138:139], 0 op_sel_hi:[0,1,0] neg_lo:[1,0,0] neg_hi:[1,0,0]
	v_pk_fma_f32 v[98:99], v[236:237], v[140:141], 0 op_sel_hi:[0,1,0] neg_lo:[1,0,0] neg_hi:[1,0,0]
	v_cvt_pk_bf16_f32 v100, v100, v101
	v_cvt_pk_bf16_f32 v101, v98, v99
	ds_write_b64 v186, v[100:101] offset:1088
	v_pk_fma_f32 v[100:101], v[238:239], v[130:131], 0 op_sel_hi:[0,1,0] neg_lo:[1,0,0] neg_hi:[1,0,0]
	v_pk_fma_f32 v[98:99], v[238:239], v[132:133], 0 op_sel_hi:[0,1,0] neg_lo:[1,0,0] neg_hi:[1,0,0]
	v_cvt_pk_bf16_f32 v100, v100, v101
	v_cvt_pk_bf16_f32 v101, v98, v99
	ds_write_b64 v186, v[100:101] offset:1632
	v_pk_fma_f32 v[100:101], v[240:241], v[126:127], 0 op_sel_hi:[0,1,0] neg_lo:[1,0,0] neg_hi:[1,0,0]
	v_pk_fma_f32 v[98:99], v[240:241], v[128:129], 0 op_sel_hi:[0,1,0] neg_lo:[1,0,0] neg_hi:[1,0,0]
	v_cvt_pk_bf16_f32 v100, v100, v101
	v_cvt_pk_bf16_f32 v101, v98, v99
	ds_write_b64 v186, v[100:101] offset:2176
	v_pk_fma_f32 v[100:101], v[242:243], v[122:123], 0 op_sel_hi:[0,1,0] neg_lo:[1,0,0] neg_hi:[1,0,0]
	v_pk_fma_f32 v[98:99], v[242:243], v[124:125], 0 op_sel_hi:[0,1,0] neg_lo:[1,0,0] neg_hi:[1,0,0]
	v_cvt_pk_bf16_f32 v100, v100, v101
	v_cvt_pk_bf16_f32 v101, v98, v99
	ds_write_b64 v186, v[100:101] offset:2720
	v_pk_fma_f32 v[100:101], v[244:245], v[114:115], 0 op_sel_hi:[0,1,0] neg_lo:[1,0,0] neg_hi:[1,0,0]
	v_pk_fma_f32 v[98:99], v[244:245], v[116:117], 0 op_sel_hi:[0,1,0] neg_lo:[1,0,0] neg_hi:[1,0,0]
	v_cvt_pk_bf16_f32 v100, v100, v101
	v_cvt_pk_bf16_f32 v101, v98, v99
	ds_write_b64 v186, v[100:101] offset:3264
	v_pk_fma_f32 v[100:101], v[246:247], v[102:103], 0 op_sel_hi:[0,1,0] neg_lo:[1,0,0] neg_hi:[1,0,0]
	v_pk_fma_f32 v[98:99], v[246:247], v[104:105], 0 op_sel_hi:[0,1,0] neg_lo:[1,0,0] neg_hi:[1,0,0]
	v_cvt_pk_bf16_f32 v100, v100, v101
	v_cvt_pk_bf16_f32 v101, v98, v99
	ds_write_b64 v186, v[100:101] offset:3808
	ds_read_b128 v[98:101], v1
	ds_read_b128 v[102:105], v1 offset:64
	ds_read_b128 v[106:109], v1 offset:128
	ds_read_b128 v[110:113], v1 offset:192
	v_lshl_add_u64 v[114:115], v[168:169], 0, s[0:1]
	v_lshl_add_u64 v[126:127], v[176:177], 0, s[0:1]
	v_lshl_add_u64 v[176:177], v[180:181], 0, s[0:1]
	v_lshl_add_u64 v[180:181], v[182:183], 0, s[0:1]
	v_lshl_add_u64 v[116:117], v[170:171], 0, s[0:1]
	v_lshl_add_u64 v[122:123], v[172:173], 0, s[0:1]
	v_lshl_add_u64 v[124:125], v[174:175], 0, s[0:1]
	v_lshl_add_u64 v[128:129], v[178:179], 0, s[0:1]
	global_load_dwordx4 v[130:133], v[114:115], off nt
	global_load_dwordx4 v[138:141], v[116:117], off nt
	global_load_dwordx4 v[142:145], v[122:123], off nt
	global_load_dwordx4 v[146:149], v[124:125], off nt
	global_load_dwordx4 v[168:171], v[126:127], off nt
	global_load_dwordx4 v[172:175], v[128:129], off nt
	s_nop 0
	global_load_dwordx4 v[176:179], v[176:177], off nt
	s_nop 0
	global_load_dwordx4 v[180:183], v[180:181], off nt
	v_mov_b32_e32 v114, v188
	s_waitcnt vmcnt(15)
	s_waitcnt vmcnt(14)
	s_waitcnt vmcnt(13)
	s_waitcnt vmcnt(12)
	s_waitcnt vmcnt(11)
	s_waitcnt vmcnt(10)
	s_waitcnt vmcnt(9)
	s_waitcnt vmcnt(8)
	ds_read_b32 v232, v187 offset:64
	ds_read_b32 v234, v187 offset:72
	ds_read_b32 v236, v187 offset:80
	ds_read_b32 v238, v187 offset:88
	ds_read_b32 v240, v187 offset:96
	ds_read_b32 v242, v187 offset:104
	ds_read_b32 v244, v187 offset:112
	ds_read_b32 v246, v187 offset:120
	s_waitcnt lgkmcnt(0)
	v_pk_fma_f32 v[116:117], v[232:233], v[118:119], 0 op_sel_hi:[0,1,0] neg_lo:[1,0,0] neg_hi:[1,0,0]
	v_pk_fma_f32 v[114:115], v[232:233], v[120:121], 0 op_sel_hi:[0,1,0] neg_lo:[1,0,0] neg_hi:[1,0,0]
	v_cvt_pk_bf16_f32 v116, v116, v117
	v_cvt_pk_bf16_f32 v117, v114, v115
	ds_write_b64 v186, v[116:117]
	v_pk_fma_f32 v[116:117], v[234:235], v[134:135], 0 op_sel_hi:[0,1,0] neg_lo:[1,0,0] neg_hi:[1,0,0]
	v_pk_fma_f32 v[114:115], v[234:235], v[136:137], 0 op_sel_hi:[0,1,0] neg_lo:[1,0,0] neg_hi:[1,0,0]
	v_cvt_pk_bf16_f32 v116, v116, v117
	v_cvt_pk_bf16_f32 v117, v114, v115
	ds_write_b64 v186, v[116:117] offset:544
	v_pk_fma_f32 v[116:117], v[236:237], v[150:151], 0 op_sel_hi:[0,1,0] neg_lo:[1,0,0] neg_hi:[1,0,0]
	v_pk_fma_f32 v[114:115], v[236:237], v[152:153], 0 op_sel_hi:[0,1,0] neg_lo:[1,0,0] neg_hi:[1,0,0]
	v_cvt_pk_bf16_f32 v116, v116, v117
	v_cvt_pk_bf16_f32 v117, v114, v115
	ds_write_b64 v186, v[116:117] offset:1088
	v_pk_fma_f32 v[116:117], v[238:239], v[156:157], 0 op_sel_hi:[0,1,0] neg_lo:[1,0,0] neg_hi:[1,0,0]
	v_pk_fma_f32 v[114:115], v[238:239], v[158:159], 0 op_sel_hi:[0,1,0] neg_lo:[1,0,0] neg_hi:[1,0,0]
	v_cvt_pk_bf16_f32 v116, v116, v117
	v_cvt_pk_bf16_f32 v117, v114, v115
	ds_write_b64 v186, v[116:117] offset:1632
	v_pk_fma_f32 v[116:117], v[240:241], v[160:161], 0 op_sel_hi:[0,1,0] neg_lo:[1,0,0] neg_hi:[1,0,0]
	v_pk_fma_f32 v[114:115], v[240:241], v[162:163], 0 op_sel_hi:[0,1,0] neg_lo:[1,0,0] neg_hi:[1,0,0]
	v_cvt_pk_bf16_f32 v116, v116, v117
	v_cvt_pk_bf16_f32 v117, v114, v115
	ds_write_b64 v186, v[116:117] offset:2176
	v_pk_fma_f32 v[116:117], v[242:243], v[164:165], 0 op_sel_hi:[0,1,0] neg_lo:[1,0,0] neg_hi:[1,0,0]
	v_pk_fma_f32 v[114:115], v[242:243], v[166:167], 0 op_sel_hi:[0,1,0] neg_lo:[1,0,0] neg_hi:[1,0,0]
	v_cvt_pk_bf16_f32 v116, v116, v117
	v_cvt_pk_bf16_f32 v117, v114, v115
	ds_write_b64 v186, v[116:117] offset:2720
	v_pk_fma_f32 v[116:117], v[244:245], v[192:193], 0 op_sel_hi:[0,1,0] neg_lo:[1,0,0] neg_hi:[1,0,0]
	v_pk_fma_f32 v[114:115], v[244:245], v[194:195], 0 op_sel_hi:[0,1,0] neg_lo:[1,0,0] neg_hi:[1,0,0]
	v_cvt_pk_bf16_f32 v116, v116, v117
	v_cvt_pk_bf16_f32 v117, v114, v115
	ds_write_b64 v186, v[116:117] offset:3264
	v_pk_fma_f32 v[116:117], v[246:247], v[196:197], 0 op_sel_hi:[0,1,0] neg_lo:[1,0,0] neg_hi:[1,0,0]
	v_pk_fma_f32 v[114:115], v[246:247], v[198:199], 0 op_sel_hi:[0,1,0] neg_lo:[1,0,0] neg_hi:[1,0,0]
	v_cvt_pk_bf16_f32 v116, v116, v117
	v_cvt_pk_bf16_f32 v117, v114, v115
	ds_write_b64 v186, v[116:117] offset:3808
	ds_read_b128 v[114:117], v1
	ds_read_b128 v[118:121], v1 offset:64
	ds_read_b128 v[122:125], v1 offset:128
	ds_read_b128 v[126:129], v1 offset:192
	s_waitcnt vmcnt(7)
	s_waitcnt vmcnt(6)
	s_waitcnt vmcnt(5)
	s_waitcnt vmcnt(4)
	s_waitcnt vmcnt(3)
	s_waitcnt vmcnt(2)
	s_waitcnt vmcnt(1)
	s_waitcnt vmcnt(0)
	ds_read_b32 v232, v187 offset:128
	ds_read_b32 v234, v187 offset:136
	ds_read_b32 v236, v187 offset:144
	ds_read_b32 v238, v187 offset:152
	ds_read_b32 v240, v187 offset:160
	ds_read_b32 v242, v187 offset:168
	ds_read_b32 v244, v187 offset:176
	ds_read_b32 v246, v187 offset:184
	s_waitcnt lgkmcnt(0)
	v_pk_fma_f32 v[130:131], v[232:233], v[130:131], 0 op_sel_hi:[0,1,0] neg_lo:[1,0,0] neg_hi:[1,0,0]
	v_pk_fma_f32 v[132:133], v[232:233], v[132:133], 0 op_sel_hi:[0,1,0] neg_lo:[1,0,0] neg_hi:[1,0,0]
	v_cvt_pk_bf16_f32 v130, v130, v131
	v_cvt_pk_bf16_f32 v131, v132, v133
	ds_write_b64 v186, v[130:131]
	v_pk_fma_f32 v[132:133], v[234:235], v[138:139], 0 op_sel_hi:[0,1,0] neg_lo:[1,0,0] neg_hi:[1,0,0]
	v_pk_fma_f32 v[130:131], v[234:235], v[140:141], 0 op_sel_hi:[0,1,0] neg_lo:[1,0,0] neg_hi:[1,0,0]
	v_cvt_pk_bf16_f32 v132, v132, v133
	v_cvt_pk_bf16_f32 v133, v130, v131
	ds_write_b64 v186, v[132:133] offset:544
	v_pk_fma_f32 v[132:133], v[236:237], v[142:143], 0 op_sel_hi:[0,1,0] neg_lo:[1,0,0] neg_hi:[1,0,0]
	v_pk_fma_f32 v[130:131], v[236:237], v[144:145], 0 op_sel_hi:[0,1,0] neg_lo:[1,0,0] neg_hi:[1,0,0]
	v_cvt_pk_bf16_f32 v132, v132, v133
	v_cvt_pk_bf16_f32 v133, v130, v131
	ds_write_b64 v186, v[132:133] offset:1088
	v_pk_fma_f32 v[132:133], v[238:239], v[146:147], 0 op_sel_hi:[0,1,0] neg_lo:[1,0,0] neg_hi:[1,0,0]
	v_pk_fma_f32 v[130:131], v[238:239], v[148:149], 0 op_sel_hi:[0,1,0] neg_lo:[1,0,0] neg_hi:[1,0,0]
	v_cvt_pk_bf16_f32 v132, v132, v133
	v_cvt_pk_bf16_f32 v133, v130, v131
	ds_write_b64 v186, v[132:133] offset:1632
	v_pk_fma_f32 v[132:133], v[240:241], v[168:169], 0 op_sel_hi:[0,1,0] neg_lo:[1,0,0] neg_hi:[1,0,0]
	v_pk_fma_f32 v[130:131], v[240:241], v[170:171], 0 op_sel_hi:[0,1,0] neg_lo:[1,0,0] neg_hi:[1,0,0]
	v_cvt_pk_bf16_f32 v132, v132, v133
	v_cvt_pk_bf16_f32 v133, v130, v131
	ds_write_b64 v186, v[132:133] offset:2176
	v_pk_fma_f32 v[132:133], v[242:243], v[172:173], 0 op_sel_hi:[0,1,0] neg_lo:[1,0,0] neg_hi:[1,0,0]
	v_pk_fma_f32 v[130:131], v[242:243], v[174:175], 0 op_sel_hi:[0,1,0] neg_lo:[1,0,0] neg_hi:[1,0,0]
	v_cvt_pk_bf16_f32 v132, v132, v133
	v_cvt_pk_bf16_f32 v133, v130, v131
	ds_write_b64 v186, v[132:133] offset:2720
	v_pk_fma_f32 v[132:133], v[244:245], v[176:177], 0 op_sel_hi:[0,1,0] neg_lo:[1,0,0] neg_hi:[1,0,0]
	v_pk_fma_f32 v[130:131], v[244:245], v[178:179], 0 op_sel_hi:[0,1,0] neg_lo:[1,0,0] neg_hi:[1,0,0]
	v_cvt_pk_bf16_f32 v132, v132, v133
	v_cvt_pk_bf16_f32 v133, v130, v131
	ds_write_b64 v186, v[132:133] offset:3264
	v_pk_fma_f32 v[132:133], v[246:247], v[180:181], 0 op_sel_hi:[0,1,0] neg_lo:[1,0,0] neg_hi:[1,0,0]
	v_pk_fma_f32 v[130:131], v[246:247], v[182:183], 0 op_sel_hi:[0,1,0] neg_lo:[1,0,0] neg_hi:[1,0,0]
	v_cvt_pk_bf16_f32 v132, v132, v133
	v_cvt_pk_bf16_f32 v133, v130, v131
	ds_write_b64 v186, v[132:133] offset:3808
	ds_read_b128 v[130:133], v1
	ds_read_b128 v[134:137], v1 offset:64
	ds_read_b128 v[138:141], v1 offset:128
	ds_read_b128 v[142:145], v1 offset:192
	s_ashr_i32 s7, s6, 31
	s_lshl_b64 s[0:1], s[6:7], 2
	s_add_u32 s0, s4, s0
	s_addc_u32 s1, s5, s1
	v_lshlrev_b32_e32 v1, 4, v0
	s_add_i32 s20, s34, 1
	s_add_i32 s34, s34, -1
	v_or_b32_e32 v153, s10, v206
	s_xor_b32 s26, s3, 2
	s_lshl_b64 s[10:11], s[10:11], 3
	s_and_b32 s20, s20, 3
	s_and_b32 s27, s34, 3
	s_add_u32 s10, s14, s10
	s_addc_u32 s11, s15, s11
	s_lshl_b32 s42, s35, 2
	s_add_i32 s41, s42, 0x26a20
	s_add_i32 s42, s42, 0x26a00
	v_lshlrev_b32_e32 v190, 3, v206
	s_cmp_eq_u32 s35, 3
	v_lshlrev_b32_e32 v150, 3, v0
	v_and_b32_e32 v151, 1, v0
	v_lshl_add_u64 v[0:1], v[154:155], 3, s[14:15]
	v_lshl_add_u64 v[192:193], s[10:11], 0, v[190:191]
	s_cselect_b64 s[10:11], -1, 0
	s_lshl_b32 s14, s3, 2
	s_add_u32 s24, s16, s14
	v_or_b32_e32 v155, 0x20000, v150
	v_add_u32_e32 v156, 0x20880, v150
	v_lshlrev_b32_e32 v150, 1, v153
	s_addc_u32 s25, s17, 0
	s_lshl_b32 s43, s3, 9
	v_lshl_add_u32 v212, s26, 9, v150
	s_lshl_b32 s15, s26, 8
	s_add_i32 s26, s43, 0x200
	v_mov_b32_e32 v152, 0x880
	v_cmp_lt_u32_e64 s[0:1], 15, v206
	v_cmp_eq_u32_e32 vcc, 1, v151
	s_and_b32 s45, s26, 0x600
	s_add_i32 s26, s43, 0x500
	v_cndmask_b32_e32 v211, 0, v152, vcc
	s_and_b32 s56, s26, 0x700
	s_add_i32 s26, s43, 0x540
	v_lshl_add_u32 v213, s20, 9, v150
	v_lshl_add_u32 v214, s27, 9, v150
	s_and_b32 s57, s26, 0x740
	s_add_i32 s26, s43, 0x580
	s_and_b32 s58, s26, 0x780
	s_add_i32 s26, s43, 0x5c0
	s_and_b32 s59, s26, 0x7c0
	s_add_i32 s26, s43, 0x600
	s_and_b32 s60, s26, 0x600
	s_add_i32 s26, s43, 0x640
	s_and_b32 s61, s26, 0x640
	s_add_i32 s26, s43, 0x680
	s_and_b32 s62, s26, 0x680
	s_add_i32 s26, s43, 0x6c0
	s_and_b32 s63, s26, 0x6c0
	s_add_i32 s26, s43, 0x700
	s_and_b32 s64, s26, 0x700
	s_add_i32 s26, s43, 0x740
	s_and_b32 s65, s26, 0x740
	s_add_i32 s26, s43, 0x780
	s_lshl_b32 s14, s27, 8
	s_lshl_b32 s20, s20, 8
	s_add_i32 s27, s43, 0x240
	s_add_i32 s28, s43, 0x280
	s_add_i32 s29, s43, 0x2c0
	s_add_i32 s30, s43, 0x300
	s_add_i32 s31, s43, 0x340
	s_add_i32 s34, s43, 0x380
	s_add_i32 s35, s43, 0x3c0
	s_add_i32 s36, s43, 0x440
	s_add_i32 s37, s43, 0x480
	s_add_i32 s38, s43, 0x4c0
	s_and_b32 s66, s26, 0x780
	s_add_i32 s26, s43, 0x7c0
	s_mul_hi_i32 s23, s18, 0x65
	s_mul_i32 s22, s18, 0x65
	v_cmp_eq_u32_e64 s[4:5], 1, v185
	v_cmp_eq_u32_e64 s[6:7], 2, v185
	v_cmp_eq_u32_e64 s[8:9], 63, v206
	s_xor_b32 s44, s43, 0x400
	s_and_b32 s46, s27, 0x640
	s_and_b32 s47, s28, 0x680
	s_waitcnt lgkmcnt(0)
	v_mov_b32_e32 v146, 0x20000
	s_and_b32 s48, s29, 0x6c0
	s_and_b32 s49, s30, 0x700
	s_and_b32 s50, s31, 0x740
	s_and_b32 s51, s34, 0x780
	s_and_b32 s52, s35, 0x7c0
	s_and_b32 s53, s36, 0x640
	s_and_b32 s54, s37, 0x680
	s_and_b32 s55, s38, 0x6c0
	s_and_b32 s67, s26, 0x7c0
	s_and_b64 s[26:27], s[10:11], s[12:13]
	v_lshl_add_u32 v215, v154, 1, v146
	v_mov_b32_e32 v216, 1
	s_lshl_b32 s28, s14, 3
	s_lshl_b32 s30, s15, 3
	s_lshl_b32 s34, s20, 3
	s_movk_i32 s68, 0x7fff
	s_mov_b32 s69, 0
	v_and_b32_e32 v220, 24, v206
	v_lshlrev_b32_e32 v220, 2, v220
	v_and_b32_e32 v221, 2, v206
	v_lshl_or_b32 v220, v221, 3, v220
	v_and_b32_e32 v221, 32, v206
	v_lshrrev_b32_e32 v221, 2, v221
	v_or_b32_e32 v220, v220, v221
	v_and_b32_e32 v221, 4, v206
	v_or_b32_e32 v220, v220, v221
	v_and_b32_e32 v221, 1, v206
	v_lshl_or_b32 v220, v221, 1, v220
	v_mov_b32_e32 v220, v254
	s_lshr_b32 s76, s19, 8
	s_add_i32 s76, s76, 0x20000
	v_add_u32_e32 v220, s76, v220
	v_add_u32_e32 v225, s45, v220
	v_add_u32_e32 v226, s44, v220
	v_add_u32_e32 v227, s60, v220
	v_add_u32_e32 v228, s43, v220
	v_and_b32_e32 v221, 1, v206
	v_mul_u32_u24_e32 v221, 0x880, v221
	v_lshrrev_b32_e32 v220, 4, v206
	v_lshl_add_u32 v221, v220, 5, v221
	v_and_b32_e32 v220, 2, v206
	v_lshl_add_u32 v221, v220, 3, v221
	v_add_u32_e32 v222, 0x20000, v221
	v_cmp_ne_u32_e32 vcc, 0, v220
	v_mov_b32_e32 v220, 0x44444444
	v_mov_b32_e32 v221, 0xeeeeeeee
	s_nop 1
	v_cndmask_b32_e32 v223, v220, v221, vcc
	v_cmp_lt_u32_e64 s[74:75], 47, v206
	s_lshr_b32 s82, s19, 15
	s_mul_i32 s83, s82, 0x1100
	s_add_i32 s83, s83, 0x22200
	v_lshl_add_u32 v254, v206, 2, s83
	v_mov_b32_e32 v220, s41
	s_nop 1
	v_cndmask_b32_e64 v254, v254, v220, s[12:13]
	v_mov_b32_e32 v224, v184
	s_mov_b32 s86, 0x55555555
	s_mov_b32 s87, 0x55555555
	s_lshr_b32 s78, s19, 15
	s_lshl_b32 s79, s78, 11
	v_add_u32_e32 v255, s79, v224
	ds_read_b128 v[166:169], v224 offset:0
	ds_read_b128 v[170:173], v224 offset:1024
	ds_read_b128 v[174:177], v224 offset:2048
	ds_read_b128 v[178:181], v224 offset:3072
	ds_read_b128 v[182:185], v224 offset:4096
	ds_read_b128 v[186:189], v224 offset:5120
	s_mov_b32 s20, 0
